# plus non-temporal stores for the post-projection (P3) outputs and the attention/mLSTM mixer outputs (P5)
# speedup vs baseline: 1.0190x; 1.0040x over previous
.LBB0_440:
	s_or_b64 exec, exec, s[2:3]
	v_and_b32_e32 v68, 63, v70
	v_ashrrev_i32_e32 v40, 8, v70
	v_bfe_u32 v41, v70, 6, 2
	s_waitcnt vmcnt(0)
	v_lshl_add_u32 v0, v68, 6, 0
	v_lshlrev_b32_e32 v1, 5, v40
	v_lshlrev_b32_e32 v2, 2, v41
	v_add3_u32 v0, v0, v1, v2
	s_waitcnt lgkmcnt(0)
	s_barrier
	ds_read2_b32 v[2:3], v0 offset1:4
	s_mov_b32 s2, 0xbfb8aa3b
	v_and_b32_e32 v71, 64, v84
	v_cmp_gt_u32_e64 s[6:7], s37, v70
	s_ashr_i32 s36, s30, 6
	s_waitcnt lgkmcnt(0)
	v_mul_f32_e64 v0, |v3|, s2
	v_exp_f32_e32 v4, v0
	v_max_f32_e32 v0, v3, v3
	v_min_f32_e32 v3, 0, v0
	s_mov_b32 s2, 0x3f2aaaab
	v_add_f32_e32 v5, 1.0, v4
	v_add_f32_e32 v0, -1.0, v5
	v_sub_f32_e32 v1, v0, v5
	v_add_f32_e32 v1, 1.0, v1
	v_sub_f32_e32 v0, v4, v0
	v_add_f32_e32 v6, v0, v1
	v_frexp_mant_f32_e32 v7, v5
	v_cvt_f64_f32_e32 v[0:1], v5
	v_frexp_exp_i32_f64_e32 v0, v[0:1]
	v_cmp_gt_f32_e32 vcc, s2, v7
	s_mov_b32 s2, 0x3f317218
	s_and_b32 s16, s30, 63
	v_subbrev_co_u32_e32 v0, vcc, 0, v0, vcc
	v_sub_u32_e32 v1, 0, v0
	v_ldexp_f32 v5, v5, v1
	v_ldexp_f32 v1, v6, v1
	v_add_f32_e32 v6, -1.0, v5
	v_add_f32_e32 v9, 1.0, v5
	v_add_f32_e32 v7, 1.0, v6
	v_add_f32_e32 v10, -1.0, v9
	v_sub_f32_e32 v7, v5, v7
	v_sub_f32_e32 v5, v5, v10
	v_add_f32_e32 v7, v1, v7
	v_add_f32_e32 v1, v1, v5
	v_add_f32_e32 v5, v9, v1
	v_rcp_f32_e32 v10, v5
	v_add_f32_e32 v8, v6, v7
	v_sub_f32_e32 v6, v8, v6
	v_sub_f32_e32 v6, v7, v6
	v_sub_f32_e32 v7, v5, v9
	v_sub_f32_e32 v1, v1, v7
	v_mul_f32_e32 v7, v8, v10
	v_mul_f32_e32 v9, v5, v7
	v_fma_f32 v11, v7, v5, -v9
	v_fmac_f32_e32 v11, v7, v1
	v_add_f32_e32 v12, v9, v11
	v_sub_f32_e32 v13, v8, v12
	v_sub_f32_e32 v8, v8, v13
	v_sub_f32_e32 v9, v12, v9
	v_sub_f32_e32 v8, v8, v12
	v_add_f32_e32 v6, v6, v8
	v_sub_f32_e32 v8, v9, v11
	v_add_f32_e32 v6, v8, v6
	v_add_f32_e32 v8, v13, v6
	v_mul_f32_e32 v9, v10, v8
	v_mul_f32_e32 v11, v5, v9
	v_fma_f32 v5, v9, v5, -v11
	v_fmac_f32_e32 v5, v9, v1
	v_sub_f32_e32 v1, v13, v8
	v_add_f32_e32 v1, v6, v1
	v_add_f32_e32 v6, v11, v5
	v_sub_f32_e32 v12, v8, v6
	v_sub_f32_e32 v8, v8, v12
	v_sub_f32_e32 v11, v6, v11
	v_sub_f32_e32 v6, v8, v6
	v_add_f32_e32 v1, v1, v6
	v_sub_f32_e32 v5, v11, v5
	v_cvt_f32_i32_e32 v0, v0
	v_add_f32_e32 v1, v5, v1
	v_add_f32_e32 v5, v7, v9
	v_add_f32_e32 v1, v12, v1
	v_sub_f32_e32 v6, v5, v7
	v_mul_f32_e32 v1, v10, v1
	v_sub_f32_e32 v6, v9, v6
	v_add_f32_e32 v1, v6, v1
	v_mul_f32_e32 v9, 0x3f317218, v0
	v_add_f32_e32 v6, v5, v1
	v_fma_f32 v10, v0, s2, -v9
	v_mul_f32_e32 v7, v6, v6
	v_fmac_f32_e32 v10, 0xb102e308, v0
	v_sub_f32_e32 v0, v6, v5
	v_fmamk_f32 v8, v7, 0x3e9b6dac, v69
	v_sub_f32_e32 v0, v1, v0
	v_add_f32_e32 v1, v9, v10
	v_fmaak_f32 v8, v7, v8, 0x3f2aaada
	v_sub_f32_e32 v5, v1, v9
	v_ldexp_f32 v9, v6, 1
	v_mul_f32_e32 v6, v6, v7
	v_mul_f32_e32 v6, v6, v8
	v_add_f32_e32 v7, v9, v6
	v_sub_f32_e32 v8, v7, v9
	v_ldexp_f32 v0, v0, 1
	v_sub_f32_e32 v6, v6, v8
	v_add_f32_e32 v0, v0, v6
	v_add_f32_e32 v6, v7, v0
	v_sub_f32_e32 v7, v6, v7
	v_sub_f32_e32 v0, v0, v7
	v_add_f32_e32 v7, v1, v6
	v_sub_f32_e32 v8, v7, v1
	v_sub_f32_e32 v9, v7, v8
	v_sub_f32_e32 v5, v10, v5
	v_sub_f32_e32 v1, v1, v9
	v_sub_f32_e32 v6, v6, v8
	v_add_f32_e32 v1, v6, v1
	v_add_f32_e32 v6, v5, v0
	v_sub_f32_e32 v8, v6, v5
	v_sub_f32_e32 v9, v6, v8
	v_sub_f32_e32 v5, v5, v9
	v_sub_f32_e32 v0, v0, v8
	v_add_f32_e32 v1, v6, v1
	v_add_f32_e32 v0, v0, v5
	v_add_f32_e32 v5, v7, v1
	v_sub_f32_e32 v6, v5, v7
	v_sub_f32_e32 v1, v1, v6
	v_add_f32_e32 v0, v0, v1
	s_mov_b32 s2, 0x7f800000
	v_add_f32_e32 v0, v5, v0
	v_cmp_neq_f32_e32 vcc, s2, v4
	s_mov_b32 s2, 0x33800000
	s_nop 0
	v_cndmask_b32_e32 v0, v87, v0, vcc
	v_cmp_ngt_f32_e32 vcc, -1.0, v4
	s_nop 1
	v_cndmask_b32_e32 v0, v88, v0, vcc
	v_cmp_neq_f32_e32 vcc, -1.0, v4
	s_nop 1
	v_cndmask_b32_e32 v0, v89, v0, vcc
	v_cmp_lt_f32_e64 vcc, |v4|, s2
	s_nop 1
	v_cndmask_b32_e32 v0, v0, v4, vcc
	v_sub_f32_e32 v1, v3, v0
	v_add_u32_e32 v0, -1, v84
	v_cmp_lt_i32_e32 vcc, v0, v71
	v_add_u32_e32 v3, -2, v84
	v_cmp_lt_i32_e64 s[2:3], v3, v71
	v_cndmask_b32_e32 v0, v0, v84, vcc
	v_lshlrev_b32_e32 v0, 2, v0
	ds_bpermute_b32 v0, v0, v1
	v_cmp_eq_u32_e32 vcc, 0, v68
	v_cndmask_b32_e64 v3, v3, v84, s[2:3]
	v_lshlrev_b32_e32 v3, 2, v3
	v_cmp_gt_u32_e64 s[2:3], 2, v68
	s_waitcnt lgkmcnt(0)
	v_add_f32_e32 v0, v1, v0
	v_cndmask_b32_e32 v0, v0, v1, vcc
	ds_bpermute_b32 v3, v3, v0
	s_waitcnt lgkmcnt(0)
	v_add_f32_e32 v3, v0, v3
	v_cndmask_b32_e64 v0, v3, v0, s[2:3]
	v_add_u32_e32 v3, -4, v84
	v_cmp_lt_i32_e64 s[2:3], v3, v71
	s_nop 1
	v_cndmask_b32_e64 v3, v3, v84, s[2:3]
	v_lshlrev_b32_e32 v3, 2, v3
	ds_bpermute_b32 v3, v3, v0
	v_cmp_gt_u32_e64 s[2:3], 4, v68
	s_waitcnt lgkmcnt(0)
	v_add_f32_e32 v3, v0, v3
	v_cndmask_b32_e64 v0, v3, v0, s[2:3]
	v_add_u32_e32 v3, -8, v84
	v_cmp_lt_i32_e64 s[2:3], v3, v71
	s_nop 1
	v_cndmask_b32_e64 v3, v3, v84, s[2:3]
	v_lshlrev_b32_e32 v3, 2, v3
	ds_bpermute_b32 v3, v3, v0
	v_cmp_gt_u32_e64 s[2:3], 8, v68
	s_waitcnt lgkmcnt(0)
	v_add_f32_e32 v3, v0, v3
	v_cndmask_b32_e64 v0, v3, v0, s[2:3]
	v_add_u32_e32 v3, -16, v84
	v_cmp_lt_i32_e64 s[2:3], v3, v71
	s_nop 1
	v_cndmask_b32_e64 v3, v3, v84, s[2:3]
	v_lshlrev_b32_e32 v3, 2, v3
	ds_bpermute_b32 v3, v3, v0
	v_cmp_gt_u32_e64 s[2:3], 16, v68
	s_waitcnt lgkmcnt(0)
	v_add_f32_e32 v3, v0, v3
	v_cndmask_b32_e64 v0, v3, v0, s[2:3]
	v_subrev_u32_e32 v3, 32, v84
	v_cmp_lt_i32_e64 s[4:5], v3, v71
	s_nop 1
	v_cndmask_b32_e64 v3, v3, v84, s[4:5]
	v_lshlrev_b32_e32 v3, 2, v3
	ds_bpermute_b32 v3, v3, v0
	v_cmp_gt_u32_e64 s[4:5], 32, v68
	s_waitcnt lgkmcnt(0)
	v_add_f32_e32 v3, v0, v3
	v_cndmask_b32_e64 v3, v3, v0, s[4:5]
	ds_bpermute_b32 v0, v85, v3
	s_waitcnt lgkmcnt(0)
	v_sub_f32_e32 v4, v0, v3
	v_add_f32_e32 v1, v1, v4
	v_cndmask_b32_e64 v1, v1, v3, s[6:7]
	v_sub_f32_e32 v1, v0, v1
	v_add_f32_e32 v1, v2, v1
	v_mov_b32_e32 v2, 0xff7fffff
	v_mov_b32_e32 v3, 0xff7fffff
	s_nop 0
	v_mov_b32_dpp v2, v1 quad_perm:[1,0,3,2] row_mask:0xf bank_mask:0xf
	v_max_f32_e32 v2, v2, v2
	v_max_f32_e32 v2, v1, v2
	s_nop 1
	v_mov_b32_dpp v3, v2 quad_perm:[2,3,0,1] row_mask:0xf bank_mask:0xf
	v_max_f32_e32 v3, v3, v3
	v_max_f32_e32 v2, v2, v3
	v_mov_b32_e32 v3, 0xff7fffff
	s_nop 1
	v_mov_b32_dpp v3, v2 row_half_mirror row_mask:0xf bank_mask:0xf
	v_max_f32_e32 v3, v3, v3
	v_max_f32_e32 v2, v2, v3
	v_mov_b32_e32 v3, 0xff7fffff
	s_nop 1
	v_mov_b32_dpp v3, v2 row_mirror row_mask:0xf bank_mask:0xf
	v_max_f32_e32 v3, v3, v3
	v_max_f32_e32 v2, v2, v3
	v_mov_b32_e32 v3, 0xff7fffff
	s_nop 1
	v_mov_b32_dpp v3, v2 row_bcast:15 row_mask:0xa bank_mask:0xf
	v_max_f32_e32 v3, v3, v3
	v_max_f32_e32 v2, v2, v3
	v_mov_b32_e32 v3, 0xff7fffff
	s_nop 1
	v_mov_b32_dpp v3, v2 row_bcast:31 row_mask:0xc bank_mask:0xf
	v_max_f32_e32 v3, v3, v3
	v_max_f32_e32 v2, v2, v3
	s_nop 0
	v_readlane_b32 s10, v2, 63
	v_lshl_add_u32 v2, v70, 2, 0
	s_nop 0
	v_subrev_f32_e32 v1, s10, v1
	v_mul_f32_e32 v1, 0x3fb8aa3b, v1
	v_exp_f32_e32 v1, v1
	ds_write_b32 v2, v1 offset:4096
	s_and_saveexec_b64 s[8:9], vcc
	s_cbranch_execz .LBB0_442
	s_lshl_b32 s11, s36, 10
	v_lshl_add_u32 v1, v40, 7, s11
	s_lshl_b32 s11, s16, 1
	s_xor_b32 s28, s11, 0x7e
	v_mov_b32_e32 v2, s28
	v_mov_b32_e32 v3, s11
	v_cndmask_b32_e64 v2, v2, v3, s[6:7]
	v_or_b32_e32 v1, v1, v2
	v_lshl_add_u32 v2, v41, 8, v1
	v_readlane_b32 s28, v255, 11
	v_ashrrev_i32_e32 v3, 31, v2
	v_readlane_b32 s29, v255, 12
	v_mov_b32_e32 v1, s10
	s_nop 0
	v_lshl_add_u64 v[2:3], v[2:3], 2, s[28:29]
	global_store_dwordx2 v[2:3], v[0:1], off nt

.LBB0_453:
	v_pk_fma_f32 v[24:25], v[2:3], v[28:29], v[12:13]
	s_waitcnt vmcnt(13)
	v_lshlrev_b32_e32 v36, 16, v26
	v_pk_fma_f32 v[24:25], v[4:5], v[30:31], v[24:25]
	v_and_b32_e32 v37, 0xffff0000, v26
	v_pk_fma_f32 v[24:25], v[6:7], v[32:33], v[24:25]
	s_nop 0
	v_pk_fma_f32 v[24:25], v[8:9], v[34:35], v[24:25]
	s_nop 0
	v_pk_fma_f32 v[24:25], v[10:11], v[36:37], v[24:25]
	s_nop 0
	v_mul_f32_e32 v26, 0xbfb8aa3b, v24
	v_mul_f32_e32 v27, 0xbfb8aa3b, v25
	v_exp_f32_e32 v26, v26
	v_exp_f32_e32 v27, v27
	v_add_f32_e32 v26, 1.0, v26
	v_add_f32_e32 v27, 1.0, v27
	v_rcp_f32_e32 v26, v26
	v_rcp_f32_e32 v27, v27
	s_nop 0
	v_pk_mul_f32 v[26:27], v[24:25], v[26:27]
	v_lshl_add_u64 v[24:25], s[94:95], 0, v[16:17]
	s_and_saveexec_b64 s[28:29], s[8:9]
	s_xor_b64 s[28:29], exec, s[28:29]
	s_cbranch_execz .LBB0_455
	v_cvt_pk_bf16_f32 v28, v26, v27
	v_add_co_u32_e32 v26, vcc, 0x51360000, v24
	s_nop 1
	v_addc_co_u32_e32 v27, vcc, 0, v25, vcc
	global_store_dword v[26:27], v28, off offset:512 nt
.LBB0_455:
	s_andn2_saveexec_b64 s[28:29], s[28:29]
	s_cbranch_execz .LBB0_457
	ds_read2st64_b32 v[28:29], v43 offset1:4
	v_pk_mul_f32 v[26:27], v[26:27], s[80:81] op_sel_hi:[1,0]
	s_nop 0
	v_cvt_pk_bf16_f32 v58, v26, v27
	v_lshl_add_u64 v[26:27], s[94:95], 0, v[22:23]
	global_store_dword v[26:27], v58, off nt
	v_lshlrev_b32_e32 v26, 16, v58
	v_and_b32_e32 v27, 0xffff0000, v58
	s_waitcnt lgkmcnt(0)
	v_pk_fma_f32 v[14:15], v[28:29], v[26:27], v[14:15] op_sel_hi:[0,1,1]
	v_mov_b32_e32 v28, v29
	v_pk_fma_f32 v[18:19], v[28:29], v[26:27], v[18:19] op_sel_hi:[0,1,1]
	ds_write_b32 v44, v58
.LBB0_457:
	s_or_b64 exec, exec, s[28:29]
	v_pk_fma_f32 v[26:27], v[2:3], v[30:31], v[12:13]
	s_waitcnt vmcnt(12)
	v_lshlrev_b32_e32 v28, 16, v38
	v_pk_fma_f32 v[26:27], v[4:5], v[32:33], v[26:27]
	v_and_b32_e32 v29, 0xffff0000, v38
	v_pk_fma_f32 v[26:27], v[6:7], v[34:35], v[26:27]
	s_nop 0
	v_pk_fma_f32 v[26:27], v[8:9], v[36:37], v[26:27]
	s_nop 0
	v_pk_fma_f32 v[26:27], v[10:11], v[28:29], v[26:27]
	s_nop 0
	v_mul_f32_e32 v30, 0xbfb8aa3b, v26
	v_mul_f32_e32 v31, 0xbfb8aa3b, v27
	v_exp_f32_e32 v30, v30
	v_exp_f32_e32 v31, v31
	v_add_f32_e32 v30, 1.0, v30
	v_add_f32_e32 v31, 1.0, v31
	v_rcp_f32_e32 v30, v30
	v_rcp_f32_e32 v31, v31
	s_nop 0
	v_pk_mul_f32 v[30:31], v[26:27], v[30:31]
	s_and_saveexec_b64 s[28:29], s[8:9]
	s_xor_b64 s[28:29], exec, s[28:29]
	s_cbranch_execz .LBB0_459
	v_add_co_u32_e32 v26, vcc, 0x51360000, v24
	v_cvt_pk_bf16_f32 v30, v30, v31
	s_nop 0
	v_addc_co_u32_e32 v27, vcc, 0, v25, vcc
	global_store_dword v[26:27], v30, off offset:1536 nt
.LBB0_459:
	s_or_saveexec_b64 s[28:29], s[28:29]
	v_lshl_add_u64 v[26:27], s[94:95], 0, v[20:21]
	s_xor_b64 exec, exec, s[28:29]
	s_cbranch_execz .LBB0_461
	v_add_u32_e32 v58, 4, v43
	ds_read2st64_b32 v[58:59], v58 offset1:4
	v_pk_mul_f32 v[30:31], v[30:31], s[80:81] op_sel_hi:[1,0]
	s_nop 0
	v_cvt_pk_bf16_f32 v38, v30, v31
	v_add_co_u32_e32 v30, vcc, 0x52360000, v26
	ds_write_b32 v44, v38 offset:64
	s_nop 0
	v_addc_co_u32_e32 v31, vcc, 0, v27, vcc
	global_store_dword v[30:31], v38, off offset:1536 nt
	v_lshlrev_b32_e32 v30, 16, v38
	v_and_b32_e32 v31, 0xffff0000, v38
	s_waitcnt lgkmcnt(1)
	v_mov_b32_e32 v38, v59
	v_pk_fma_f32 v[14:15], v[58:59], v[30:31], v[14:15] op_sel_hi:[0,1,1]
	s_waitcnt vmcnt(12)
	v_pk_fma_f32 v[18:19], v[38:39], v[30:31], v[18:19] op_sel_hi:[0,1,1]
.LBB0_461:
	s_or_b64 exec, exec, s[28:29]
	v_pk_fma_f32 v[30:31], v[2:3], v[32:33], v[12:13]
	s_waitcnt vmcnt(11)
	v_lshlrev_b32_e32 v38, 16, v39
	v_pk_fma_f32 v[30:31], v[4:5], v[34:35], v[30:31]
	v_and_b32_e32 v39, 0xffff0000, v39
	v_pk_fma_f32 v[30:31], v[6:7], v[36:37], v[30:31]
	s_nop 0
	v_pk_fma_f32 v[30:31], v[8:9], v[28:29], v[30:31]
	s_nop 0
	v_pk_fma_f32 v[30:31], v[10:11], v[38:39], v[30:31]
	s_nop 0
	v_mul_f32_e32 v32, 0xbfb8aa3b, v30
	v_mul_f32_e32 v33, 0xbfb8aa3b, v31
	v_exp_f32_e32 v32, v32
	v_exp_f32_e32 v33, v33
	v_add_f32_e32 v32, 1.0, v32
	v_add_f32_e32 v33, 1.0, v33
	v_rcp_f32_e32 v32, v32
	v_rcp_f32_e32 v33, v33
	s_nop 0
	v_pk_mul_f32 v[30:31], v[30:31], v[32:33]
	s_and_saveexec_b64 s[28:29], s[8:9]
	s_xor_b64 s[28:29], exec, s[28:29]
	s_cbranch_execz .LBB0_463
	v_cvt_pk_bf16_f32 v32, v30, v31
	v_add_co_u32_e32 v30, vcc, 0x51360000, v24
	s_nop 1
	v_addc_co_u32_e32 v31, vcc, 0, v25, vcc
	global_store_dword v[30:31], v32, off offset:2560 nt
.LBB0_463:
	s_andn2_saveexec_b64 s[28:29], s[28:29]
	s_cbranch_execz .LBB0_465
	v_add_u32_e32 v32, 8, v43
	ds_read2st64_b32 v[32:33], v32 offset1:4
	v_pk_mul_f32 v[30:31], v[30:31], s[80:81] op_sel_hi:[1,0]
	s_nop 0
	v_cvt_pk_bf16_f32 v58, v30, v31
	v_add_co_u32_e32 v30, vcc, 0x52360000, v26
	ds_write_b32 v44, v58 offset:128
	s_nop 0
	v_addc_co_u32_e32 v31, vcc, 0, v27, vcc
	global_store_dword v[30:31], v58, off offset:2560 nt
	v_lshlrev_b32_e32 v30, 16, v58
	v_and_b32_e32 v31, 0xffff0000, v58
	s_waitcnt lgkmcnt(1)
	v_pk_fma_f32 v[14:15], v[32:33], v[30:31], v[14:15] op_sel_hi:[0,1,1]
	v_mov_b32_e32 v32, v33
	v_pk_fma_f32 v[18:19], v[32:33], v[30:31], v[18:19] op_sel_hi:[0,1,1]
.LBB0_465:
	s_or_b64 exec, exec, s[28:29]
	v_pk_fma_f32 v[32:33], v[2:3], v[34:35], v[12:13]
	s_waitcnt vmcnt(10)
	v_lshlrev_b32_e32 v30, 16, v57
	v_pk_fma_f32 v[32:33], v[4:5], v[36:37], v[32:33]
	v_and_b32_e32 v31, 0xffff0000, v57
	v_pk_fma_f32 v[32:33], v[6:7], v[28:29], v[32:33]
	s_nop 0
	v_pk_fma_f32 v[32:33], v[8:9], v[38:39], v[32:33]
	s_nop 0
	v_pk_fma_f32 v[32:33], v[10:11], v[30:31], v[32:33]
	s_nop 0
	v_mul_f32_e32 v34, 0xbfb8aa3b, v32
	v_mul_f32_e32 v35, 0xbfb8aa3b, v33
	v_exp_f32_e32 v34, v34
	v_exp_f32_e32 v35, v35
	v_add_f32_e32 v34, 1.0, v34
	v_add_f32_e32 v35, 1.0, v35
	v_rcp_f32_e32 v34, v34
	v_rcp_f32_e32 v35, v35
	s_nop 0
	v_pk_mul_f32 v[32:33], v[32:33], v[34:35]
	s_and_saveexec_b64 s[28:29], s[8:9]
	s_xor_b64 s[28:29], exec, s[28:29]
	s_cbranch_execz .LBB0_467
	v_cvt_pk_bf16_f32 v34, v32, v33
	v_add_co_u32_e32 v32, vcc, 0x51360000, v24
	s_nop 1
	v_addc_co_u32_e32 v33, vcc, 0, v25, vcc
	global_store_dword v[32:33], v34, off offset:3584 nt
.LBB0_467:
	s_andn2_saveexec_b64 s[28:29], s[28:29]
	s_cbranch_execz .LBB0_469
	v_add_u32_e32 v34, 12, v43
	ds_read2st64_b32 v[34:35], v34 offset1:4
	v_pk_mul_f32 v[32:33], v[32:33], s[80:81] op_sel_hi:[1,0]
	s_nop 0
	v_cvt_pk_bf16_f32 v57, v32, v33
	v_add_co_u32_e32 v32, vcc, 0x52360000, v26
	ds_write_b32 v44, v57 offset:192
	s_nop 0
	v_addc_co_u32_e32 v33, vcc, 0, v27, vcc
	global_store_dword v[32:33], v57, off offset:3584 nt
	v_lshlrev_b32_e32 v32, 16, v57
	v_and_b32_e32 v33, 0xffff0000, v57
	s_waitcnt lgkmcnt(1)
	v_pk_fma_f32 v[14:15], v[34:35], v[32:33], v[14:15] op_sel_hi:[0,1,1]
	v_mov_b32_e32 v34, v35
	v_pk_fma_f32 v[18:19], v[34:35], v[32:33], v[18:19] op_sel_hi:[0,1,1]
.LBB0_469:
	s_or_b64 exec, exec, s[28:29]
	v_pk_fma_f32 v[34:35], v[2:3], v[36:37], v[12:13]
	s_waitcnt vmcnt(9)
	v_lshlrev_b32_e32 v32, 16, v56
	v_pk_fma_f32 v[34:35], v[4:5], v[28:29], v[34:35]
	v_and_b32_e32 v33, 0xffff0000, v56
	v_pk_fma_f32 v[34:35], v[6:7], v[38:39], v[34:35]
	s_nop 0
	v_pk_fma_f32 v[34:35], v[8:9], v[30:31], v[34:35]
	s_nop 0
	v_pk_fma_f32 v[34:35], v[10:11], v[32:33], v[34:35]
	s_nop 0
	v_mul_f32_e32 v36, 0xbfb8aa3b, v34
	v_mul_f32_e32 v37, 0xbfb8aa3b, v35
	v_exp_f32_e32 v36, v36
	v_exp_f32_e32 v37, v37
	v_add_f32_e32 v36, 1.0, v36
	v_add_f32_e32 v37, 1.0, v37
	v_rcp_f32_e32 v36, v36
	v_rcp_f32_e32 v37, v37
	s_nop 0
	v_pk_mul_f32 v[34:35], v[34:35], v[36:37]
	s_and_saveexec_b64 s[28:29], s[8:9]
	s_xor_b64 s[28:29], exec, s[28:29]
	s_cbranch_execz .LBB0_471
	v_cvt_pk_bf16_f32 v36, v34, v35
	v_add_co_u32_e32 v34, vcc, 0x51361000, v24
	s_nop 1
	v_addc_co_u32_e32 v35, vcc, 0, v25, vcc
	global_store_dword v[34:35], v36, off offset:512 nt
.LBB0_471:
	s_andn2_saveexec_b64 s[28:29], s[28:29]
	s_cbranch_execz .LBB0_473
	v_add_u32_e32 v36, 16, v43
	ds_read2st64_b32 v[36:37], v36 offset1:4
	v_pk_mul_f32 v[34:35], v[34:35], s[80:81] op_sel_hi:[1,0]
	s_nop 0
	v_cvt_pk_bf16_f32 v56, v34, v35
	v_add_co_u32_e32 v34, vcc, 0x52361000, v26
	ds_write_b32 v44, v56 offset:2048
	s_nop 0
	v_addc_co_u32_e32 v35, vcc, 0, v27, vcc
	global_store_dword v[34:35], v56, off offset:512 nt
	v_lshlrev_b32_e32 v34, 16, v56
	v_and_b32_e32 v35, 0xffff0000, v56
	s_waitcnt lgkmcnt(1)
	v_pk_fma_f32 v[14:15], v[36:37], v[34:35], v[14:15] op_sel_hi:[0,1,1]
	v_mov_b32_e32 v36, v37
	v_pk_fma_f32 v[18:19], v[36:37], v[34:35], v[18:19] op_sel_hi:[0,1,1]
.LBB0_473:
	s_or_b64 exec, exec, s[28:29]
	v_pk_fma_f32 v[28:29], v[2:3], v[28:29], v[12:13]
	s_waitcnt vmcnt(8)
	v_lshlrev_b32_e32 v34, 16, v55
	v_pk_fma_f32 v[28:29], v[4:5], v[38:39], v[28:29]
	v_and_b32_e32 v35, 0xffff0000, v55
	v_pk_fma_f32 v[28:29], v[6:7], v[30:31], v[28:29]
	s_nop 0
	v_pk_fma_f32 v[28:29], v[8:9], v[32:33], v[28:29]
	s_nop 0
	v_pk_fma_f32 v[28:29], v[10:11], v[34:35], v[28:29]
	s_nop 0
	v_mul_f32_e32 v36, 0xbfb8aa3b, v28
	v_mul_f32_e32 v37, 0xbfb8aa3b, v29
	v_exp_f32_e32 v36, v36
	v_exp_f32_e32 v37, v37
	v_add_f32_e32 v36, 1.0, v36
	v_add_f32_e32 v37, 1.0, v37
	v_rcp_f32_e32 v36, v36
	v_rcp_f32_e32 v37, v37
	s_nop 0
	v_pk_mul_f32 v[28:29], v[28:29], v[36:37]
	s_and_saveexec_b64 s[28:29], s[8:9]
	s_xor_b64 s[28:29], exec, s[28:29]
	s_cbranch_execz .LBB0_475
	v_cvt_pk_bf16_f32 v36, v28, v29
	v_add_co_u32_e32 v28, vcc, 0x51361000, v24
	s_nop 1
	v_addc_co_u32_e32 v29, vcc, 0, v25, vcc
	global_store_dword v[28:29], v36, off offset:1536 nt
.LBB0_475:
	s_andn2_saveexec_b64 s[28:29], s[28:29]
	s_cbranch_execz .LBB0_477
	v_add_u32_e32 v36, 20, v43
	ds_read2st64_b32 v[36:37], v36 offset1:4
	v_pk_mul_f32 v[28:29], v[28:29], s[80:81] op_sel_hi:[1,0]
	s_nop 0
	v_cvt_pk_bf16_f32 v55, v28, v29
	v_add_co_u32_e32 v28, vcc, 0x52361000, v26
	ds_write_b32 v44, v55 offset:2112
	s_nop 0
	v_addc_co_u32_e32 v29, vcc, 0, v27, vcc
	global_store_dword v[28:29], v55, off offset:1536 nt
	v_lshlrev_b32_e32 v28, 16, v55
	v_and_b32_e32 v29, 0xffff0000, v55
	s_waitcnt lgkmcnt(1)
	v_pk_fma_f32 v[14:15], v[36:37], v[28:29], v[14:15] op_sel_hi:[0,1,1]
	v_mov_b32_e32 v36, v37
	v_pk_fma_f32 v[18:19], v[36:37], v[28:29], v[18:19] op_sel_hi:[0,1,1]
.LBB0_477:
	s_or_b64 exec, exec, s[28:29]
	v_pk_fma_f32 v[28:29], v[2:3], v[38:39], v[12:13]
	s_waitcnt vmcnt(7)
	v_lshlrev_b32_e32 v36, 16, v54
	v_pk_fma_f32 v[28:29], v[4:5], v[30:31], v[28:29]
	v_and_b32_e32 v37, 0xffff0000, v54
	v_pk_fma_f32 v[28:29], v[6:7], v[32:33], v[28:29]
	s_nop 0
	v_pk_fma_f32 v[28:29], v[8:9], v[34:35], v[28:29]
	s_nop 0
	v_pk_fma_f32 v[28:29], v[10:11], v[36:37], v[28:29]
	s_nop 0
	v_mul_f32_e32 v38, 0xbfb8aa3b, v28
	v_mul_f32_e32 v39, 0xbfb8aa3b, v29
	v_exp_f32_e32 v38, v38
	v_exp_f32_e32 v39, v39
	v_add_f32_e32 v38, 1.0, v38
	v_add_f32_e32 v39, 1.0, v39
	v_rcp_f32_e32 v38, v38
	v_rcp_f32_e32 v39, v39
	s_nop 0
	v_pk_mul_f32 v[28:29], v[28:29], v[38:39]
	s_and_saveexec_b64 s[28:29], s[8:9]
	s_xor_b64 s[28:29], exec, s[28:29]
	s_cbranch_execz .LBB0_479
	v_cvt_pk_bf16_f32 v38, v28, v29
	v_add_co_u32_e32 v28, vcc, 0x51361000, v24
	s_nop 1
	v_addc_co_u32_e32 v29, vcc, 0, v25, vcc
	global_store_dword v[28:29], v38, off offset:2560 nt
.LBB0_479:
	s_andn2_saveexec_b64 s[28:29], s[28:29]
	s_cbranch_execz .LBB0_481
	v_add_u32_e32 v38, 24, v43
	ds_read2st64_b32 v[38:39], v38 offset1:4
	v_pk_mul_f32 v[28:29], v[28:29], s[80:81] op_sel_hi:[1,0]
	s_nop 0
	v_cvt_pk_bf16_f32 v54, v28, v29
	v_add_co_u32_e32 v28, vcc, 0x52361000, v26
	ds_write_b32 v44, v54 offset:2176
	s_nop 0
	v_addc_co_u32_e32 v29, vcc, 0, v27, vcc
	global_store_dword v[28:29], v54, off offset:2560 nt
	v_lshlrev_b32_e32 v28, 16, v54
	v_and_b32_e32 v29, 0xffff0000, v54
	s_waitcnt lgkmcnt(1)
	v_pk_fma_f32 v[14:15], v[38:39], v[28:29], v[14:15] op_sel_hi:[0,1,1]
	v_mov_b32_e32 v38, v39
	v_pk_fma_f32 v[18:19], v[38:39], v[28:29], v[18:19] op_sel_hi:[0,1,1]
.LBB0_481:
	s_or_b64 exec, exec, s[28:29]
	v_pk_fma_f32 v[30:31], v[2:3], v[30:31], v[12:13]
	s_waitcnt vmcnt(6)
	v_lshlrev_b32_e32 v28, 16, v53
	v_pk_fma_f32 v[30:31], v[4:5], v[32:33], v[30:31]
	v_and_b32_e32 v29, 0xffff0000, v53
	v_pk_fma_f32 v[30:31], v[6:7], v[34:35], v[30:31]
	s_nop 0
	v_pk_fma_f32 v[30:31], v[8:9], v[36:37], v[30:31]
	s_nop 0
	v_pk_fma_f32 v[30:31], v[10:11], v[28:29], v[30:31]
	s_nop 0
	v_mul_f32_e32 v38, 0xbfb8aa3b, v30
	v_mul_f32_e32 v39, 0xbfb8aa3b, v31
	v_exp_f32_e32 v38, v38
	v_exp_f32_e32 v39, v39
	v_add_f32_e32 v38, 1.0, v38
	v_add_f32_e32 v39, 1.0, v39
	v_rcp_f32_e32 v38, v38
	v_rcp_f32_e32 v39, v39
	s_nop 0
	v_pk_mul_f32 v[30:31], v[30:31], v[38:39]
	s_and_saveexec_b64 s[28:29], s[8:9]
	s_xor_b64 s[28:29], exec, s[28:29]
	s_cbranch_execz .LBB0_483
	v_cvt_pk_bf16_f32 v38, v30, v31
	v_add_co_u32_e32 v30, vcc, 0x51361000, v24
	s_nop 1
	v_addc_co_u32_e32 v31, vcc, 0, v25, vcc
	global_store_dword v[30:31], v38, off offset:3584 nt
.LBB0_483:
	s_andn2_saveexec_b64 s[28:29], s[28:29]
	s_cbranch_execz .LBB0_485
	v_add_u32_e32 v38, 28, v43
	ds_read2st64_b32 v[38:39], v38 offset1:4
	v_pk_mul_f32 v[30:31], v[30:31], s[80:81] op_sel_hi:[1,0]
	s_nop 0
	v_cvt_pk_bf16_f32 v53, v30, v31
	v_add_co_u32_e32 v30, vcc, 0x52361000, v26
	ds_write_b32 v44, v53 offset:2240
	s_nop 0
	v_addc_co_u32_e32 v31, vcc, 0, v27, vcc
	global_store_dword v[30:31], v53, off offset:3584 nt
	v_lshlrev_b32_e32 v30, 16, v53
	v_and_b32_e32 v31, 0xffff0000, v53
	s_waitcnt lgkmcnt(1)
	v_pk_fma_f32 v[14:15], v[38:39], v[30:31], v[14:15] op_sel_hi:[0,1,1]
	v_mov_b32_e32 v38, v39
	v_pk_fma_f32 v[18:19], v[38:39], v[30:31], v[18:19] op_sel_hi:[0,1,1]
.LBB0_485:
	s_or_b64 exec, exec, s[28:29]
	v_pk_fma_f32 v[32:33], v[2:3], v[32:33], v[12:13]
	s_waitcnt vmcnt(5)
	v_lshlrev_b32_e32 v30, 16, v52
	v_pk_fma_f32 v[32:33], v[4:5], v[34:35], v[32:33]
	v_and_b32_e32 v31, 0xffff0000, v52
	v_pk_fma_f32 v[32:33], v[6:7], v[36:37], v[32:33]
	s_nop 0
	v_pk_fma_f32 v[32:33], v[8:9], v[28:29], v[32:33]
	s_nop 0
	v_pk_fma_f32 v[32:33], v[10:11], v[30:31], v[32:33]
	s_nop 0
	v_mul_f32_e32 v38, 0xbfb8aa3b, v32
	v_mul_f32_e32 v39, 0xbfb8aa3b, v33
	v_exp_f32_e32 v38, v38
	v_exp_f32_e32 v39, v39
	v_add_f32_e32 v38, 1.0, v38
	v_add_f32_e32 v39, 1.0, v39
	v_rcp_f32_e32 v38, v38
	v_rcp_f32_e32 v39, v39
	s_nop 0
	v_pk_mul_f32 v[32:33], v[32:33], v[38:39]
	s_and_saveexec_b64 s[28:29], s[8:9]
	s_xor_b64 s[28:29], exec, s[28:29]
	s_cbranch_execz .LBB0_487
	v_cvt_pk_bf16_f32 v38, v32, v33
	v_add_co_u32_e32 v32, vcc, 0x51362000, v24
	s_nop 1
	v_addc_co_u32_e32 v33, vcc, 0, v25, vcc
	global_store_dword v[32:33], v38, off offset:512 nt
.LBB0_487:
	s_andn2_saveexec_b64 s[28:29], s[28:29]
	s_cbranch_execz .LBB0_489
	v_add_u32_e32 v38, 32, v43
	ds_read2st64_b32 v[38:39], v38 offset1:4
	v_pk_mul_f32 v[32:33], v[32:33], s[80:81] op_sel_hi:[1,0]
	s_nop 0
	v_cvt_pk_bf16_f32 v52, v32, v33
	v_add_co_u32_e32 v32, vcc, 0x52362000, v26
	ds_write_b32 v44, v52 offset:256
	s_nop 0
	v_addc_co_u32_e32 v33, vcc, 0, v27, vcc
	global_store_dword v[32:33], v52, off offset:512 nt
	v_lshlrev_b32_e32 v32, 16, v52
	v_and_b32_e32 v33, 0xffff0000, v52
	s_waitcnt lgkmcnt(1)
	v_pk_fma_f32 v[14:15], v[38:39], v[32:33], v[14:15] op_sel_hi:[0,1,1]
	v_mov_b32_e32 v38, v39
	v_pk_fma_f32 v[18:19], v[38:39], v[32:33], v[18:19] op_sel_hi:[0,1,1]
.LBB0_489:
	s_or_b64 exec, exec, s[28:29]
	v_pk_fma_f32 v[34:35], v[2:3], v[34:35], v[12:13]
	s_waitcnt vmcnt(4)
	v_lshlrev_b32_e32 v32, 16, v51
	v_pk_fma_f32 v[34:35], v[4:5], v[36:37], v[34:35]
	v_and_b32_e32 v33, 0xffff0000, v51
	v_pk_fma_f32 v[34:35], v[6:7], v[28:29], v[34:35]
	s_nop 0
	v_pk_fma_f32 v[34:35], v[8:9], v[30:31], v[34:35]
	s_nop 0
	v_pk_fma_f32 v[34:35], v[10:11], v[32:33], v[34:35]
	s_nop 0
	v_mul_f32_e32 v38, 0xbfb8aa3b, v34
	v_mul_f32_e32 v39, 0xbfb8aa3b, v35
	v_exp_f32_e32 v38, v38
	v_exp_f32_e32 v39, v39
	v_add_f32_e32 v38, 1.0, v38
	v_add_f32_e32 v39, 1.0, v39
	v_rcp_f32_e32 v38, v38
	v_rcp_f32_e32 v39, v39
	s_nop 0
	v_pk_mul_f32 v[34:35], v[34:35], v[38:39]
	s_and_saveexec_b64 s[28:29], s[8:9]
	s_xor_b64 s[28:29], exec, s[28:29]
	s_cbranch_execz .LBB0_491
	v_cvt_pk_bf16_f32 v38, v34, v35
	v_add_co_u32_e32 v34, vcc, 0x51362000, v24
	s_nop 1
	v_addc_co_u32_e32 v35, vcc, 0, v25, vcc
	global_store_dword v[34:35], v38, off offset:1536 nt
.LBB0_491:
	s_andn2_saveexec_b64 s[28:29], s[28:29]
	s_cbranch_execz .LBB0_493
	v_add_u32_e32 v38, 36, v43
	ds_read2st64_b32 v[38:39], v38 offset1:4
	v_pk_mul_f32 v[34:35], v[34:35], s[80:81] op_sel_hi:[1,0]
	s_nop 0
	v_cvt_pk_bf16_f32 v51, v34, v35
	v_add_co_u32_e32 v34, vcc, 0x52362000, v26
	ds_write_b32 v44, v51 offset:320
	s_nop 0
	v_addc_co_u32_e32 v35, vcc, 0, v27, vcc
	global_store_dword v[34:35], v51, off offset:1536 nt
	v_lshlrev_b32_e32 v34, 16, v51
	v_and_b32_e32 v35, 0xffff0000, v51
	s_waitcnt lgkmcnt(1)
	v_pk_fma_f32 v[14:15], v[38:39], v[34:35], v[14:15] op_sel_hi:[0,1,1]
	v_mov_b32_e32 v38, v39
	v_pk_fma_f32 v[18:19], v[38:39], v[34:35], v[18:19] op_sel_hi:[0,1,1]
.LBB0_493:
	s_or_b64 exec, exec, s[28:29]
	v_pk_fma_f32 v[36:37], v[2:3], v[36:37], v[12:13]
	s_waitcnt vmcnt(3)
	v_lshlrev_b32_e32 v34, 16, v50
	v_pk_fma_f32 v[36:37], v[4:5], v[28:29], v[36:37]
	v_and_b32_e32 v35, 0xffff0000, v50
	v_pk_fma_f32 v[36:37], v[6:7], v[30:31], v[36:37]
	s_nop 0
	v_pk_fma_f32 v[36:37], v[8:9], v[32:33], v[36:37]
	s_nop 0
	v_pk_fma_f32 v[36:37], v[10:11], v[34:35], v[36:37]
	s_nop 0
	v_mul_f32_e32 v38, 0xbfb8aa3b, v36
	v_mul_f32_e32 v39, 0xbfb8aa3b, v37
	v_exp_f32_e32 v38, v38
	v_exp_f32_e32 v39, v39
	v_add_f32_e32 v38, 1.0, v38
	v_add_f32_e32 v39, 1.0, v39
	v_rcp_f32_e32 v38, v38
	v_rcp_f32_e32 v39, v39
	s_nop 0
	v_pk_mul_f32 v[36:37], v[36:37], v[38:39]
	s_and_saveexec_b64 s[28:29], s[8:9]
	s_xor_b64 s[28:29], exec, s[28:29]
	s_cbranch_execz .LBB0_495
	v_cvt_pk_bf16_f32 v38, v36, v37
	v_add_co_u32_e32 v36, vcc, 0x51362000, v24
	s_nop 1
	v_addc_co_u32_e32 v37, vcc, 0, v25, vcc
	global_store_dword v[36:37], v38, off offset:2560 nt
.LBB0_495:
	s_andn2_saveexec_b64 s[28:29], s[28:29]
	s_cbranch_execz .LBB0_497
	v_add_u32_e32 v38, 40, v43
	ds_read2st64_b32 v[38:39], v38 offset1:4
	v_pk_mul_f32 v[36:37], v[36:37], s[80:81] op_sel_hi:[1,0]
	s_nop 0
	v_cvt_pk_bf16_f32 v50, v36, v37
	v_add_co_u32_e32 v36, vcc, 0x52362000, v26
	ds_write_b32 v44, v50 offset:384
	s_nop 0
	v_addc_co_u32_e32 v37, vcc, 0, v27, vcc
	global_store_dword v[36:37], v50, off offset:2560 nt
	v_lshlrev_b32_e32 v36, 16, v50
	v_and_b32_e32 v37, 0xffff0000, v50
	s_waitcnt lgkmcnt(1)
	v_pk_fma_f32 v[14:15], v[38:39], v[36:37], v[14:15] op_sel_hi:[0,1,1]
	v_mov_b32_e32 v38, v39
	v_pk_fma_f32 v[18:19], v[38:39], v[36:37], v[18:19] op_sel_hi:[0,1,1]
.LBB0_497:
	s_or_b64 exec, exec, s[28:29]
	v_pk_fma_f32 v[28:29], v[2:3], v[28:29], v[12:13]
	s_waitcnt vmcnt(2)
	v_lshlrev_b32_e32 v36, 16, v49
	v_pk_fma_f32 v[28:29], v[4:5], v[30:31], v[28:29]
	v_and_b32_e32 v37, 0xffff0000, v49
	v_pk_fma_f32 v[28:29], v[6:7], v[32:33], v[28:29]
	s_nop 0
	v_pk_fma_f32 v[28:29], v[8:9], v[34:35], v[28:29]
	s_nop 0
	v_pk_fma_f32 v[28:29], v[10:11], v[36:37], v[28:29]
	s_nop 0
	v_mul_f32_e32 v38, 0xbfb8aa3b, v28
	v_mul_f32_e32 v39, 0xbfb8aa3b, v29
	v_exp_f32_e32 v38, v38
	v_exp_f32_e32 v39, v39
	v_add_f32_e32 v38, 1.0, v38
	v_add_f32_e32 v39, 1.0, v39
	v_rcp_f32_e32 v38, v38
	v_rcp_f32_e32 v39, v39
	s_nop 0
	v_pk_mul_f32 v[28:29], v[28:29], v[38:39]
	s_and_saveexec_b64 s[28:29], s[8:9]
	s_xor_b64 s[28:29], exec, s[28:29]
	s_cbranch_execz .LBB0_499
	v_cvt_pk_bf16_f32 v38, v28, v29
	v_add_co_u32_e32 v28, vcc, 0x51362000, v24
	s_nop 1
	v_addc_co_u32_e32 v29, vcc, 0, v25, vcc
	global_store_dword v[28:29], v38, off offset:3584 nt
.LBB0_499:
	s_andn2_saveexec_b64 s[28:29], s[28:29]
	s_cbranch_execz .LBB0_501
	v_add_u32_e32 v38, 44, v43
	ds_read2st64_b32 v[38:39], v38 offset1:4
	v_pk_mul_f32 v[28:29], v[28:29], s[80:81] op_sel_hi:[1,0]
	s_nop 0
	v_cvt_pk_bf16_f32 v49, v28, v29
	v_add_co_u32_e32 v28, vcc, 0x52362000, v26
	ds_write_b32 v44, v49 offset:448
	s_nop 0
	v_addc_co_u32_e32 v29, vcc, 0, v27, vcc
	global_store_dword v[28:29], v49, off offset:3584 nt
	v_lshlrev_b32_e32 v28, 16, v49
	v_and_b32_e32 v29, 0xffff0000, v49
	s_waitcnt lgkmcnt(1)
	v_pk_fma_f32 v[14:15], v[38:39], v[28:29], v[14:15] op_sel_hi:[0,1,1]
	v_mov_b32_e32 v38, v39
	v_pk_fma_f32 v[18:19], v[38:39], v[28:29], v[18:19] op_sel_hi:[0,1,1]
.LBB0_501:
	s_or_b64 exec, exec, s[28:29]
	v_pk_fma_f32 v[30:31], v[2:3], v[30:31], v[12:13]
	s_waitcnt vmcnt(1)
	v_lshlrev_b32_e32 v28, 16, v48
	v_pk_fma_f32 v[30:31], v[4:5], v[32:33], v[30:31]
	v_and_b32_e32 v29, 0xffff0000, v48
	v_pk_fma_f32 v[30:31], v[6:7], v[34:35], v[30:31]
	s_nop 0
	v_pk_fma_f32 v[30:31], v[8:9], v[36:37], v[30:31]
	s_nop 0
	v_pk_fma_f32 v[30:31], v[10:11], v[28:29], v[30:31]
	s_nop 0
	v_mul_f32_e32 v38, 0xbfb8aa3b, v30
	v_mul_f32_e32 v39, 0xbfb8aa3b, v31
	v_exp_f32_e32 v38, v38
	v_exp_f32_e32 v39, v39
	v_add_f32_e32 v38, 1.0, v38
	v_add_f32_e32 v39, 1.0, v39
	v_rcp_f32_e32 v38, v38
	v_rcp_f32_e32 v39, v39
	s_nop 0
	v_pk_mul_f32 v[30:31], v[30:31], v[38:39]
	s_and_saveexec_b64 s[28:29], s[8:9]
	s_xor_b64 s[28:29], exec, s[28:29]
	s_cbranch_execz .LBB0_503
	v_cvt_pk_bf16_f32 v38, v30, v31
	v_add_co_u32_e32 v30, vcc, 0x51363000, v24
	s_nop 1
	v_addc_co_u32_e32 v31, vcc, 0, v25, vcc
	global_store_dword v[30:31], v38, off offset:512 nt
.LBB0_503:
	s_andn2_saveexec_b64 s[28:29], s[28:29]
	s_cbranch_execz .LBB0_505
	v_add_u32_e32 v38, 48, v43
	ds_read2st64_b32 v[38:39], v38 offset1:4
	v_pk_mul_f32 v[30:31], v[30:31], s[80:81] op_sel_hi:[1,0]
	s_nop 0
	v_cvt_pk_bf16_f32 v48, v30, v31
	v_add_co_u32_e32 v30, vcc, 0x52363000, v26
	ds_write_b32 v44, v48 offset:2304
	s_nop 0
	v_addc_co_u32_e32 v31, vcc, 0, v27, vcc
	global_store_dword v[30:31], v48, off offset:512 nt
	v_lshlrev_b32_e32 v30, 16, v48
	v_and_b32_e32 v31, 0xffff0000, v48
	s_waitcnt lgkmcnt(1)
	v_pk_fma_f32 v[14:15], v[38:39], v[30:31], v[14:15] op_sel_hi:[0,1,1]
	v_mov_b32_e32 v38, v39
	v_pk_fma_f32 v[18:19], v[38:39], v[30:31], v[18:19] op_sel_hi:[0,1,1]
.LBB0_505:
	s_or_b64 exec, exec, s[28:29]
	v_pk_fma_f32 v[32:33], v[2:3], v[32:33], v[12:13]
	s_waitcnt vmcnt(0)
	v_lshlrev_b32_e32 v30, 16, v47
	v_pk_fma_f32 v[32:33], v[4:5], v[34:35], v[32:33]
	v_and_b32_e32 v31, 0xffff0000, v47
	v_pk_fma_f32 v[32:33], v[6:7], v[36:37], v[32:33]
	s_nop 0
	v_pk_fma_f32 v[32:33], v[8:9], v[28:29], v[32:33]
	s_nop 0
	v_pk_fma_f32 v[32:33], v[10:11], v[30:31], v[32:33]
	s_nop 0
	v_mul_f32_e32 v38, 0xbfb8aa3b, v32
	v_mul_f32_e32 v39, 0xbfb8aa3b, v33
	v_exp_f32_e32 v38, v38
	v_exp_f32_e32 v39, v39
	v_add_f32_e32 v38, 1.0, v38
	v_add_f32_e32 v39, 1.0, v39
	v_rcp_f32_e32 v38, v38
	v_rcp_f32_e32 v39, v39
	s_nop 0
	v_pk_mul_f32 v[32:33], v[32:33], v[38:39]
	s_and_saveexec_b64 s[28:29], s[8:9]
	s_xor_b64 s[28:29], exec, s[28:29]
	s_cbranch_execz .LBB0_507
	v_cvt_pk_bf16_f32 v38, v32, v33
	v_add_co_u32_e32 v32, vcc, 0x51363000, v24
	s_nop 1
	v_addc_co_u32_e32 v33, vcc, 0, v25, vcc
	global_store_dword v[32:33], v38, off offset:1536 nt
.LBB0_507:
	s_andn2_saveexec_b64 s[28:29], s[28:29]
	s_cbranch_execz .LBB0_509
	v_add_u32_e32 v38, 52, v43
	ds_read2st64_b32 v[38:39], v38 offset1:4
	v_pk_mul_f32 v[32:33], v[32:33], s[80:81] op_sel_hi:[1,0]
	s_nop 0
	v_cvt_pk_bf16_f32 v47, v32, v33
	v_add_co_u32_e32 v32, vcc, 0x52363000, v26
	ds_write_b32 v44, v47 offset:2368
	s_nop 0
	v_addc_co_u32_e32 v33, vcc, 0, v27, vcc
	global_store_dword v[32:33], v47, off offset:1536 nt
	v_lshlrev_b32_e32 v32, 16, v47
	v_and_b32_e32 v33, 0xffff0000, v47
	s_waitcnt lgkmcnt(1)
	v_pk_fma_f32 v[14:15], v[38:39], v[32:33], v[14:15] op_sel_hi:[0,1,1]
	v_mov_b32_e32 v38, v39
	v_pk_fma_f32 v[18:19], v[38:39], v[32:33], v[18:19] op_sel_hi:[0,1,1]
.LBB0_509:
	s_or_b64 exec, exec, s[28:29]
	v_pk_fma_f32 v[34:35], v[2:3], v[34:35], v[12:13]
	v_lshlrev_b32_e32 v32, 16, v46
	v_pk_fma_f32 v[34:35], v[4:5], v[36:37], v[34:35]
	v_and_b32_e32 v33, 0xffff0000, v46
	v_pk_fma_f32 v[34:35], v[6:7], v[28:29], v[34:35]
	s_nop 0
	v_pk_fma_f32 v[34:35], v[8:9], v[30:31], v[34:35]
	s_nop 0
	v_pk_fma_f32 v[34:35], v[10:11], v[32:33], v[34:35]
	s_nop 0
	v_mul_f32_e32 v38, 0xbfb8aa3b, v34
	v_mul_f32_e32 v39, 0xbfb8aa3b, v35
	v_exp_f32_e32 v38, v38
	v_exp_f32_e32 v39, v39
	v_add_f32_e32 v38, 1.0, v38
	v_add_f32_e32 v39, 1.0, v39
	v_rcp_f32_e32 v38, v38
	v_rcp_f32_e32 v39, v39
	s_nop 0
	v_pk_mul_f32 v[34:35], v[34:35], v[38:39]
	s_and_saveexec_b64 s[28:29], s[8:9]
	s_xor_b64 s[28:29], exec, s[28:29]
	s_cbranch_execz .LBB0_511
	v_cvt_pk_bf16_f32 v38, v34, v35
	v_add_co_u32_e32 v34, vcc, 0x51363000, v24
	s_nop 1
	v_addc_co_u32_e32 v35, vcc, 0, v25, vcc
	global_store_dword v[34:35], v38, off offset:2560 nt
.LBB0_511:
	s_andn2_saveexec_b64 s[28:29], s[28:29]
	s_cbranch_execz .LBB0_513
	v_add_u32_e32 v38, 56, v43
	ds_read2st64_b32 v[38:39], v38 offset1:4
	v_pk_mul_f32 v[34:35], v[34:35], s[80:81] op_sel_hi:[1,0]
	s_nop 0
	v_cvt_pk_bf16_f32 v46, v34, v35
	v_add_co_u32_e32 v34, vcc, 0x52363000, v26
	ds_write_b32 v44, v46 offset:2432
	s_nop 0
	v_addc_co_u32_e32 v35, vcc, 0, v27, vcc
	global_store_dword v[34:35], v46, off offset:2560 nt
	v_lshlrev_b32_e32 v34, 16, v46
	v_and_b32_e32 v35, 0xffff0000, v46
	s_waitcnt lgkmcnt(1)
	v_pk_fma_f32 v[14:15], v[38:39], v[34:35], v[14:15] op_sel_hi:[0,1,1]
	v_mov_b32_e32 v38, v39
	v_pk_fma_f32 v[18:19], v[38:39], v[34:35], v[18:19] op_sel_hi:[0,1,1]
.LBB0_513:
	s_or_b64 exec, exec, s[28:29]
	v_pk_fma_f32 v[36:37], v[2:3], v[36:37], v[12:13]
	v_lshlrev_b32_e32 v34, 16, v45
	v_pk_fma_f32 v[36:37], v[4:5], v[28:29], v[36:37]
	v_and_b32_e32 v35, 0xffff0000, v45
	v_pk_fma_f32 v[36:37], v[6:7], v[30:31], v[36:37]
	s_nop 0
	v_pk_fma_f32 v[36:37], v[8:9], v[32:33], v[36:37]
	s_nop 0
	v_pk_fma_f32 v[36:37], v[10:11], v[34:35], v[36:37]
	s_nop 0
	v_mul_f32_e32 v38, 0xbfb8aa3b, v36
	v_mul_f32_e32 v39, 0xbfb8aa3b, v37
	v_exp_f32_e32 v38, v38
	v_exp_f32_e32 v39, v39
	v_add_f32_e32 v38, 1.0, v38
	v_add_f32_e32 v39, 1.0, v39
	v_rcp_f32_e32 v38, v38
	v_rcp_f32_e32 v39, v39
	s_nop 0
	v_pk_mul_f32 v[36:37], v[36:37], v[38:39]
	s_and_saveexec_b64 s[28:29], s[8:9]
	s_xor_b64 s[28:29], exec, s[28:29]
	s_cbranch_execz .LBB0_515
	v_add_co_u32_e32 v24, vcc, 0x51363000, v24
	v_cvt_pk_bf16_f32 v26, v36, v37
	s_nop 0
	v_addc_co_u32_e32 v25, vcc, 0, v25, vcc
	global_store_dword v[24:25], v26, off offset:3584 nt
.LBB0_515:
	s_andn2_saveexec_b64 s[28:29], s[28:29]
	s_cbranch_execz .LBB0_448
	v_pk_mul_f32 v[24:25], v[36:37], s[80:81] op_sel_hi:[1,0]
	s_nop 0
	v_cvt_pk_bf16_f32 v36, v24, v25
	v_add_co_u32_e32 v24, vcc, 0x52363000, v26
	v_add_u32_e32 v26, 60, v43
	s_nop 0
	v_addc_co_u32_e32 v25, vcc, 0, v27, vcc
	ds_read2st64_b32 v[26:27], v26 offset1:4
	global_store_dword v[24:25], v36, off offset:3584 nt
	v_lshlrev_b32_e32 v24, 16, v36
	v_and_b32_e32 v25, 0xffff0000, v36
	ds_write_b32 v44, v36 offset:2496
	s_waitcnt lgkmcnt(1)
	v_pk_fma_f32 v[14:15], v[26:27], v[24:25], v[14:15] op_sel_hi:[0,1,1]
	v_mov_b32_e32 v26, v27
	v_pk_fma_f32 v[18:19], v[26:27], v[24:25], v[18:19] op_sel_hi:[0,1,1]
	s_branch .LBB0_448
.LBB0_517:
	s_and_saveexec_b64 s[28:29], s[8:9]
	s_xor_b64 s[8:9], exec, s[28:29]
	s_lshl_b32 s10, s36, 3
	s_or_saveexec_b64 s[8:9], s[8:9]
	v_mov_b32_e32 v2, s10
	s_xor_b64 exec, exec, s[8:9]
	s_cbranch_execz .LBB0_521
	s_lshl_b32 s10, s36, 3
	v_lshl_add_u32 v4, v1, 1, s10
	v_ashrrev_i32_e32 v5, 31, v4
	v_or_b32_e32 v6, 1, v4
	v_lshlrev_b64 v[4:5], 15, v[4:5]
	v_and_b32_e32 v3, 0x7e, v0
	v_lshl_add_u64 v[4:5], s[48:49], 0, v[4:5]
	s_lshl_b32 s78, s16, 9
	v_lshl_add_u64 v[4:5], v[4:5], 0, s[78:79]
	v_lshlrev_b32_e32 v64, 2, v3
	v_lshl_add_u64 v[4:5], v[4:5], 0, v[64:65]
	v_ashrrev_i32_e32 v7, 31, v6
	global_store_dwordx2 v[4:5], v[14:15], off nt
	v_lshlrev_b64 v[4:5], 15, v[6:7]
	v_lshl_add_u64 v[4:5], s[48:49], 0, v[4:5]
	s_xor_b32 s78, s78, 0x7e00
	v_lshl_add_u64 v[4:5], v[4:5], 0, s[78:79]
	v_mov_b32_e32 v2, s10
	v_lshl_add_u64 v[4:5], v[4:5], 0, v[64:65]
	global_store_dwordx2 v[4:5], v[18:19], off nt

.LBB0_522:
	v_lshl_add_u64 v[0:1], s[18:19], 0, v[74:75]
	global_load_dwordx4 v[0:3], v[0:1], off
	v_lshl_add_u64 v[4:5], s[18:19], 0, v[76:77]
	global_load_dwordx4 v[4:7], v[4:5], off
	v_add_u32_e32 v19, s9, v95
	ds_read_b32 v8, v19
	ds_read_b32 v10, v19 offset:1024
	v_add_u32_e32 v32, s8, v93
	v_add_u32_e32 v33, s33, v93
	v_add_u32_e32 v34, s8, v94
	v_add_u32_e32 v35, s33, v94
	s_waitcnt vmcnt(1)
	v_lshlrev_b32_e32 v12, 16, v0
	v_and_b32_e32 v13, 0xffff0000, v0
	v_lshlrev_b32_e32 v0, 16, v1
	v_and_b32_e32 v1, 0xffff0000, v1
	v_lshlrev_b32_e32 v14, 16, v2
	v_and_b32_e32 v15, 0xffff0000, v2
	v_lshlrev_b32_e32 v2, 16, v3
	v_and_b32_e32 v3, 0xffff0000, v3
	s_waitcnt lgkmcnt(1)
	v_pk_mul_f32 v[20:21], v[8:9], v[12:13] op_sel_hi:[0,1]
	v_pk_mul_f32 v[22:23], v[8:9], v[0:1] op_sel_hi:[0,1]
	v_pk_mul_f32 v[26:27], v[8:9], v[14:15] op_sel_hi:[0,1]
	v_pk_mul_f32 v[28:29], v[8:9], v[2:3] op_sel_hi:[0,1]
	s_waitcnt lgkmcnt(0)
	v_pk_mul_f32 v[12:13], v[10:11], v[12:13] op_sel_hi:[0,1]
	v_pk_mul_f32 v[24:25], v[10:11], v[0:1] op_sel_hi:[0,1]
	v_pk_mul_f32 v[14:15], v[10:11], v[14:15] op_sel_hi:[0,1]
	v_pk_mul_f32 v[30:31], v[10:11], v[2:3] op_sel_hi:[0,1]
	v_cvt_pk_bf16_f32 v0, v20, v21
	v_cvt_pk_bf16_f32 v1, v22, v23
	v_cvt_pk_bf16_f32 v2, v26, v27
	v_cvt_pk_bf16_f32 v3, v28, v29
	v_cvt_pk_bf16_f32 v8, v12, v13
	v_cvt_pk_bf16_f32 v9, v24, v25
	v_cvt_pk_bf16_f32 v10, v14, v15
	v_cvt_pk_bf16_f32 v11, v30, v31
	ds_write_b128 v32, v[0:3]
	ds_write_b128 v33, v[8:11]
	ds_read_b32 v0, v19 offset:128
	ds_read_b32 v2, v19 offset:1152
	s_waitcnt vmcnt(0)
	v_lshlrev_b32_e32 v16, 16, v4
	v_and_b32_e32 v17, 0xffff0000, v4
	v_lshlrev_b32_e32 v4, 16, v5
	v_and_b32_e32 v5, 0xffff0000, v5
	v_lshlrev_b32_e32 v18, 16, v6
	v_and_b32_e32 v19, 0xffff0000, v6
	v_lshlrev_b32_e32 v6, 16, v7
	v_and_b32_e32 v7, 0xffff0000, v7
	s_waitcnt lgkmcnt(1)
	v_pk_mul_f32 v[8:9], v[0:1], v[16:17] op_sel_hi:[0,1]
	s_waitcnt lgkmcnt(0)
	v_pk_mul_f32 v[10:11], v[2:3], v[16:17] op_sel_hi:[0,1]
	v_pk_mul_f32 v[12:13], v[0:1], v[4:5] op_sel_hi:[0,1]
	v_pk_mul_f32 v[16:17], v[0:1], v[18:19] op_sel_hi:[0,1]
	v_pk_mul_f32 v[20:21], v[0:1], v[6:7] op_sel_hi:[0,1]
	v_pk_mul_f32 v[14:15], v[2:3], v[4:5] op_sel_hi:[0,1]
	v_pk_mul_f32 v[18:19], v[2:3], v[18:19] op_sel_hi:[0,1]
	v_pk_mul_f32 v[22:23], v[2:3], v[6:7] op_sel_hi:[0,1]
	v_cvt_pk_bf16_f32 v0, v8, v9
	v_cvt_pk_bf16_f32 v1, v12, v13
	v_cvt_pk_bf16_f32 v2, v16, v17
	v_cvt_pk_bf16_f32 v3, v20, v21
	v_cvt_pk_bf16_f32 v4, v10, v11
	v_cvt_pk_bf16_f32 v5, v14, v15
	v_cvt_pk_bf16_f32 v6, v18, v19
	v_cvt_pk_bf16_f32 v7, v22, v23
	ds_write_b128 v34, v[0:3]
	ds_write_b128 v35, v[4:7]
	s_waitcnt lgkmcnt(0)
	s_barrier
	ds_read_b64_tr_b16 v[48:49], v64 offset:0
	ds_read_b64_tr_b16 v[50:51], v64 offset:0x800
	ds_read_b64_tr_b16 v[0:1], v96 offset:0
	ds_read_b64_tr_b16 v[2:3], v96 offset:0x800
	ds_read_b64_tr_b16 v[16:17], v96 offset:0x200
	ds_read_b64_tr_b16 v[18:19], v96 offset:0xa00
	ds_read_b64_tr_b16 v[32:33], v96 offset:0x400
	ds_read_b64_tr_b16 v[34:35], v96 offset:0xc00
	ds_read_b64_tr_b16 v[52:53], v96 offset:0x600
	ds_read_b64_tr_b16 v[54:55], v96 offset:0xe00
	s_waitcnt lgkmcnt(0)
	ds_read_b64_tr_b16 v[80:81], v64 offset:0x1000
	ds_read_b64_tr_b16 v[82:83], v64 offset:0x1800
	ds_read_b64_tr_b16 v[98:99], v96 offset:0x1000
	ds_read_b64_tr_b16 v[100:101], v96 offset:0x1800
	ds_read_b64_tr_b16 v[102:103], v96 offset:0x1200
	ds_read_b64_tr_b16 v[104:105], v96 offset:0x1a00
	ds_read_b64_tr_b16 v[106:107], v96 offset:0x1400
	ds_read_b64_tr_b16 v[108:109], v96 offset:0x1c00
	ds_read_b64_tr_b16 v[110:111], v96 offset:0x1600
	ds_read_b64_tr_b16 v[112:113], v96 offset:0x1e00
	s_waitcnt lgkmcnt(0)
	s_nop 0
	v_mfma_f32_32x32x16_bf16 v[0:15], v[48:51], v[0:3], 0
	v_mfma_f32_32x32x16_bf16 v[16:31], v[48:51], v[16:19], 0
	v_mfma_f32_32x32x16_bf16 v[32:47], v[48:51], v[32:35], 0
	v_mfma_f32_32x32x16_bf16 v[48:63], v[48:51], v[52:55], 0
	v_mfma_f32_32x32x16_bf16 v[0:15], v[80:83], v[98:101], v[0:15]
	ds_read_b64_tr_b16 v[98:99], v64 offset:0x2000
	ds_read_b64_tr_b16 v[100:101], v64 offset:0x2800
	v_mfma_f32_32x32x16_bf16 v[16:31], v[80:83], v[102:105], v[16:31]
	ds_read_b64_tr_b16 v[102:103], v96 offset:0x2000
	ds_read_b64_tr_b16 v[104:105], v96 offset:0x2800
	v_mfma_f32_32x32x16_bf16 v[32:47], v[80:83], v[106:109], v[32:47]
	ds_read_b64_tr_b16 v[106:107], v96 offset:0x2200
	ds_read_b64_tr_b16 v[108:109], v96 offset:0x2a00
	ds_read_b64_tr_b16 v[114:115], v96 offset:0x2400
	ds_read_b64_tr_b16 v[116:117], v96 offset:0x2c00
	ds_read_b64_tr_b16 v[118:119], v96 offset:0x2600
	ds_read_b64_tr_b16 v[120:121], v96 offset:0x2e00
	s_waitcnt lgkmcnt(0)
	v_mfma_f32_32x32x16_bf16 v[48:63], v[80:83], v[110:113], v[48:63]
	ds_read_b64_tr_b16 v[80:81], v64 offset:0x3000
	ds_read_b64_tr_b16 v[82:83], v64 offset:0x3800
	v_mfma_f32_32x32x16_bf16 v[0:15], v[98:101], v[102:105], v[0:15]
	ds_read_b64_tr_b16 v[102:103], v96 offset:0x3000
	ds_read_b64_tr_b16 v[104:105], v96 offset:0x3800
	v_mfma_f32_32x32x16_bf16 v[16:31], v[98:101], v[106:109], v[16:31]
	ds_read_b64_tr_b16 v[106:107], v96 offset:0x3200
	ds_read_b64_tr_b16 v[108:109], v96 offset:0x3a00
	ds_read_b64_tr_b16 v[110:111], v96 offset:0x3400
	ds_read_b64_tr_b16 v[112:113], v96 offset:0x3c00
	v_mfma_f32_32x32x16_bf16 v[32:47], v[98:101], v[114:117], v[32:47]
	ds_read_b64_tr_b16 v[114:115], v96 offset:0x3600
	ds_read_b64_tr_b16 v[116:117], v96 offset:0x3e00
	s_waitcnt lgkmcnt(0)
	v_mfma_f32_32x32x16_bf16 v[48:63], v[98:101], v[118:121], v[48:63]
	v_mfma_f32_32x32x16_bf16 v[0:15], v[80:83], v[102:105], v[0:15]
	s_mov_b32 s6, 0x53360000
	s_addk_i32 s9, 0x100
	v_lshl_add_u64 v[74:75], v[74:75], 0, s[86:87]
	v_lshl_add_u64 v[76:77], v[76:77], 0, s[86:87]
	v_add_u32_e32 v96, 0x4000, v96
	s_cmpk_eq_i32 s9, 0x400
	v_mfma_f32_32x32x16_bf16 v[16:31], v[80:83], v[106:109], v[16:31]
	v_mfma_f32_32x32x16_bf16 v[32:47], v[80:83], v[110:113], v[32:47]
	s_nop 10
	v_cvt_pk_bf16_f32 v0, v0, v16
	v_mfma_f32_32x32x16_bf16 v[48:63], v[80:83], v[114:117], v[48:63]
	v_lshl_add_u64 v[80:81], s[18:19], 0, v[78:79]
	v_add_co_u32_e64 v82, s[6:7], s6, v80
	s_nop 1
	v_addc_co_u32_e64 v83, s[6:7], 0, v81, s[6:7]
	s_mov_b32 s6, 0x53361000
	s_nop 5
	v_cvt_pk_bf16_f32 v16, v32, v48
	v_mov_b32_e32 v48, 0
	v_mov_b32_e32 v32, 0
	s_nop 0
	v_mov_b32_dpp v48, v16 quad_perm:[1,0,3,2] row_mask:0xf bank_mask:0xf
	v_mov_b32_dpp v32, v0 quad_perm:[1,0,3,2] row_mask:0xf bank_mask:0xf
	v_cndmask_b32_e32 v0, v48, v0, vcc
	v_cndmask_b32_e32 v16, v16, v32, vcc
	v_and_b32_e32 v32, 0xffff, v0
	v_lshrrev_b32_e32 v0, 16, v0
	v_and_or_b32 v0, v16, s17, v0
	v_lshl_or_b32 v32, v16, 16, v32
	global_store_dword v[82:83], v0, off offset:576 nt
	v_cvt_pk_bf16_f32 v0, v1, v17
	v_mov_b32_e32 v16, 0
	v_cvt_pk_bf16_f32 v1, v33, v49
	v_mov_b32_e32 v17, 0
	v_mov_b32_dpp v16, v0 quad_perm:[1,0,3,2] row_mask:0xf bank_mask:0xf
	global_store_dword v[82:83], v32, off offset:512 nt
	v_mov_b32_dpp v17, v1 quad_perm:[1,0,3,2] row_mask:0xf bank_mask:0xf
	v_cndmask_b32_e32 v1, v1, v16, vcc
	v_cndmask_b32_e32 v0, v17, v0, vcc
	v_lshlrev_b32_e32 v16, 16, v1
	v_and_or_b32 v16, v0, s81, v16
	v_lshrrev_b32_e32 v0, 16, v0
	v_and_or_b32 v0, v1, s17, v0
	global_store_dword v[82:83], v0, off offset:832 nt
	v_cvt_pk_bf16_f32 v0, v2, v18
	v_mov_b32_e32 v2, 0
	global_store_dword v[82:83], v16, off offset:768 nt
	v_cvt_pk_bf16_f32 v1, v34, v50
	v_mov_b32_dpp v2, v0 quad_perm:[1,0,3,2] row_mask:0xf bank_mask:0xf
	v_mov_b32_e32 v16, 0
	s_nop 1
	v_mov_b32_dpp v16, v1 quad_perm:[1,0,3,2] row_mask:0xf bank_mask:0xf
	v_cndmask_b32_e32 v1, v1, v2, vcc
	v_cndmask_b32_e32 v0, v16, v0, vcc
	v_lshlrev_b32_e32 v2, 16, v1
	v_and_or_b32 v2, v0, s81, v2
	v_lshrrev_b32_e32 v0, 16, v0
	v_and_or_b32 v0, v1, s17, v0
	global_store_dword v[82:83], v2, off offset:1024 nt
	global_store_dword v[82:83], v0, off offset:1088 nt
	v_cvt_pk_bf16_f32 v0, v3, v19
	v_mov_b32_e32 v2, 0
	v_cvt_pk_bf16_f32 v1, v35, v51
	v_mov_b32_e32 v3, 0
	v_mov_b32_dpp v2, v0 quad_perm:[1,0,3,2] row_mask:0xf bank_mask:0xf
	s_nop 0
	v_mov_b32_dpp v3, v1 quad_perm:[1,0,3,2] row_mask:0xf bank_mask:0xf
	v_cndmask_b32_e32 v1, v1, v2, vcc
	v_cndmask_b32_e32 v0, v3, v0, vcc
	v_lshlrev_b32_e32 v2, 16, v1
	v_and_or_b32 v2, v0, s81, v2
	v_lshrrev_b32_e32 v0, 16, v0
	v_and_or_b32 v0, v1, s17, v0
	global_store_dword v[82:83], v2, off offset:1280 nt
	global_store_dword v[82:83], v0, off offset:1344 nt
	v_cvt_pk_bf16_f32 v0, v4, v20
	v_mov_b32_e32 v2, 0
	v_cvt_pk_bf16_f32 v1, v36, v52
	v_mov_b32_e32 v3, 0
	v_mov_b32_dpp v2, v0 quad_perm:[1,0,3,2] row_mask:0xf bank_mask:0xf
	s_nop 0
	v_mov_b32_dpp v3, v1 quad_perm:[1,0,3,2] row_mask:0xf bank_mask:0xf
	v_cndmask_b32_e32 v1, v1, v2, vcc
	v_cndmask_b32_e32 v0, v3, v0, vcc
	v_lshlrev_b32_e32 v2, 16, v1
	v_and_or_b32 v2, v0, s81, v2
	v_lshrrev_b32_e32 v0, 16, v0
	v_and_or_b32 v0, v1, s17, v0
	global_store_dword v[82:83], v2, off offset:2560 nt
	global_store_dword v[82:83], v0, off offset:2624 nt
	v_cvt_pk_bf16_f32 v0, v5, v21
	v_mov_b32_e32 v2, 0
	v_cvt_pk_bf16_f32 v1, v37, v53
	v_mov_b32_e32 v3, 0
	v_mov_b32_dpp v2, v0 quad_perm:[1,0,3,2] row_mask:0xf bank_mask:0xf
	v_mov_b32_e32 v5, 0
	v_mov_b32_dpp v3, v1 quad_perm:[1,0,3,2] row_mask:0xf bank_mask:0xf
	v_cndmask_b32_e32 v1, v1, v2, vcc
	v_cndmask_b32_e32 v0, v3, v0, vcc
	v_lshlrev_b32_e32 v2, 16, v1
	v_and_or_b32 v2, v0, s81, v2
	v_lshrrev_b32_e32 v0, 16, v0
	v_and_or_b32 v0, v1, s17, v0
	global_store_dword v[82:83], v2, off offset:2816 nt
	global_store_dword v[82:83], v0, off offset:2880 nt
	v_cvt_pk_bf16_f32 v0, v6, v22
	v_mov_b32_e32 v2, 0
	v_cvt_pk_bf16_f32 v1, v38, v54
	v_mov_b32_e32 v3, 0
	v_mov_b32_dpp v2, v0 quad_perm:[1,0,3,2] row_mask:0xf bank_mask:0xf
	s_nop 0
	v_mov_b32_dpp v3, v1 quad_perm:[1,0,3,2] row_mask:0xf bank_mask:0xf
	v_cndmask_b32_e32 v1, v1, v2, vcc
	v_cndmask_b32_e32 v0, v3, v0, vcc
	v_lshlrev_b32_e32 v2, 16, v1
	v_and_or_b32 v2, v0, s81, v2
	v_lshrrev_b32_e32 v0, 16, v0
	v_and_or_b32 v0, v1, s17, v0
	global_store_dword v[82:83], v2, off offset:3072 nt
	global_store_dword v[82:83], v0, off offset:3136 nt
	v_cvt_pk_bf16_f32 v0, v7, v23
	v_mov_b32_e32 v2, 0
	v_cvt_pk_bf16_f32 v1, v39, v55
	v_mov_b32_e32 v3, 0
	v_mov_b32_dpp v2, v0 quad_perm:[1,0,3,2] row_mask:0xf bank_mask:0xf
	s_nop 0
	v_mov_b32_dpp v3, v1 quad_perm:[1,0,3,2] row_mask:0xf bank_mask:0xf
	v_cndmask_b32_e32 v1, v1, v2, vcc
	v_cndmask_b32_e32 v0, v3, v0, vcc
	v_lshlrev_b32_e32 v2, 16, v1
	v_and_or_b32 v2, v0, s81, v2
	v_lshrrev_b32_e32 v0, 16, v0
	v_and_or_b32 v0, v1, s17, v0
	global_store_dword v[82:83], v2, off offset:3328 nt
	global_store_dword v[82:83], v0, off offset:3392 nt
	v_cvt_pk_bf16_f32 v0, v8, v24
	v_mov_b32_e32 v2, 0
	v_cvt_pk_bf16_f32 v1, v40, v56
	v_mov_b32_e32 v3, 0
	v_mov_b32_dpp v2, v0 quad_perm:[1,0,3,2] row_mask:0xf bank_mask:0xf
	v_cndmask_b32_e32 v2, v1, v2, vcc
	v_mov_b32_dpp v3, v1 quad_perm:[1,0,3,2] row_mask:0xf bank_mask:0xf
	v_cndmask_b32_e32 v3, v3, v0, vcc
	v_lshlrev_b32_e32 v0, 16, v2
	v_and_or_b32 v4, v3, s81, v0
	v_add_co_u32_e64 v0, s[6:7], s6, v80
	v_lshrrev_b32_e32 v3, 16, v3
	s_nop 0
	v_addc_co_u32_e64 v1, s[6:7], 0, v81, s[6:7]
	v_and_or_b32 v2, v2, s17, v3
	global_store_dword v[0:1], v4, off offset:512 nt
	global_store_dword v[0:1], v2, off offset:576 nt
	v_cvt_pk_bf16_f32 v2, v9, v25
	v_mov_b32_e32 v4, 0
	v_cvt_pk_bf16_f32 v3, v41, v57
	s_mov_b64 s[6:7], 0x400000
	v_mov_b32_dpp v4, v2 quad_perm:[1,0,3,2] row_mask:0xf bank_mask:0xf
	v_mov_b32_dpp v5, v3 quad_perm:[1,0,3,2] row_mask:0xf bank_mask:0xf
	v_cndmask_b32_e32 v3, v3, v4, vcc
	v_cndmask_b32_e32 v2, v5, v2, vcc
	v_lshlrev_b32_e32 v4, 16, v3
	v_and_or_b32 v4, v2, s81, v4
	v_lshrrev_b32_e32 v2, 16, v2
	v_and_or_b32 v2, v3, s17, v2
	global_store_dword v[0:1], v4, off offset:768 nt
	global_store_dword v[0:1], v2, off offset:832 nt
	v_cvt_pk_bf16_f32 v2, v10, v26
	v_mov_b32_e32 v4, 0
	v_cvt_pk_bf16_f32 v3, v42, v58
	v_mov_b32_e32 v5, 0
	v_mov_b32_dpp v4, v2 quad_perm:[1,0,3,2] row_mask:0xf bank_mask:0xf
	v_lshl_add_u64 v[78:79], v[78:79], 0, s[6:7]
	v_mov_b32_dpp v5, v3 quad_perm:[1,0,3,2] row_mask:0xf bank_mask:0xf
	v_cndmask_b32_e32 v3, v3, v4, vcc
	v_cndmask_b32_e32 v2, v5, v2, vcc
	v_lshlrev_b32_e32 v4, 16, v3
	v_and_or_b32 v4, v2, s81, v4
	v_lshrrev_b32_e32 v2, 16, v2
	v_and_or_b32 v2, v3, s17, v2
	global_store_dword v[0:1], v4, off offset:1024 nt
	global_store_dword v[0:1], v2, off offset:1088 nt
	v_cvt_pk_bf16_f32 v2, v11, v27
	v_mov_b32_e32 v4, 0
	v_cvt_pk_bf16_f32 v3, v43, v59
	v_mov_b32_e32 v5, 0
	v_mov_b32_dpp v4, v2 quad_perm:[1,0,3,2] row_mask:0xf bank_mask:0xf
	s_nop 0
	v_mov_b32_dpp v5, v3 quad_perm:[1,0,3,2] row_mask:0xf bank_mask:0xf
	v_cndmask_b32_e32 v3, v3, v4, vcc
	v_cndmask_b32_e32 v2, v5, v2, vcc
	v_lshlrev_b32_e32 v4, 16, v3
	v_and_or_b32 v4, v2, s81, v4
	v_lshrrev_b32_e32 v2, 16, v2
	v_and_or_b32 v2, v3, s17, v2
	global_store_dword v[0:1], v4, off offset:1280 nt
	global_store_dword v[0:1], v2, off offset:1344 nt
	v_cvt_pk_bf16_f32 v2, v12, v28
	v_mov_b32_e32 v4, 0
	v_cvt_pk_bf16_f32 v3, v44, v60
	v_mov_b32_e32 v5, 0
	v_mov_b32_dpp v4, v2 quad_perm:[1,0,3,2] row_mask:0xf bank_mask:0xf
	s_nop 0
	v_mov_b32_dpp v5, v3 quad_perm:[1,0,3,2] row_mask:0xf bank_mask:0xf
	v_cndmask_b32_e32 v3, v3, v4, vcc
	v_cndmask_b32_e32 v2, v5, v2, vcc
	v_lshlrev_b32_e32 v4, 16, v3
	v_and_or_b32 v4, v2, s81, v4
	v_lshrrev_b32_e32 v2, 16, v2
	v_and_or_b32 v2, v3, s17, v2
	global_store_dword v[0:1], v4, off offset:2560 nt
	global_store_dword v[0:1], v2, off offset:2624 nt
	v_cvt_pk_bf16_f32 v2, v13, v29
	v_mov_b32_e32 v4, 0
	v_cvt_pk_bf16_f32 v3, v45, v61
	v_mov_b32_e32 v5, 0
	v_mov_b32_dpp v4, v2 quad_perm:[1,0,3,2] row_mask:0xf bank_mask:0xf
	s_nop 0
	v_mov_b32_dpp v5, v3 quad_perm:[1,0,3,2] row_mask:0xf bank_mask:0xf
	v_cndmask_b32_e32 v3, v3, v4, vcc
	v_cndmask_b32_e32 v2, v5, v2, vcc
	v_lshlrev_b32_e32 v4, 16, v3
	v_and_or_b32 v4, v2, s81, v4
	v_lshrrev_b32_e32 v2, 16, v2
	v_and_or_b32 v2, v3, s17, v2
	global_store_dword v[0:1], v4, off offset:2816 nt
	global_store_dword v[0:1], v2, off offset:2880 nt
	v_cvt_pk_bf16_f32 v2, v14, v30
	v_mov_b32_e32 v4, 0
	v_cvt_pk_bf16_f32 v3, v46, v62
	v_mov_b32_e32 v5, 0
	v_mov_b32_dpp v4, v2 quad_perm:[1,0,3,2] row_mask:0xf bank_mask:0xf
	s_nop 0
	v_mov_b32_dpp v5, v3 quad_perm:[1,0,3,2] row_mask:0xf bank_mask:0xf
	v_cndmask_b32_e32 v3, v3, v4, vcc
	v_cndmask_b32_e32 v2, v5, v2, vcc
	v_lshlrev_b32_e32 v4, 16, v3
	v_and_or_b32 v4, v2, s81, v4
	v_lshrrev_b32_e32 v2, 16, v2
	v_and_or_b32 v2, v3, s17, v2
	global_store_dword v[0:1], v4, off offset:3072 nt
	global_store_dword v[0:1], v2, off offset:3136 nt
	v_cvt_pk_bf16_f32 v2, v15, v31
	v_mov_b32_e32 v4, 0
	v_cvt_pk_bf16_f32 v3, v47, v63
	v_mov_b32_e32 v5, 0
	v_mov_b32_dpp v4, v2 quad_perm:[1,0,3,2] row_mask:0xf bank_mask:0xf
	s_nop 0
	v_mov_b32_dpp v5, v3 quad_perm:[1,0,3,2] row_mask:0xf bank_mask:0xf
	v_cndmask_b32_e32 v3, v3, v4, vcc
	v_cndmask_b32_e32 v2, v5, v2, vcc
	v_lshlrev_b32_e32 v4, 16, v3
	v_and_or_b32 v4, v2, s81, v4
	v_lshrrev_b32_e32 v2, 16, v2
	v_and_or_b32 v2, v3, s17, v2
	global_store_dword v[0:1], v4, off offset:3328 nt
	global_store_dword v[0:1], v2, off offset:3392 nt
	s_barrier
	s_cbranch_scc0 .LBB0_522
	v_ashrrev_i32_e32 v24, 6, v70
	s_lshl_b64 s[94:95], s[30:31], 6
	v_readfirstlane_b32 s8, v24
	s_cmp_gt_i32 s8, 5
	s_cselect_b64 s[96:97], -1, 0
	s_cmp_lt_i32 s8, 6
	s_cselect_b32 s7, s21, s23
	s_cselect_b32 s6, s20, s22
	v_lshlrev_b32_e32 v4, 5, v66
	global_load_dwordx4 v[0:3], v4, s[6:7]
	s_nop 0
	global_load_dwordx4 v[4:7], v4, s[6:7] offset:16
	v_and_b32_e32 v8, 4, v70
	v_cmp_eq_u32_e64 s[6:7], 0, v8
	v_xor_b32_e32 v8, 1, v84
	v_add_u32_e32 v9, 64, v71
	v_cmp_lt_i32_e32 vcc, v8, v9
	s_lshl_b32 s10, s8, 7
	s_mov_b32 s78, s10
	v_cndmask_b32_e32 v8, v84, v8, vcc
	v_lshlrev_b32_e32 v25, 2, v8
	v_xor_b32_e32 v8, 2, v84
	v_cmp_lt_i32_e32 vcc, v8, v9
	s_ashr_i32 s11, s10, 31
	s_lshl_b64 s[28:29], s[78:79], 1
	v_cndmask_b32_e32 v8, v84, v8, vcc
	v_lshlrev_b32_e32 v74, 2, v8
	v_xor_b32_e32 v8, 4, v84
	v_cmp_lt_i32_e32 vcc, v8, v9
	v_bfe_u32 v28, v70, 4, 2
	v_mov_b32_e32 v29, v65
	v_cndmask_b32_e32 v8, v84, v8, vcc
	v_lshlrev_b32_e32 v75, 2, v8
	v_xor_b32_e32 v8, 8, v84
	v_cmp_lt_i32_e32 vcc, v8, v9
	s_add_u32 s28, s18, s28
	v_mov_b64_e32 v[10:11], s[70:71]
	v_cndmask_b32_e32 v8, v84, v8, vcc
	v_lshlrev_b32_e32 v76, 2, v8
	v_lshl_add_u64 v[8:9], s[72:73], 0, v[28:29]
	s_addc_u32 s29, s19, s29
	s_lshl_b64 s[50:51], s[10:11], 1
	v_mad_u64_u32 v[34:35], s[10:11], v8, s1, v[10:11]
	v_mov_b32_e32 v12, v35
	v_mad_u64_u32 v[12:13], s[10:11], v9, s1, v[12:13]
	v_lshlrev_b64 v[8:9], 13, v[8:9]
	v_or_b32_e32 v8, v8, v72
	v_lshl_add_u64 v[36:37], s[40:41], 0, v[8:9]
	v_lshl_add_u64 v[8:9], s[74:75], 0, v[28:29]
	v_mad_u64_u32 v[38:39], s[10:11], v8, s1, v[10:11]
	v_mov_b32_e32 v35, v12
	v_mov_b32_e32 v12, v39
	v_mad_u64_u32 v[12:13], s[10:11], v9, s1, v[12:13]
	v_lshlrev_b64 v[8:9], 13, v[8:9]
	v_or_b32_e32 v8, v8, v72
	v_lshl_add_u64 v[40:41], s[40:41], 0, v[8:9]
	v_lshl_add_u64 v[8:9], s[76:77], 0, v[28:29]
	v_mad_u64_u32 v[42:43], s[10:11], v8, s1, v[10:11]
	v_mov_b32_e32 v39, v12
	v_mov_b32_e32 v12, v43
	v_mad_u64_u32 v[12:13], s[10:11], v9, s1, v[12:13]
	v_lshlrev_b64 v[8:9], 13, v[8:9]
	v_or_b32_e32 v8, v8, v72
	v_lshl_add_u64 v[44:45], s[40:41], 0, v[8:9]
	v_lshl_add_u64 v[8:9], s[64:65], 0, v[28:29]
	v_mad_u64_u32 v[46:47], s[10:11], v8, s1, v[10:11]
	v_mov_b32_e32 v10, v47
	v_mad_u64_u32 v[10:11], s[10:11], v9, s1, v[10:11]
	v_lshlrev_b64 v[8:9], 13, v[8:9]
	v_lshrrev_b32_e32 v27, 4, v68
	v_and_b32_e32 v64, 0x60, v73
	v_or_b32_e32 v8, v8, v72
	v_lshlrev_b32_e32 v26, 3, v66
	s_mov_b32 s31, 0
	v_cmp_gt_u32_e64 s[8:9], 8, v66
	v_lshl_add_u64 v[30:31], s[38:39], 0, v[64:65]
	v_lshl_add_u64 v[32:33], s[42:43], 0, v[64:65]
	v_or_b32_e32 v77, 4, v27
	v_or_b32_e32 v78, 8, v27
	v_or_b32_e32 v79, 12, v27
	v_mov_b32_e32 v43, v12
	v_mov_b32_e32 v47, v10
	v_lshl_add_u64 v[48:49], s[40:41], 0, v[8:9]
	s_mov_b32 s78, 0
	s_branch .LBB0_525
.LBB0_524:
	s_waitcnt vmcnt(0) lgkmcnt(6)
	v_pk_mul_f32 v[20:21], v[20:21], v[72:73]
	s_waitcnt lgkmcnt(2)
	v_pk_mul_f32 v[12:13], v[12:13], v[60:61]
	v_cndmask_b32_e64 v21, v21, -v21, s[6:7]
	v_cndmask_b32_e64 v20, v20, -v20, s[6:7]
	v_cndmask_b32_e64 v13, v13, -v13, s[6:7]
	v_cndmask_b32_e64 v12, v12, -v12, s[6:7]
	v_pk_fma_f32 v[16:17], v[16:17], v[70:71], v[20:21]
	v_pk_mul_f32 v[20:21], v[22:23], v[62:63]
	v_pk_fma_f32 v[12:13], v[8:9], v[54:55], v[12:13]
	s_waitcnt lgkmcnt(0)
	v_pk_mul_f32 v[8:9], v[14:15], v[56:57]
	v_cndmask_b32_e64 v21, v21, -v21, s[6:7]
	v_cndmask_b32_e64 v20, v20, -v20, s[6:7]
	v_cndmask_b32_e64 v9, v9, -v9, s[6:7]
	v_cndmask_b32_e64 v8, v8, -v8, s[6:7]
	v_pk_fma_f32 v[18:19], v[18:19], v[58:59], v[20:21]
	v_pk_fma_f32 v[14:15], v[10:11], v[50:51], v[8:9]
	s_add_i32 s78, s78, 4
	s_add_i32 s31, s31, 16
	v_cvt_pk_bf16_f32 v8, v16, v17
	v_cvt_pk_bf16_f32 v9, v18, v19
	v_cvt_pk_bf16_f32 v10, v12, v13
	v_cvt_pk_bf16_f32 v11, v14, v15
	v_lshl_add_u64 v[12:13], v[52:53], 0, v[64:65]
	v_lshl_add_u64 v[34:35], v[34:35], 0, s[90:91]
	v_lshl_add_u64 v[36:37], v[36:37], 0, s[82:83]
	v_lshl_add_u64 v[38:39], v[38:39], 0, s[90:91]
	v_lshl_add_u64 v[40:41], v[40:41], 0, s[82:83]
	v_lshl_add_u64 v[42:43], v[42:43], 0, s[90:91]
	v_lshl_add_u64 v[44:45], v[44:45], 0, s[82:83]
	v_lshl_add_u64 v[46:47], v[46:47], 0, s[90:91]
	s_cmp_eq_u32 s31, 64
	v_lshl_add_u64 v[48:49], v[48:49], 0, s[82:83]
	global_store_dwordx4 v[12:13], v[8:11], off nt
	s_cbranch_scc1 .LBB0_541

.LBB0_529:
	s_waitcnt vmcnt(0) lgkmcnt(6)
	v_pk_mul_f32 v[20:21], v[20:21], v[72:73]
	s_waitcnt lgkmcnt(2)
	v_pk_mul_f32 v[12:13], v[12:13], v[60:61]
	v_cndmask_b32_e64 v21, v21, -v21, s[6:7]
	v_cndmask_b32_e64 v20, v20, -v20, s[6:7]
	v_cndmask_b32_e64 v13, v13, -v13, s[6:7]
	v_cndmask_b32_e64 v12, v12, -v12, s[6:7]
	v_pk_fma_f32 v[16:17], v[16:17], v[70:71], v[20:21]
	v_pk_mul_f32 v[20:21], v[22:23], v[62:63]
	v_pk_fma_f32 v[12:13], v[8:9], v[54:55], v[12:13]
	s_waitcnt lgkmcnt(0)
	v_pk_mul_f32 v[8:9], v[14:15], v[56:57]
	v_cndmask_b32_e64 v21, v21, -v21, s[6:7]
	v_cndmask_b32_e64 v20, v20, -v20, s[6:7]
	v_cndmask_b32_e64 v9, v9, -v9, s[6:7]
	v_cndmask_b32_e64 v8, v8, -v8, s[6:7]
	v_pk_fma_f32 v[18:19], v[18:19], v[58:59], v[20:21]
	v_pk_fma_f32 v[14:15], v[10:11], v[50:51], v[8:9]
	v_lshlrev_b32_e32 v64, 1, v26
	v_cvt_pk_bf16_f32 v8, v16, v17
	v_cvt_pk_bf16_f32 v9, v18, v19
	v_cvt_pk_bf16_f32 v10, v12, v13
	v_cvt_pk_bf16_f32 v11, v14, v15
	v_lshl_add_u64 v[12:13], v[52:53], 0, v[64:65]
	global_store_dwordx4 v[12:13], v[8:11], off nt
	s_mov_b64 s[36:37], -1
	s_nop 0
	v_lshl_add_u64 v[8:9], v[44:45], 0, s[50:51]
	global_load_dwordx4 v[50:53], v[8:9], off
	v_add_u32_e32 v8, 4, v29
	v_mov_b32_e32 v10, s16
	v_cndmask_b32_e64 v8, v8, v10, s[8:9]
	v_mov_b32_e32 v9, v65
	v_lshlrev_b32_e32 v8, 5, v8
	v_lshlrev_b64 v[8:9], 2, v[8:9]
	v_lshl_add_u64 v[12:13], v[30:31], 0, v[8:9]
	v_lshl_add_u64 v[20:21], v[32:33], 0, v[8:9]
	global_load_dwordx4 v[8:11], v[12:13], off offset:16
	global_load_dwordx4 v[16:19], v[12:13], off
	s_nop 0
	global_load_dwordx4 v[12:15], v[20:21], off offset:16
	s_nop 0
	global_load_dwordx4 v[20:23], v[20:21], off
	s_waitcnt vmcnt(4)
	v_lshlrev_b32_e32 v58, 16, v50
	v_and_b32_e32 v59, 0xffff0000, v50
	v_lshlrev_b32_e32 v54, 16, v53
	v_and_b32_e32 v55, 0xffff0000, v53
	v_lshlrev_b32_e32 v56, 16, v52
	v_and_b32_e32 v57, 0xffff0000, v52
	v_lshlrev_b32_e32 v52, 16, v51
	v_and_b32_e32 v53, 0xffff0000, v51
	v_pk_mul_f32 v[70:71], v[58:59], v[58:59]
	v_pk_mul_f32 v[62:63], v[52:53], v[52:53]
	v_add_f32_e32 v70, v70, v71
	v_add_f32_e32 v62, v62, v70
	v_pk_mul_f32 v[60:61], v[56:57], v[56:57]
	v_add_f32_e32 v62, v63, v62
	v_add_f32_e32 v60, v60, v62
	v_pk_mul_f32 v[50:51], v[54:55], v[54:55]
	v_add_f32_e32 v60, v61, v60
	v_add_f32_e32 v50, v50, v60
	v_add_f32_e32 v50, v51, v50
	ds_bpermute_b32 v51, v25, v50
	s_waitcnt lgkmcnt(0)
	v_add_f32_e32 v50, v50, v51
	ds_bpermute_b32 v51, v74, v50
	s_waitcnt lgkmcnt(0)
	v_add_f32_e32 v50, v50, v51
	ds_bpermute_b32 v51, v75, v50
	s_waitcnt lgkmcnt(0)
	v_add_f32_e32 v50, v50, v51
	ds_bpermute_b32 v51, v76, v50
	s_waitcnt lgkmcnt(0)
	v_add_f32_e32 v50, v50, v51
	v_fmamk_f32 v50, v50, 0x3c000000, v86
	v_mul_f32_e32 v51, 0x4b800000, v50
	v_cmp_gt_f32_e32 vcc, s0, v50
	s_nop 1
	v_cndmask_b32_e32 v50, v50, v51, vcc
	v_rsq_f32_e32 v50, v50
	s_nop 0
	v_mul_f32_e32 v51, 0x45800000, v50
	v_cndmask_b32_e32 v50, v50, v51, vcc
	v_pk_mul_f32 v[60:61], v[0:1], v[50:51] op_sel_hi:[1,0]
	v_pk_mul_f32 v[62:63], v[2:3], v[50:51] op_sel_hi:[1,0]
	v_pk_mul_f32 v[72:73], v[4:5], v[50:51] op_sel_hi:[1,0]
	v_pk_mul_f32 v[50:51], v[6:7], v[50:51] op_sel_hi:[1,0]
	v_pk_mul_f32 v[70:71], v[60:61], v[58:59]
	v_pk_mul_f32 v[58:59], v[62:63], v[52:53]
	v_pk_mul_f32 v[52:53], v[72:73], v[56:57]
	v_pk_mul_f32 v[50:51], v[50:51], v[54:55]
	ds_bpermute_b32 v72, v75, v70
	ds_bpermute_b32 v73, v75, v71
	ds_bpermute_b32 v62, v75, v58
	ds_bpermute_b32 v63, v75, v59
	ds_bpermute_b32 v60, v75, v52
	ds_bpermute_b32 v61, v75, v53
	ds_bpermute_b32 v56, v75, v50
	ds_bpermute_b32 v57, v75, v51
	v_cndmask_b32_e64 v54, 0, 1, s[96:97]
	v_cmp_ne_u32_e64 s[10:11], 1, v54
	s_andn2_b64 vcc, exec, s[96:97]
	s_cbranch_vccnz .LBB0_531
	v_or_b32_e32 v54, s84, v77
	v_or_b32_e32 v54, s94, v54
	v_mov_b32_e32 v55, s95
	v_lshlrev_b64 v[54:55], 9, v[54:55]
	v_lshl_add_u64 v[54:55], s[28:29], 0, v[54:55]
	v_lshl_add_u64 v[54:55], v[54:55], 0, s[88:89]
	s_mov_b64 s[36:37], 0

.LBB0_533:
	s_waitcnt vmcnt(0) lgkmcnt(6)
	v_pk_mul_f32 v[20:21], v[20:21], v[72:73]
	s_waitcnt lgkmcnt(2)
	v_pk_mul_f32 v[12:13], v[12:13], v[60:61]
	v_cndmask_b32_e64 v21, v21, -v21, s[6:7]
	v_cndmask_b32_e64 v20, v20, -v20, s[6:7]
	v_cndmask_b32_e64 v13, v13, -v13, s[6:7]
	v_cndmask_b32_e64 v12, v12, -v12, s[6:7]
	v_pk_fma_f32 v[16:17], v[16:17], v[70:71], v[20:21]
	v_pk_mul_f32 v[20:21], v[22:23], v[62:63]
	v_pk_fma_f32 v[12:13], v[8:9], v[52:53], v[12:13]
	s_waitcnt lgkmcnt(0)
	v_pk_mul_f32 v[8:9], v[14:15], v[56:57]
	v_cndmask_b32_e64 v21, v21, -v21, s[6:7]
	v_cndmask_b32_e64 v20, v20, -v20, s[6:7]
	v_cndmask_b32_e64 v9, v9, -v9, s[6:7]
	v_cndmask_b32_e64 v8, v8, -v8, s[6:7]
	v_pk_fma_f32 v[18:19], v[18:19], v[58:59], v[20:21]
	v_pk_fma_f32 v[14:15], v[10:11], v[50:51], v[8:9]
	v_cvt_pk_bf16_f32 v8, v16, v17
	v_cvt_pk_bf16_f32 v9, v18, v19
	v_cvt_pk_bf16_f32 v10, v12, v13
	v_cvt_pk_bf16_f32 v11, v14, v15
	v_lshl_add_u64 v[12:13], v[54:55], 0, v[64:65]
	global_store_dwordx4 v[12:13], v[8:11], off nt
	s_mov_b64 s[36:37], -1
	s_nop 0
	v_lshl_add_u64 v[8:9], v[40:41], 0, s[50:51]
	global_load_dwordx4 v[50:53], v[8:9], off
	v_add_u32_e32 v8, 8, v29
	v_mov_b32_e32 v10, s16
	v_cndmask_b32_e64 v8, v8, v10, s[8:9]
	v_mov_b32_e32 v9, v65
	v_lshlrev_b32_e32 v8, 5, v8
	v_lshlrev_b64 v[8:9], 2, v[8:9]
	v_lshl_add_u64 v[12:13], v[30:31], 0, v[8:9]
	v_lshl_add_u64 v[20:21], v[32:33], 0, v[8:9]
	global_load_dwordx4 v[8:11], v[12:13], off offset:16
	global_load_dwordx4 v[16:19], v[12:13], off
	s_nop 0
	global_load_dwordx4 v[12:15], v[20:21], off offset:16
	s_nop 0
	global_load_dwordx4 v[20:23], v[20:21], off
	s_waitcnt vmcnt(4)
	v_lshlrev_b32_e32 v58, 16, v50
	v_and_b32_e32 v59, 0xffff0000, v50
	v_lshlrev_b32_e32 v56, 16, v53
	v_and_b32_e32 v57, 0xffff0000, v53
	v_lshlrev_b32_e32 v54, 16, v52
	v_and_b32_e32 v55, 0xffff0000, v52
	v_lshlrev_b32_e32 v52, 16, v51
	v_and_b32_e32 v53, 0xffff0000, v51
	v_pk_mul_f32 v[70:71], v[58:59], v[58:59]
	v_pk_mul_f32 v[62:63], v[52:53], v[52:53]
	v_add_f32_e32 v70, v70, v71
	v_add_f32_e32 v62, v62, v70
	v_pk_mul_f32 v[60:61], v[54:55], v[54:55]
	v_add_f32_e32 v62, v63, v62
	v_add_f32_e32 v60, v60, v62
	v_pk_mul_f32 v[50:51], v[56:57], v[56:57]
	v_add_f32_e32 v60, v61, v60
	v_add_f32_e32 v50, v50, v60
	v_add_f32_e32 v50, v51, v50
	ds_bpermute_b32 v51, v25, v50
	s_waitcnt lgkmcnt(0)
	v_add_f32_e32 v50, v50, v51
	ds_bpermute_b32 v51, v74, v50
	s_waitcnt lgkmcnt(0)
	v_add_f32_e32 v50, v50, v51
	ds_bpermute_b32 v51, v75, v50
	s_waitcnt lgkmcnt(0)
	v_add_f32_e32 v50, v50, v51
	ds_bpermute_b32 v51, v76, v50
	s_waitcnt lgkmcnt(0)
	v_add_f32_e32 v50, v50, v51
	v_fmamk_f32 v50, v50, 0x3c000000, v86
	v_mul_f32_e32 v51, 0x4b800000, v50
	v_cmp_gt_f32_e32 vcc, s0, v50
	s_nop 1
	v_cndmask_b32_e32 v50, v50, v51, vcc
	v_rsq_f32_e32 v50, v50
	s_nop 0
	v_mul_f32_e32 v51, 0x45800000, v50
	v_cndmask_b32_e32 v50, v50, v51, vcc
	v_pk_mul_f32 v[60:61], v[0:1], v[50:51] op_sel_hi:[1,0]
	v_pk_mul_f32 v[62:63], v[2:3], v[50:51] op_sel_hi:[1,0]
	v_pk_mul_f32 v[72:73], v[4:5], v[50:51] op_sel_hi:[1,0]
	v_pk_mul_f32 v[50:51], v[6:7], v[50:51] op_sel_hi:[1,0]
	v_pk_mul_f32 v[70:71], v[60:61], v[58:59]
	v_pk_mul_f32 v[58:59], v[62:63], v[52:53]
	v_pk_mul_f32 v[54:55], v[72:73], v[54:55]
	v_pk_mul_f32 v[50:51], v[50:51], v[56:57]
	ds_bpermute_b32 v72, v75, v70
	ds_bpermute_b32 v73, v75, v71
	ds_bpermute_b32 v62, v75, v58
	ds_bpermute_b32 v63, v75, v59
	ds_bpermute_b32 v60, v75, v54
	ds_bpermute_b32 v61, v75, v55
	ds_bpermute_b32 v56, v75, v50
	ds_bpermute_b32 v57, v75, v51
	s_and_b64 vcc, exec, s[10:11]
	s_cbranch_vccnz .LBB0_535
	v_or_b32_e32 v52, s84, v78
	v_or_b32_e32 v52, s94, v52
	v_mov_b32_e32 v53, s95
	v_lshlrev_b64 v[52:53], 9, v[52:53]
	v_lshl_add_u64 v[52:53], s[28:29], 0, v[52:53]
	v_lshl_add_u64 v[52:53], v[52:53], 0, s[88:89]
	s_mov_b64 s[36:37], 0

.LBB0_537:
	s_waitcnt vmcnt(0) lgkmcnt(6)
	v_pk_mul_f32 v[20:21], v[20:21], v[72:73]
	s_waitcnt lgkmcnt(2)
	v_pk_mul_f32 v[12:13], v[12:13], v[60:61]
	v_cndmask_b32_e64 v21, v21, -v21, s[6:7]
	v_cndmask_b32_e64 v20, v20, -v20, s[6:7]
	v_cndmask_b32_e64 v13, v13, -v13, s[6:7]
	v_cndmask_b32_e64 v12, v12, -v12, s[6:7]
	v_pk_fma_f32 v[16:17], v[16:17], v[70:71], v[20:21]
	v_pk_mul_f32 v[20:21], v[22:23], v[62:63]
	v_pk_fma_f32 v[12:13], v[8:9], v[54:55], v[12:13]
	s_waitcnt lgkmcnt(0)
	v_pk_mul_f32 v[8:9], v[14:15], v[56:57]
	v_cndmask_b32_e64 v21, v21, -v21, s[6:7]
	v_cndmask_b32_e64 v20, v20, -v20, s[6:7]
	v_cndmask_b32_e64 v9, v9, -v9, s[6:7]
	v_cndmask_b32_e64 v8, v8, -v8, s[6:7]
	v_pk_fma_f32 v[18:19], v[18:19], v[58:59], v[20:21]
	v_pk_fma_f32 v[14:15], v[10:11], v[50:51], v[8:9]
	v_cvt_pk_bf16_f32 v8, v16, v17
	v_cvt_pk_bf16_f32 v9, v18, v19
	v_cvt_pk_bf16_f32 v10, v12, v13
	v_cvt_pk_bf16_f32 v11, v14, v15
	v_lshl_add_u64 v[12:13], v[52:53], 0, v[64:65]
	global_store_dwordx4 v[12:13], v[8:11], off nt
	s_nop 1
	v_lshl_add_u64 v[8:9], v[36:37], 0, s[50:51]
	global_load_dwordx4 v[50:53], v[8:9], off
	v_add_u32_e32 v8, 12, v29
	v_mov_b32_e32 v10, s16
	v_cndmask_b32_e64 v8, v8, v10, s[8:9]
	v_mov_b32_e32 v9, v65
	v_lshlrev_b32_e32 v8, 5, v8
	v_lshlrev_b64 v[8:9], 2, v[8:9]
	v_lshl_add_u64 v[12:13], v[30:31], 0, v[8:9]
	v_lshl_add_u64 v[20:21], v[32:33], 0, v[8:9]
	global_load_dwordx4 v[8:11], v[12:13], off offset:16
	global_load_dwordx4 v[16:19], v[12:13], off
	s_nop 0
	global_load_dwordx4 v[12:15], v[20:21], off offset:16
	s_nop 0
	global_load_dwordx4 v[20:23], v[20:21], off
	s_waitcnt vmcnt(4)
	v_lshlrev_b32_e32 v58, 16, v50
	v_and_b32_e32 v59, 0xffff0000, v50
	v_lshlrev_b32_e32 v56, 16, v53
	v_and_b32_e32 v57, 0xffff0000, v53
	v_lshlrev_b32_e32 v54, 16, v52
	v_and_b32_e32 v55, 0xffff0000, v52
	v_lshlrev_b32_e32 v52, 16, v51
	v_and_b32_e32 v53, 0xffff0000, v51
	v_pk_mul_f32 v[70:71], v[58:59], v[58:59]
	v_pk_mul_f32 v[62:63], v[52:53], v[52:53]
	v_add_f32_e32 v29, v70, v71
	v_add_f32_e32 v29, v62, v29
	v_pk_mul_f32 v[60:61], v[54:55], v[54:55]
	v_add_f32_e32 v29, v63, v29
	v_add_f32_e32 v29, v60, v29
	v_pk_mul_f32 v[50:51], v[56:57], v[56:57]
	v_add_f32_e32 v29, v61, v29
	v_add_f32_e32 v29, v50, v29
	v_add_f32_e32 v29, v51, v29
	ds_bpermute_b32 v50, v25, v29
	s_waitcnt lgkmcnt(0)
	v_add_f32_e32 v29, v29, v50
	ds_bpermute_b32 v50, v74, v29
	s_waitcnt lgkmcnt(0)
	v_add_f32_e32 v29, v29, v50
	ds_bpermute_b32 v50, v75, v29
	s_waitcnt lgkmcnt(0)
	v_add_f32_e32 v29, v29, v50
	ds_bpermute_b32 v50, v76, v29
	s_waitcnt lgkmcnt(0)
	v_add_f32_e32 v29, v29, v50
	v_fmamk_f32 v29, v29, 0x3c000000, v86
	v_mul_f32_e32 v50, 0x4b800000, v29
	v_cmp_gt_f32_e32 vcc, s0, v29
	s_nop 1
	v_cndmask_b32_e32 v29, v29, v50, vcc
	v_rsq_f32_e32 v29, v29
	s_nop 0
	v_mul_f32_e32 v50, 0x45800000, v29
	v_cndmask_b32_e32 v50, v29, v50, vcc
	v_pk_mul_f32 v[60:61], v[0:1], v[50:51] op_sel_hi:[1,0]
	v_pk_mul_f32 v[62:63], v[2:3], v[50:51] op_sel_hi:[1,0]
	v_pk_mul_f32 v[72:73], v[4:5], v[50:51] op_sel_hi:[1,0]
	v_pk_mul_f32 v[50:51], v[6:7], v[50:51] op_sel_hi:[1,0]
	v_pk_mul_f32 v[70:71], v[60:61], v[58:59]
	v_pk_mul_f32 v[58:59], v[62:63], v[52:53]
	v_pk_mul_f32 v[54:55], v[72:73], v[54:55]
	v_pk_mul_f32 v[50:51], v[50:51], v[56:57]
	ds_bpermute_b32 v72, v75, v70
	ds_bpermute_b32 v73, v75, v71
	ds_bpermute_b32 v62, v75, v58
	ds_bpermute_b32 v63, v75, v59
	ds_bpermute_b32 v60, v75, v54
	ds_bpermute_b32 v61, v75, v55
	ds_bpermute_b32 v56, v75, v50
	ds_bpermute_b32 v57, v75, v51
	s_and_b64 vcc, exec, s[10:11]
	s_mov_b64 s[10:11], -1
	s_cbranch_vccnz .LBB0_539
	v_or_b32_e32 v29, s84, v79
	v_or_b32_e32 v52, s94, v29
	v_mov_b32_e32 v53, s95
	v_lshlrev_b64 v[52:53], 9, v[52:53]
	v_lshl_add_u64 v[52:53], s[28:29], 0, v[52:53]
	v_lshl_add_u64 v[52:53], v[52:53], 0, s[88:89]
	s_mov_b64 s[10:11], 0

.LBB0_544:
	v_lshl_add_u64 v[20:21], s[18:19], 0, v[18:19]
	global_load_dword v23, v[20:21], off offset:-768
	global_load_dword v25, v[20:21], off offset:-512
	global_load_dword v29, v[20:21], off offset:-256
	v_mov_b32_e32 v36, v65
	v_mov_b32_e32 v37, v65
	s_waitcnt vmcnt(2)
	v_lshlrev_b32_e32 v22, 16, v23
	v_and_b32_e32 v23, 0xffff0000, v23
	s_waitcnt vmcnt(0)
	v_lshlrev_b32_e32 v28, 16, v29
	v_and_b32_e32 v29, 0xffff0000, v29
	v_lshlrev_b32_e32 v26, 16, v25
	v_and_b32_e32 v27, 0xffff0000, v25
	v_mov_b32_e32 v34, v23
	v_mov_b32_e32 v35, v29
	v_pk_mul_f32 v[30:31], v[26:27], v[26:27]
	v_mov_b32_e32 v32, v22
	v_mov_b32_e32 v33, v28
	v_pk_mul_f32 v[34:35], v[34:35], v[34:35]
	v_add_f32_e32 v25, v30, v31
	v_pk_fma_f32 v[30:31], v[32:33], v[32:33], v[34:35]
	s_nop 0
	v_add_f32_e32 v25, v30, v25
	v_add_f32_e32 v25, v25, v31
	s_nop 1
	v_add_f32_dpp v25, v25, v25 quad_perm:[1,0,3,2] row_mask:0xf bank_mask:0xf bound_ctrl:1
	s_nop 1
	v_add_f32_dpp v25, v25, v25 quad_perm:[2,3,0,1] row_mask:0xf bank_mask:0xf bound_ctrl:1
	s_nop 1
	v_add_f32_dpp v25, v25, v25 row_half_mirror row_mask:0xf bank_mask:0xf bound_ctrl:1
	s_nop 1
	v_add_f32_dpp v25, v25, v25 row_mirror row_mask:0xf bank_mask:0xf bound_ctrl:1
	s_nop 1
	v_mov_b32_dpp v36, v25 row_bcast:15 row_mask:0xa bank_mask:0xf
	v_add_f32_e32 v25, v25, v36
	s_nop 1
	v_mov_b32_dpp v37, v25 row_bcast:31 row_mask:0xc bank_mask:0xf
	v_add_f32_e32 v25, v25, v37
	s_nop 0
	v_readlane_b32 s6, v25, 63
	s_nop 1
	v_fma_f32 v25, s6, v90, v86
	v_mul_f32_e32 v30, 0x4b800000, v25
	v_cmp_gt_f32_e32 vcc, s0, v25
	s_nop 1
	v_cndmask_b32_e32 v25, v25, v30, vcc
	v_rsq_f32_e32 v25, v25
	v_lshl_add_u64 v[30:31], s[18:19], 0, v[16:17]
	v_mul_f32_e32 v32, 0x45800000, v25
	v_cndmask_b32_e32 v32, v25, v32, vcc
	v_pk_mul_f32 v[22:23], v[32:33], v[22:23] op_sel_hi:[0,1]
	v_pk_mul_f32 v[26:27], v[32:33], v[26:27] op_sel_hi:[0,1]
	v_pk_mul_f32 v[28:29], v[32:33], v[28:29] op_sel_hi:[0,1]
	v_pk_mul_f32 v[22:23], v[2:3], v[22:23]
	v_pk_mul_f32 v[26:27], v[4:5], v[26:27]
	v_pk_mul_f32 v[28:29], v[0:1], v[28:29]
	v_cvt_pk_bf16_f32 v22, v22, v23
	v_cvt_pk_bf16_f32 v23, v26, v27
	v_cvt_pk_bf16_f32 v25, v28, v29
	global_store_dword v[30:31], v22, off offset:-256 nt
	global_store_dword v[30:31], v23, off nt
	global_store_dword v[30:31], v25, off offset:256 nt
	global_load_dword v23, v[20:21], off
	s_nop 0
	global_load_dword v25, v[20:21], off offset:256
	v_mov_b32_e32 v32, v65
	v_mov_b32_e32 v33, v65
	v_lshl_add_u64 v[20:21], s[18:19], 0, v[12:13]
	v_add_co_u32_e32 v20, vcc, 0x4b160000, v20
	s_waitcnt vmcnt(1)
	v_lshlrev_b32_e32 v22, 16, v23
	v_and_b32_e32 v23, 0xffff0000, v23
	s_waitcnt vmcnt(0)
	v_and_b32_e32 v27, 0xffff0000, v25
	v_lshlrev_b32_e32 v26, 16, v25
	v_mov_b32_e32 v30, v23
	v_mov_b32_e32 v31, v27
	v_mov_b32_e32 v28, v22
	v_mov_b32_e32 v29, v26
	v_pk_mul_f32 v[30:31], v[30:31], v[30:31]
	v_addc_co_u32_e32 v21, vcc, 0, v21, vcc
	v_pk_fma_f32 v[28:29], v[28:29], v[28:29], v[30:31]
	s_nop 0
	v_add_f32_e32 v25, v28, v29
	s_nop 1
	v_add_f32_dpp v25, v25, v25 quad_perm:[1,0,3,2] row_mask:0xf bank_mask:0xf bound_ctrl:1
	s_nop 1
	v_add_f32_dpp v25, v25, v25 quad_perm:[2,3,0,1] row_mask:0xf bank_mask:0xf bound_ctrl:1
	s_nop 1
	v_add_f32_dpp v25, v25, v25 row_half_mirror row_mask:0xf bank_mask:0xf bound_ctrl:1
	s_nop 1
	v_add_f32_dpp v25, v25, v25 row_mirror row_mask:0xf bank_mask:0xf bound_ctrl:1
	s_nop 1
	v_mov_b32_dpp v32, v25 row_bcast:15 row_mask:0xa bank_mask:0xf
	v_add_f32_e32 v25, v25, v32
	s_nop 1
	v_mov_b32_dpp v33, v25 row_bcast:31 row_mask:0xc bank_mask:0xf
	v_add_f32_e32 v25, v25, v33
	s_nop 0
	v_readlane_b32 s6, v25, 63
	s_nop 1
	v_fma_f32 v25, s6, v91, v86
	v_mul_f32_e32 v28, 0x4b800000, v25
	v_cmp_gt_f32_e64 s[6:7], s0, v25
	s_nop 1
	v_cndmask_b32_e64 v25, v25, v28, s[6:7]
	v_rsq_f32_e32 v25, v25
	s_nop 0
	v_mul_f32_e32 v28, 0x45800000, v25
	v_cndmask_b32_e64 v28, v25, v28, s[6:7]
	v_pk_mul_f32 v[22:23], v[28:29], v[22:23] op_sel_hi:[0,1]
	v_pk_mul_f32 v[26:27], v[28:29], v[26:27] op_sel_hi:[0,1]
	v_pk_mul_f32 v[22:23], v[8:9], v[22:23]
	v_pk_mul_f32 v[26:27], v[6:7], v[26:27]
	v_cvt_pk_bf16_f32 v22, v22, v23
	v_cvt_pk_bf16_f32 v23, v26, v27
	global_store_dword v[20:21], v22, off offset:512 nt
	global_store_dword v[20:21], v23, off offset:768 nt
	s_and_saveexec_b64 s[6:7], s[4:5]
	s_cbranch_execz .LBB0_543
	v_mov_b32_e32 v20, s16
	v_cndmask_b32_e64 v20, v24, v20, s[2:3]
	v_lshl_or_b32 v20, v20, 4, v66
	v_ashrrev_i32_e32 v21, 31, v20
	v_lshl_add_u64 v[26:27], s[18:19], 0, v[14:15]
	v_lshlrev_b64 v[20:21], 2, v[20:21]
	v_add_co_u32_e32 v26, vcc, 0x40561000, v26
	v_lshl_add_u64 v[22:23], s[44:45], 0, v[20:21]
	s_nop 0
	v_addc_co_u32_e32 v27, vcc, 0, v27, vcc
	v_lshl_add_u64 v[20:21], s[46:47], 0, v[20:21]
	global_load_ushort v25, v[26:27], off offset:256
	s_nop 0
	global_load_ushort v26, v[26:27], off offset:288
	s_nop 0
	global_load_dword v27, v[20:21], off
	s_nop 0
	global_load_dword v22, v[22:23], off
	v_lshl_add_u64 v[20:21], s[18:19], 0, v[10:11]
	v_add_co_u32_e32 v20, vcc, 0x4b960000, v20
	s_waitcnt vmcnt(3)
	v_lshlrev_b32_e32 v23, 16, v25
	s_waitcnt vmcnt(2)
	v_lshlrev_b32_e32 v25, 16, v26
	s_waitcnt vmcnt(1)
	v_mul_f32_e32 v26, v27, v25
	s_waitcnt vmcnt(0)
	v_mul_f32_e32 v25, v22, v25
	v_fma_f32 v22, v22, v23, -v26
	v_addc_co_u32_e32 v21, vcc, 0, v21, vcc
	v_fmac_f32_e32 v25, v27, v23
	v_cvt_pk_bf16_f32 v22, v22, s0
	v_cvt_pk_bf16_f32 v23, v25, s0
	global_store_short v[20:21], v22, off offset:512 nt
	global_store_short v[20:21], v23, off offset:544 nt
	s_branch .LBB0_543

.LBB0_903:
	s_or_b64 exec, exec, s[4:5]
	s_lshl_b64 s[2:3], s[22:23], 2
	s_add_u32 s4, s26, s2
	s_addc_u32 s5, s27, s3
	s_waitcnt lgkmcnt(0)
	v_add_u32_e32 v77, s56, v176
	v_ashrrev_i32_e32 v179, 31, v178
	v_lshl_add_u64 v[64:65], v[178:179], 2, s[4:5]
	global_load_dword v71, v[64:65], off
	global_load_dword v70, v[64:65], off offset:128
	global_load_dword v69, v[64:65], off offset:256
	global_load_dword v68, v[64:65], off offset:384
	ds_read_b128 v[78:81], v77
	v_and_b32_e32 v65, 64, v254
	v_xor_b32_e32 v64, 1, v254
	v_add_u32_e32 v76, 64, v65
	v_cmp_lt_i32_e32 vcc, v64, v76
	v_mov_b32_e32 v82, v0
	v_mov_b32_e32 v83, v48
	v_cndmask_b32_e32 v72, v254, v64, vcc
	ds_read_b128 v[64:67], v77 offset:32
	s_waitcnt lgkmcnt(1)
	v_rcp_f32_e32 v74, v78
	v_rcp_f32_e32 v0, v79
	v_mov_b32_e32 v86, v32
	v_mov_b32_e32 v87, v16
	v_mov_b32_e32 v48, v1
	v_pk_mul_f32 v[82:83], v[82:83], v[74:75] op_sel_hi:[1,0]
	v_pk_mul_f32 v[78:79], v[86:87], v[74:75] op_sel_hi:[1,0]
	v_pk_mul_f32 v[86:87], v[48:49], v[0:1] op_sel_hi:[1,0]
	v_mov_b32_e32 v16, v33
	v_pk_mul_f32 v[84:85], v[82:83], v[82:83]
	v_pk_mul_f32 v[48:49], v[86:87], v[86:87]
	v_pk_mul_f32 v[0:1], v[16:17], v[0:1] op_sel_hi:[1,0]
	v_pk_mul_f32 v[74:75], v[78:79], v[78:79]
	v_pk_mul_f32 v[16:17], v[0:1], v[0:1]
	v_mov_b32_e32 v32, v48
	v_mov_b32_e32 v33, v84
	v_mov_b32_e32 v84, v49
	v_pk_add_f32 v[32:33], v[32:33], v[84:85]
	v_mov_b32_e32 v48, v17
	v_mov_b32_e32 v49, v75
	v_pk_add_f32 v[32:33], v[48:49], v[32:33]
	v_mov_b32_e32 v17, v74
	v_lshlrev_b32_e32 v72, 2, v72
	v_pk_add_f32 v[16:17], v[16:17], v[32:33]
	ds_bpermute_b32 v33, v72, v17
	ds_bpermute_b32 v32, v72, v16
	v_xor_b32_e32 v48, 2, v254
	v_cmp_lt_i32_e32 vcc, v48, v76
	s_lshl_b64 s[2:3], s[30:31], 11
	s_add_u32 s2, s24, s2
	v_cndmask_b32_e32 v48, v254, v48, vcc
	v_lshlrev_b32_e32 v73, 2, v48
	s_waitcnt lgkmcnt(0)
	v_pk_add_f32 v[16:17], v[16:17], v[32:33]
	ds_bpermute_b32 v33, v73, v17
	ds_bpermute_b32 v32, v73, v16
	v_xor_b32_e32 v48, 4, v254
	v_cmp_lt_i32_e32 vcc, v48, v76
	s_addc_u32 s3, s25, s3
	s_add_u32 s2, s2, s22
	v_cndmask_b32_e32 v48, v254, v48, vcc
	v_lshlrev_b32_e32 v74, 2, v48
	s_waitcnt lgkmcnt(0)
	v_pk_add_f32 v[16:17], v[16:17], v[32:33]
	ds_bpermute_b32 v33, v74, v17
	ds_bpermute_b32 v32, v74, v16
	v_xor_b32_e32 v48, 8, v254
	v_cmp_lt_i32_e32 vcc, v48, v76
	s_addc_u32 s3, s3, s23
	v_mov_b32_e32 v90, 0
	v_cndmask_b32_e32 v48, v254, v48, vcc
	v_lshlrev_b32_e32 v75, 2, v48
	s_waitcnt lgkmcnt(0)
	v_pk_add_f32 v[16:17], v[16:17], v[32:33]
	ds_bpermute_b32 v33, v75, v17
	ds_bpermute_b32 v32, v75, v16
	v_xor_b32_e32 v48, 16, v254
	v_cmp_lt_i32_e32 vcc, v48, v76
	s_mov_b32 s22, 0
	s_waitcnt lgkmcnt(0)
	v_pk_add_f32 v[16:17], v[16:17], v[32:33]
	v_cndmask_b32_e32 v48, v254, v48, vcc
	v_lshlrev_b32_e32 v76, 2, v48
	ds_bpermute_b32 v33, v76, v17
	ds_bpermute_b32 v32, v76, v16
	v_lshlrev_b32_e32 v48, 2, v178
	v_ashrrev_i32_e32 v49, 31, v48
	v_lshl_add_u64 v[84:85], s[2:3], 0, v[48:49]
	v_mov_b64_e32 v[48:49], s[20:21]
	s_waitcnt lgkmcnt(0)
	v_pk_add_f32 v[16:17], v[16:17], v[32:33]
	v_lshl_or_b32 v32, v216, 2, s55
	v_pk_fma_f32 v[88:89], v[16:17], s[18:19], v[48:49] op_sel_hi:[1,0,0]
	v_ashrrev_i32_e32 v33, 31, v32
	v_mul_f32_e32 v16, 0x4b800000, v89
	v_cmp_gt_f32_e32 vcc, s33, v89
	s_nop 1
	v_cndmask_b32_e32 v16, v89, v16, vcc
	v_rsq_f32_e32 v89, v16
	v_lshl_add_u64 v[16:17], v[84:85], 0, s[14:15]
	v_mul_f32_e32 v84, 0x45800000, v89
	v_cndmask_b32_e32 v84, v89, v84, vcc
	v_mul_f32_e32 v82, v82, v84
	v_mul_f32_e32 v83, v83, v84
	s_waitcnt vmcnt(3)
	v_mul_f32_e32 v82, v71, v82
	s_waitcnt vmcnt(2)
	v_mul_f32_e32 v83, v70, v83
	v_cvt_pk_fp8_f32 v90, v82, v83
	v_mul_f32_e32 v79, v79, v84
	v_mul_f32_e32 v78, v78, v84
	s_waitcnt vmcnt(1)
	v_mul_f32_e32 v79, v69, v79
	s_waitcnt vmcnt(0)
	v_mul_f32_e32 v78, v68, v78
	v_cvt_pk_fp8_f32 v90, v79, v78 op_sel:[0,0,1]
	v_mul_f32_e32 v78, 0x4b800000, v88
	v_cmp_gt_f32_e32 vcc, s33, v88
	v_mov_b32_e32 v82, v2
	v_rcp_f32_e32 v2, v81
	v_cndmask_b32_e32 v79, v88, v78, vcc
	v_rcp_f32_e32 v78, v80
	v_mov_b32_e32 v83, v50
	v_mov_b32_e32 v50, v3
	v_mov_b32_e32 v88, v34
	v_pk_mul_f32 v[82:83], v[82:83], v[78:79] op_sel_hi:[1,0]
	v_mov_b32_e32 v89, v18
	v_pk_mul_f32 v[50:51], v[50:51], v[2:3] op_sel_hi:[1,0]
	v_mov_b32_e32 v18, v35
	v_rsq_f32_e32 v91, v79
	v_pk_mul_f32 v[84:85], v[82:83], v[82:83]
	v_pk_mul_f32 v[78:79], v[88:89], v[78:79] op_sel_hi:[1,0]
	v_pk_mul_f32 v[88:89], v[50:51], v[50:51]
	v_pk_mul_f32 v[2:3], v[18:19], v[2:3] op_sel_hi:[1,0]
	v_pk_mul_f32 v[80:81], v[78:79], v[78:79]
	v_pk_mul_f32 v[18:19], v[2:3], v[2:3]
	v_mov_b32_e32 v34, v88
	v_mov_b32_e32 v35, v84
	v_mov_b32_e32 v84, v89
	v_pk_add_f32 v[34:35], v[34:35], v[84:85]
	v_mov_b32_e32 v84, v19
	v_mov_b32_e32 v85, v81
	v_pk_add_f32 v[34:35], v[84:85], v[34:35]
	v_mov_b32_e32 v19, v80
	v_pk_add_f32 v[18:19], v[18:19], v[34:35]
	ds_bpermute_b32 v35, v72, v19
	ds_bpermute_b32 v34, v72, v18
	v_lshlrev_b64 v[80:81], 11, v[32:33]
	v_mul_f32_e32 v33, 0x45800000, v91
	v_lshl_add_u64 v[80:81], v[16:17], 0, v[80:81]
	v_cndmask_b32_e32 v33, v91, v33, vcc
	s_waitcnt lgkmcnt(0)
	v_pk_add_f32 v[18:19], v[18:19], v[34:35]
	ds_bpermute_b32 v35, v73, v19
	ds_bpermute_b32 v34, v73, v18
	global_store_dword v[80:81], v90, off nt
	v_mul_f32_e32 v80, v86, v33
	v_mul_f32_e32 v81, v87, v33
	v_mul_f32_e32 v80, v71, v80
	s_waitcnt lgkmcnt(0)
	v_pk_add_f32 v[18:19], v[18:19], v[34:35]
	ds_bpermute_b32 v35, v74, v19
	ds_bpermute_b32 v34, v74, v18
	v_mul_f32_e32 v81, v70, v81
	v_mov_b32_e32 v84, 0
	v_cvt_pk_fp8_f32 v84, v80, v81
	v_mul_f32_e32 v1, v1, v33
	s_waitcnt lgkmcnt(0)
	v_pk_add_f32 v[18:19], v[18:19], v[34:35]
	ds_bpermute_b32 v35, v75, v19
	ds_bpermute_b32 v34, v75, v18
	v_mul_f32_e32 v0, v0, v33
	v_mul_f32_e32 v1, v69, v1
	v_mul_f32_e32 v0, v68, v0
	v_cvt_pk_fp8_f32 v84, v1, v0 op_sel:[0,0,1]
	s_waitcnt lgkmcnt(0)
	v_pk_add_f32 v[0:1], v[18:19], v[34:35]
	ds_bpermute_b32 v19, v76, v1
	ds_bpermute_b32 v18, v76, v0
	v_or_b32_e32 v34, 1, v32
	v_ashrrev_i32_e32 v35, 31, v34
	v_lshlrev_b64 v[34:35], 11, v[34:35]
	v_lshl_add_u64 v[34:35], v[16:17], 0, v[34:35]
	s_waitcnt lgkmcnt(0)
	v_pk_add_f32 v[0:1], v[0:1], v[18:19]
	global_store_dword v[34:35], v84, off nt
	v_pk_fma_f32 v[0:1], v[0:1], s[18:19], v[48:49] op_sel_hi:[1,0,0]
	v_mov_b32_e32 v80, v36
	v_mul_f32_e32 v18, 0x4b800000, v1
	v_cmp_gt_f32_e32 vcc, s33, v1
	v_mov_b32_e32 v81, v20
	v_mov_b32_e32 v20, v37
	v_cndmask_b32_e32 v1, v1, v18, vcc
	v_rsq_f32_e32 v1, v1
	v_or_b32_e32 v18, 2, v32
	v_ashrrev_i32_e32 v19, 31, v18
	v_lshlrev_b64 v[18:19], 11, v[18:19]
	v_mul_f32_e32 v33, 0x45800000, v1
	v_cndmask_b32_e32 v1, v1, v33, vcc
	v_mul_f32_e32 v33, v82, v1
	v_mul_f32_e32 v34, v83, v1
	v_mul_f32_e32 v33, v71, v33
	v_mul_f32_e32 v34, v70, v34
	v_mov_b32_e32 v82, 0
	v_cvt_pk_fp8_f32 v82, v33, v34
	v_mul_f32_e32 v35, v79, v1
	v_mul_f32_e32 v1, v78, v1
	v_mul_f32_e32 v33, v69, v35
	v_mul_f32_e32 v1, v68, v1
	v_cvt_pk_fp8_f32 v82, v33, v1 op_sel:[0,0,1]
	v_mul_f32_e32 v1, 0x4b800000, v0
	v_cmp_gt_f32_e32 vcc, s33, v0
	v_mov_b32_e32 v34, v4
	v_rcp_f32_e32 v4, v65
	v_cndmask_b32_e32 v1, v0, v1, vcc
	v_rcp_f32_e32 v0, v64
	v_mov_b32_e32 v35, v52
	v_mov_b32_e32 v52, v5
	v_pk_mul_f32 v[52:53], v[52:53], v[4:5] op_sel_hi:[1,0]
	v_pk_mul_f32 v[34:35], v[34:35], v[0:1] op_sel_hi:[1,0]
	v_rsq_f32_e32 v33, v1
	v_pk_mul_f32 v[78:79], v[34:35], v[34:35]
	v_pk_mul_f32 v[0:1], v[80:81], v[0:1] op_sel_hi:[1,0]
	v_pk_mul_f32 v[80:81], v[52:53], v[52:53]
	v_pk_mul_f32 v[4:5], v[20:21], v[4:5] op_sel_hi:[1,0]
	v_pk_mul_f32 v[64:65], v[0:1], v[0:1]
	v_pk_mul_f32 v[20:21], v[4:5], v[4:5]
	v_mov_b32_e32 v36, v80
	v_mov_b32_e32 v37, v78
	v_mov_b32_e32 v78, v81
	v_pk_add_f32 v[36:37], v[36:37], v[78:79]
	v_mov_b32_e32 v78, v21
	v_mov_b32_e32 v79, v65
	v_pk_add_f32 v[36:37], v[78:79], v[36:37]
	v_mov_b32_e32 v21, v64
	v_pk_add_f32 v[20:21], v[20:21], v[36:37]
	ds_bpermute_b32 v37, v72, v21
	ds_bpermute_b32 v36, v72, v20
	v_lshl_add_u64 v[18:19], v[16:17], 0, v[18:19]
	global_store_dword v[18:19], v82, off nt
	v_mul_f32_e32 v64, 0x45800000, v33
	v_cndmask_b32_e32 v33, v33, v64, vcc
	s_waitcnt lgkmcnt(0)
	v_pk_add_f32 v[18:19], v[20:21], v[36:37]
	ds_bpermute_b32 v21, v73, v19
	ds_bpermute_b32 v20, v73, v18
	v_mul_f32_e32 v36, v50, v33
	v_mul_f32_e32 v37, v51, v33
	v_mul_f32_e32 v36, v71, v36
	v_mul_f32_e32 v37, v70, v37
	s_waitcnt lgkmcnt(0)
	v_pk_add_f32 v[18:19], v[18:19], v[20:21]
	ds_bpermute_b32 v21, v74, v19
	ds_bpermute_b32 v20, v74, v18
	v_mov_b32_e32 v50, 0
	v_cvt_pk_fp8_f32 v50, v36, v37
	v_mul_f32_e32 v3, v3, v33
	v_mul_f32_e32 v2, v2, v33
	s_waitcnt lgkmcnt(0)
	v_pk_add_f32 v[18:19], v[18:19], v[20:21]
	ds_bpermute_b32 v21, v75, v19
	ds_bpermute_b32 v20, v75, v18
	v_mul_f32_e32 v3, v69, v3
	v_mul_f32_e32 v2, v68, v2
	v_cvt_pk_fp8_f32 v50, v3, v2 op_sel:[0,0,1]
	v_mov_b32_e32 v33, 0
	s_waitcnt lgkmcnt(0)
	v_pk_add_f32 v[2:3], v[18:19], v[20:21]
	ds_bpermute_b32 v19, v76, v3
	ds_bpermute_b32 v18, v76, v2
	v_or_b32_e32 v20, 3, v32
	v_ashrrev_i32_e32 v21, 31, v20
	v_lshlrev_b64 v[20:21], 11, v[20:21]
	v_lshl_add_u64 v[20:21], v[16:17], 0, v[20:21]
	s_waitcnt lgkmcnt(0)
	v_pk_add_f32 v[2:3], v[2:3], v[18:19]
	global_store_dword v[20:21], v50, off nt
	v_pk_fma_f32 v[2:3], v[2:3], s[18:19], v[48:49] op_sel_hi:[1,0,0]
	v_or_b32_e32 v36, 8, v32
	v_mul_f32_e32 v18, 0x4b800000, v3
	v_cmp_gt_f32_e32 vcc, s33, v3
	v_ashrrev_i32_e32 v37, 31, v36
	s_nop 0
	v_cndmask_b32_e32 v3, v3, v18, vcc
	v_rsq_f32_e32 v3, v3
	s_nop 0
	v_mul_f32_e32 v18, 0x45800000, v3
	v_cndmask_b32_e32 v3, v3, v18, vcc
	v_mul_f32_e32 v18, v34, v3
	v_mul_f32_e32 v19, v35, v3
	v_mul_f32_e32 v18, v71, v18
	v_mul_f32_e32 v19, v70, v19
	v_cvt_pk_fp8_f32 v33, v18, v19
	v_mul_f32_e32 v1, v1, v3
	v_mul_f32_e32 v0, v0, v3
	v_mul_f32_e32 v1, v69, v1
	v_mul_f32_e32 v0, v68, v0
	v_cvt_pk_fp8_f32 v33, v1, v0 op_sel:[0,0,1]
	v_mul_f32_e32 v0, 0x4b800000, v2
	v_cmp_gt_f32_e32 vcc, s33, v2
	v_mov_b32_e32 v3, v54
	v_mov_b32_e32 v54, v7
	v_cndmask_b32_e32 v1, v2, v0, vcc
	v_rcp_f32_e32 v0, v66
	v_mov_b32_e32 v2, v6
	v_rcp_f32_e32 v6, v67
	v_mov_b32_e32 v18, v38
	v_pk_mul_f32 v[2:3], v[2:3], v[0:1] op_sel_hi:[1,0]
	v_mov_b32_e32 v19, v22
	v_pk_mul_f32 v[20:21], v[54:55], v[6:7] op_sel_hi:[1,0]
	v_mov_b32_e32 v22, v39
	v_rsq_f32_e32 v64, v1
	v_pk_mul_f32 v[34:35], v[2:3], v[2:3]
	v_pk_mul_f32 v[0:1], v[18:19], v[0:1] op_sel_hi:[1,0]
	v_pk_mul_f32 v[54:55], v[20:21], v[20:21]
	v_pk_mul_f32 v[18:19], v[22:23], v[6:7] op_sel_hi:[1,0]
	v_pk_mul_f32 v[50:51], v[0:1], v[0:1]
	v_pk_mul_f32 v[6:7], v[18:19], v[18:19]
	v_mov_b32_e32 v22, v54
	v_mov_b32_e32 v23, v34
	v_mov_b32_e32 v34, v55
	v_pk_add_f32 v[22:23], v[22:23], v[34:35]
	v_mov_b32_e32 v34, v7
	v_mov_b32_e32 v35, v51
	v_pk_add_f32 v[22:23], v[34:35], v[22:23]
	v_mov_b32_e32 v7, v50
	v_pk_add_f32 v[6:7], v[6:7], v[22:23]
	ds_bpermute_b32 v23, v72, v7
	ds_bpermute_b32 v22, v72, v6
	v_lshlrev_b64 v[34:35], 11, v[36:37]
	v_lshl_add_u64 v[34:35], v[16:17], 0, v[34:35]
	global_store_dword v[34:35], v33, off nt
	v_mul_f32_e32 v33, 0x45800000, v64
	s_waitcnt lgkmcnt(0)
	v_pk_add_f32 v[6:7], v[6:7], v[22:23]
	ds_bpermute_b32 v23, v73, v7
	ds_bpermute_b32 v22, v73, v6
	v_cndmask_b32_e32 v33, v64, v33, vcc
	v_mul_f32_e32 v34, v52, v33
	v_mul_f32_e32 v35, v53, v33
	v_mul_f32_e32 v34, v71, v34
	s_waitcnt lgkmcnt(0)
	v_pk_add_f32 v[6:7], v[6:7], v[22:23]
	ds_bpermute_b32 v23, v74, v7
	ds_bpermute_b32 v22, v74, v6
	v_mul_f32_e32 v35, v70, v35
	v_mov_b32_e32 v36, 0
	v_cvt_pk_fp8_f32 v36, v34, v35
	v_mul_f32_e32 v5, v5, v33
	s_waitcnt lgkmcnt(0)
	v_pk_add_f32 v[6:7], v[6:7], v[22:23]
	ds_bpermute_b32 v23, v75, v7
	ds_bpermute_b32 v22, v75, v6
	v_mul_f32_e32 v4, v4, v33
	v_mul_f32_e32 v5, v69, v5
	v_mul_f32_e32 v4, v68, v4
	v_cvt_pk_fp8_f32 v36, v5, v4 op_sel:[0,0,1]
	s_waitcnt lgkmcnt(0)
	v_pk_add_f32 v[4:5], v[6:7], v[22:23]
	ds_bpermute_b32 v7, v76, v5
	ds_bpermute_b32 v6, v76, v4
	v_mov_b32_e32 v33, 0
	v_or_b32_e32 v22, 9, v32
	v_ashrrev_i32_e32 v23, 31, v22
	v_lshlrev_b64 v[22:23], 11, v[22:23]
	s_waitcnt lgkmcnt(0)
	v_pk_add_f32 v[4:5], v[4:5], v[6:7]
	v_lshl_add_u64 v[22:23], v[16:17], 0, v[22:23]
	v_pk_fma_f32 v[34:35], v[4:5], s[18:19], v[48:49] op_sel_hi:[1,0,0]
	v_mov_b32_e32 v38, v40
	v_mul_f32_e32 v4, 0x4b800000, v35
	v_cmp_gt_f32_e32 vcc, s33, v35
	v_mov_b32_e32 v39, v24
	v_mov_b32_e32 v24, v41
	v_cndmask_b32_e32 v4, v35, v4, vcc
	v_rsq_f32_e32 v4, v4
	v_mov_b32_e32 v35, v56
	v_mov_b32_e32 v56, v9
	global_store_dword v[22:23], v36, off nt
	v_mul_f32_e32 v5, 0x45800000, v4
	v_cndmask_b32_e32 v4, v4, v5, vcc
	v_mul_f32_e32 v2, v2, v4
	v_mul_f32_e32 v3, v3, v4
	v_mul_f32_e32 v2, v71, v2
	v_mul_f32_e32 v3, v70, v3
	v_cvt_pk_fp8_f32 v33, v2, v3
	v_mul_f32_e32 v1, v1, v4
	v_mul_f32_e32 v0, v0, v4
	ds_read_b128 v[4:7], v77 offset:64
	v_mul_f32_e32 v1, v69, v1
	v_mul_f32_e32 v0, v68, v0
	v_cvt_pk_fp8_f32 v33, v1, v0 op_sel:[0,0,1]
	v_mul_f32_e32 v0, 0x4b800000, v34
	v_cmp_gt_f32_e32 vcc, s33, v34
	v_or_b32_e32 v22, 10, v32
	v_ashrrev_i32_e32 v23, 31, v22
	v_cndmask_b32_e32 v34, v34, v0, vcc
	ds_read_b128 v[0:3], v77 offset:96
	s_waitcnt lgkmcnt(1)
	v_rcp_f32_e32 v4, v4
	v_rsq_f32_e32 v54, v34
	v_mov_b32_e32 v34, v8
	v_rcp_f32_e32 v8, v5
	v_pk_mul_f32 v[34:35], v[34:35], v[4:5] op_sel_hi:[1,0]
	v_pk_mul_f32 v[4:5], v[38:39], v[4:5] op_sel_hi:[1,0]
	v_pk_mul_f32 v[36:37], v[34:35], v[34:35]
	v_pk_mul_f32 v[50:51], v[56:57], v[8:9] op_sel_hi:[1,0]
	v_pk_mul_f32 v[8:9], v[24:25], v[8:9] op_sel_hi:[1,0]
	v_pk_mul_f32 v[52:53], v[50:51], v[50:51]
	v_pk_mul_f32 v[38:39], v[4:5], v[4:5]
	v_pk_mul_f32 v[24:25], v[8:9], v[8:9]
	v_mov_b32_e32 v40, v52
	v_mov_b32_e32 v41, v36
	v_mov_b32_e32 v36, v53
	v_pk_add_f32 v[36:37], v[40:41], v[36:37]
	v_mov_b32_e32 v40, v25
	v_mov_b32_e32 v41, v39
	v_pk_add_f32 v[36:37], v[40:41], v[36:37]
	v_mov_b32_e32 v25, v38
	v_pk_add_f32 v[24:25], v[24:25], v[36:37]
	ds_bpermute_b32 v37, v72, v25
	ds_bpermute_b32 v36, v72, v24
	v_lshlrev_b64 v[22:23], 11, v[22:23]
	v_lshl_add_u64 v[22:23], v[16:17], 0, v[22:23]
	global_store_dword v[22:23], v33, off nt
	v_mul_f32_e32 v33, 0x45800000, v54
	s_waitcnt lgkmcnt(0)
	v_pk_add_f32 v[22:23], v[24:25], v[36:37]
	ds_bpermute_b32 v25, v73, v23
	ds_bpermute_b32 v24, v73, v22
	v_cndmask_b32_e32 v33, v54, v33, vcc
	v_mul_f32_e32 v20, v20, v33
	v_mul_f32_e32 v36, v71, v20
	v_mul_f32_e32 v37, v21, v33
	s_waitcnt lgkmcnt(0)
	v_pk_add_f32 v[20:21], v[22:23], v[24:25]
	ds_bpermute_b32 v23, v74, v21
	ds_bpermute_b32 v22, v74, v20
	v_mul_f32_e32 v24, v70, v37
	v_mov_b32_e32 v25, 0
	v_cvt_pk_fp8_f32 v25, v36, v24
	v_mul_f32_e32 v19, v19, v33
	s_waitcnt lgkmcnt(0)
	v_pk_add_f32 v[20:21], v[20:21], v[22:23]
	ds_bpermute_b32 v23, v75, v21
	ds_bpermute_b32 v22, v75, v20
	v_mul_f32_e32 v18, v18, v33
	v_mul_f32_e32 v19, v69, v19
	v_mul_f32_e32 v18, v68, v18
	v_cvt_pk_fp8_f32 v25, v19, v18 op_sel:[0,0,1]
	s_waitcnt lgkmcnt(0)
	v_pk_add_f32 v[18:19], v[20:21], v[22:23]
	ds_bpermute_b32 v21, v76, v19
	ds_bpermute_b32 v20, v76, v18
	v_or_b32_e32 v22, 11, v32
	v_ashrrev_i32_e32 v23, 31, v22
	v_lshlrev_b64 v[22:23], 11, v[22:23]
	v_lshl_add_u64 v[22:23], v[16:17], 0, v[22:23]
	s_waitcnt lgkmcnt(0)
	v_pk_add_f32 v[18:19], v[18:19], v[20:21]
	global_store_dword v[22:23], v25, off nt
	v_pk_fma_f32 v[18:19], v[18:19], s[18:19], v[48:49] op_sel_hi:[1,0,0]
	v_mov_b32_e32 v33, 0
	v_mul_f32_e32 v20, 0x4b800000, v19
	v_cmp_gt_f32_e32 vcc, s33, v19
	v_mov_b32_e32 v24, v42
	v_mov_b32_e32 v25, v26
	v_cndmask_b32_e32 v19, v19, v20, vcc
	v_rsq_f32_e32 v19, v19
	v_mov_b32_e32 v26, v43
	v_or_b32_e32 v20, 16, v32
	v_ashrrev_i32_e32 v21, 31, v20
	v_mul_f32_e32 v22, 0x45800000, v19
	v_cndmask_b32_e32 v19, v19, v22, vcc
	v_mul_f32_e32 v22, v34, v19
	v_mul_f32_e32 v23, v35, v19
	v_mul_f32_e32 v22, v71, v22
	v_mul_f32_e32 v23, v70, v23
	v_cvt_pk_fp8_f32 v33, v22, v23
	v_mul_f32_e32 v5, v5, v19
	v_mul_f32_e32 v4, v4, v19
	v_mul_f32_e32 v5, v69, v5
	v_mul_f32_e32 v4, v68, v4
	v_cvt_pk_fp8_f32 v33, v5, v4 op_sel:[0,0,1]
	v_mul_f32_e32 v4, 0x4b800000, v18
	v_cmp_gt_f32_e32 vcc, s33, v18
	v_mov_b32_e32 v19, v58
	v_mov_b32_e32 v58, v11
	v_cndmask_b32_e32 v5, v18, v4, vcc
	v_rcp_f32_e32 v4, v6
	v_rcp_f32_e32 v6, v7
	v_mov_b32_e32 v18, v10
	v_rsq_f32_e32 v38, v5
	v_pk_mul_f32 v[18:19], v[18:19], v[4:5] op_sel_hi:[1,0]
	v_pk_mul_f32 v[10:11], v[58:59], v[6:7] op_sel_hi:[1,0]
	v_pk_mul_f32 v[22:23], v[18:19], v[18:19]
	v_pk_mul_f32 v[4:5], v[24:25], v[4:5] op_sel_hi:[1,0]
	v_pk_mul_f32 v[34:35], v[10:11], v[10:11]
	v_pk_mul_f32 v[6:7], v[26:27], v[6:7] op_sel_hi:[1,0]
	v_pk_mul_f32 v[24:25], v[4:5], v[4:5]
	v_pk_mul_f32 v[26:27], v[6:7], v[6:7]
	v_mov_b32_e32 v36, v34
	v_mov_b32_e32 v37, v22
	v_mov_b32_e32 v22, v35
	v_pk_add_f32 v[22:23], v[36:37], v[22:23]
	v_mov_b32_e32 v34, v27
	v_mov_b32_e32 v35, v25
	v_pk_add_f32 v[22:23], v[34:35], v[22:23]
	v_mov_b32_e32 v27, v24
	v_pk_add_f32 v[22:23], v[26:27], v[22:23]
	ds_bpermute_b32 v25, v72, v23
	ds_bpermute_b32 v24, v72, v22
	v_lshlrev_b64 v[20:21], 11, v[20:21]
	v_lshl_add_u64 v[20:21], v[16:17], 0, v[20:21]
	global_store_dword v[20:21], v33, off nt
	v_mul_f32_e32 v26, 0x45800000, v38
	s_waitcnt lgkmcnt(0)
	v_pk_add_f32 v[20:21], v[22:23], v[24:25]
	ds_bpermute_b32 v23, v73, v21
	ds_bpermute_b32 v22, v73, v20
	v_cndmask_b32_e32 v24, v38, v26, vcc
	v_mul_f32_e32 v25, v50, v24
	v_mul_f32_e32 v26, v51, v24
	v_mul_f32_e32 v25, v71, v25
	s_waitcnt lgkmcnt(0)
	v_pk_add_f32 v[20:21], v[20:21], v[22:23]
	ds_bpermute_b32 v23, v74, v21
	ds_bpermute_b32 v22, v74, v20
	v_mul_f32_e32 v26, v70, v26
	v_mov_b32_e32 v27, 0
	v_cvt_pk_fp8_f32 v27, v25, v26
	v_mul_f32_e32 v9, v9, v24
	s_waitcnt lgkmcnt(0)
	v_pk_add_f32 v[20:21], v[20:21], v[22:23]
	ds_bpermute_b32 v23, v75, v21
	ds_bpermute_b32 v22, v75, v20
	v_mul_f32_e32 v8, v8, v24
	v_mul_f32_e32 v9, v69, v9
	v_mul_f32_e32 v8, v68, v8
	v_cvt_pk_fp8_f32 v27, v9, v8 op_sel:[0,0,1]
	s_waitcnt lgkmcnt(0)
	v_pk_add_f32 v[8:9], v[20:21], v[22:23]
	ds_bpermute_b32 v21, v76, v9
	ds_bpermute_b32 v20, v76, v8
	v_or_b32_e32 v22, 17, v32
	v_ashrrev_i32_e32 v23, 31, v22
	v_lshlrev_b64 v[22:23], 11, v[22:23]
	v_lshl_add_u64 v[22:23], v[16:17], 0, v[22:23]
	s_waitcnt lgkmcnt(0)
	v_pk_add_f32 v[8:9], v[8:9], v[20:21]
	global_store_dword v[22:23], v27, off nt
	v_pk_fma_f32 v[8:9], v[8:9], s[18:19], v[48:49] op_sel_hi:[1,0,0]
	v_mov_b32_e32 v33, 0
	v_mul_f32_e32 v20, 0x4b800000, v9
	v_cmp_gt_f32_e32 vcc, s33, v9
	v_rcp_f32_e32 v0, v0
	s_nop 0
	v_cndmask_b32_e32 v9, v9, v20, vcc
	v_rsq_f32_e32 v9, v9
	v_or_b32_e32 v20, 18, v32
	v_ashrrev_i32_e32 v21, 31, v20
	v_lshlrev_b64 v[20:21], 11, v[20:21]
	v_mul_f32_e32 v22, 0x45800000, v9
	v_cndmask_b32_e32 v9, v9, v22, vcc
	v_mul_f32_e32 v18, v18, v9
	v_mul_f32_e32 v19, v19, v9
	v_mul_f32_e32 v18, v71, v18
	v_mul_f32_e32 v19, v70, v19
	v_cvt_pk_fp8_f32 v33, v18, v19
	v_mul_f32_e32 v5, v5, v9
	v_mul_f32_e32 v4, v4, v9
	v_mul_f32_e32 v5, v69, v5
	v_mul_f32_e32 v4, v68, v4
	v_cvt_pk_fp8_f32 v33, v5, v4 op_sel:[0,0,1]
	v_mul_f32_e32 v4, 0x4b800000, v8
	v_cmp_gt_f32_e32 vcc, s33, v8
	v_mov_b32_e32 v5, v60
	v_mov_b32_e32 v60, v13
	v_cndmask_b32_e32 v4, v8, v4, vcc
	v_rsq_f32_e32 v34, v4
	v_mov_b32_e32 v4, v12
	v_rcp_f32_e32 v12, v1
	v_pk_mul_f32 v[4:5], v[4:5], v[0:1] op_sel_hi:[1,0]
	v_mov_b32_e32 v18, v44
	v_mov_b32_e32 v19, v28
	v_pk_mul_f32 v[22:23], v[60:61], v[12:13] op_sel_hi:[1,0]
	v_mov_b32_e32 v28, v45
	v_pk_mul_f32 v[8:9], v[4:5], v[4:5]
	v_pk_mul_f32 v[0:1], v[18:19], v[0:1] op_sel_hi:[1,0]
	v_pk_mul_f32 v[24:25], v[22:23], v[22:23]
	v_pk_mul_f32 v[12:13], v[28:29], v[12:13] op_sel_hi:[1,0]
	v_pk_mul_f32 v[18:19], v[0:1], v[0:1]
	v_pk_mul_f32 v[26:27], v[12:13], v[12:13]
	v_mov_b32_e32 v28, v24
	v_mov_b32_e32 v29, v8
	v_mov_b32_e32 v8, v25
	v_pk_add_f32 v[8:9], v[28:29], v[8:9]
	v_mov_b32_e32 v24, v27
	v_mov_b32_e32 v25, v19
	v_pk_add_f32 v[8:9], v[24:25], v[8:9]
	v_mov_b32_e32 v27, v18
	v_pk_add_f32 v[8:9], v[26:27], v[8:9]
	ds_bpermute_b32 v19, v72, v9
	ds_bpermute_b32 v18, v72, v8
	v_lshl_add_u64 v[20:21], v[16:17], 0, v[20:21]
	global_store_dword v[20:21], v33, off nt
	v_mul_f32_e32 v20, 0x45800000, v34
	v_cndmask_b32_e32 v20, v34, v20, vcc
	s_waitcnt lgkmcnt(0)
	v_pk_add_f32 v[8:9], v[8:9], v[18:19]
	ds_bpermute_b32 v19, v73, v9
	ds_bpermute_b32 v18, v73, v8
	v_mul_f32_e32 v10, v10, v20
	v_mul_f32_e32 v21, v71, v10
	v_mul_f32_e32 v24, v11, v20
	v_mul_f32_e32 v7, v7, v20
	s_waitcnt lgkmcnt(0)
	v_pk_add_f32 v[8:9], v[8:9], v[18:19]
	ds_bpermute_b32 v11, v74, v9
	ds_bpermute_b32 v10, v74, v8
	v_mul_f32_e32 v18, v70, v24
	v_mov_b32_e32 v19, 0
	v_cvt_pk_fp8_f32 v19, v21, v18
	v_mul_f32_e32 v6, v6, v20
	s_waitcnt lgkmcnt(0)
	v_pk_add_f32 v[8:9], v[8:9], v[10:11]
	ds_bpermute_b32 v11, v75, v9
	ds_bpermute_b32 v10, v75, v8
	v_mul_f32_e32 v7, v69, v7
	v_mul_f32_e32 v6, v68, v6
	v_cvt_pk_fp8_f32 v19, v7, v6 op_sel:[0,0,1]
	v_mov_b32_e32 v26, 0
	s_waitcnt lgkmcnt(0)
	v_pk_add_f32 v[6:7], v[8:9], v[10:11]
	ds_bpermute_b32 v9, v76, v7
	ds_bpermute_b32 v8, v76, v6
	v_or_b32_e32 v10, 19, v32
	v_ashrrev_i32_e32 v11, 31, v10
	v_lshlrev_b64 v[10:11], 11, v[10:11]
	v_lshl_add_u64 v[10:11], v[16:17], 0, v[10:11]
	s_waitcnt lgkmcnt(0)
	v_pk_add_f32 v[6:7], v[6:7], v[8:9]
	global_store_dword v[10:11], v19, off nt
	v_pk_fma_f32 v[6:7], v[6:7], s[18:19], v[48:49] op_sel_hi:[1,0,0]
	v_mov_b32_e32 v11, v30
	v_mul_f32_e32 v8, 0x4b800000, v7
	v_cmp_gt_f32_e32 vcc, s33, v7
	v_mov_b32_e32 v30, v47
	s_nop 0
	v_cndmask_b32_e32 v7, v7, v8, vcc
	v_rsq_f32_e32 v7, v7
	v_or_b32_e32 v8, 24, v32
	v_ashrrev_i32_e32 v9, 31, v8
	v_lshlrev_b64 v[8:9], 11, v[8:9]
	v_mul_f32_e32 v10, 0x45800000, v7
	v_cndmask_b32_e32 v7, v7, v10, vcc
	v_mul_f32_e32 v4, v4, v7
	v_mul_f32_e32 v5, v5, v7
	v_mul_f32_e32 v4, v71, v4
	v_mul_f32_e32 v5, v70, v5
	v_cvt_pk_fp8_f32 v26, v4, v5
	v_mul_f32_e32 v1, v1, v7
	v_mul_f32_e32 v0, v0, v7
	v_mul_f32_e32 v1, v69, v1
	v_mul_f32_e32 v0, v68, v0
	v_cvt_pk_fp8_f32 v26, v1, v0 op_sel:[0,0,1]
	v_mul_f32_e32 v0, 0x4b800000, v6
	v_cmp_gt_f32_e32 vcc, s33, v6
	v_mov_b32_e32 v4, v14
	v_mov_b32_e32 v5, v62
	v_cndmask_b32_e32 v1, v6, v0, vcc
	v_rcp_f32_e32 v0, v2
	v_rcp_f32_e32 v2, v3
	v_mov_b32_e32 v62, v15
	v_mov_b32_e32 v10, v46
	v_pk_mul_f32 v[4:5], v[4:5], v[0:1] op_sel_hi:[1,0]
	v_pk_mul_f32 v[14:15], v[62:63], v[2:3] op_sel_hi:[1,0]
	v_rsq_f32_e32 v27, v1
	v_pk_mul_f32 v[6:7], v[4:5], v[4:5]
	v_pk_mul_f32 v[0:1], v[10:11], v[0:1] op_sel_hi:[1,0]
	v_pk_mul_f32 v[18:19], v[14:15], v[14:15]
	v_pk_mul_f32 v[2:3], v[30:31], v[2:3] op_sel_hi:[1,0]
	v_pk_mul_f32 v[10:11], v[0:1], v[0:1]
	v_pk_mul_f32 v[20:21], v[2:3], v[2:3]
	v_mov_b32_e32 v24, v18
	v_mov_b32_e32 v25, v6
	v_mov_b32_e32 v6, v19
	v_pk_add_f32 v[6:7], v[24:25], v[6:7]
	v_mov_b32_e32 v18, v21
	v_mov_b32_e32 v19, v11
	v_pk_add_f32 v[6:7], v[18:19], v[6:7]
	v_mov_b32_e32 v21, v10
	v_pk_add_f32 v[6:7], v[20:21], v[6:7]
	ds_bpermute_b32 v11, v72, v7
	ds_bpermute_b32 v10, v72, v6
	v_lshl_add_u64 v[8:9], v[16:17], 0, v[8:9]
	global_store_dword v[8:9], v26, off nt
	v_mul_f32_e32 v18, 0x45800000, v27
	v_mov_b32_e32 v19, 0
	s_waitcnt lgkmcnt(0)
	v_pk_add_f32 v[6:7], v[6:7], v[10:11]
	ds_bpermute_b32 v9, v73, v7
	ds_bpermute_b32 v8, v73, v6
	v_cndmask_b32_e32 v10, v27, v18, vcc
	v_mul_f32_e32 v11, v22, v10
	v_mul_f32_e32 v18, v23, v10
	v_mul_f32_e32 v11, v71, v11
	s_waitcnt lgkmcnt(0)
	v_pk_add_f32 v[6:7], v[6:7], v[8:9]
	ds_bpermute_b32 v9, v74, v7
	ds_bpermute_b32 v8, v74, v6
	v_mul_f32_e32 v18, v70, v18
	v_cvt_pk_fp8_f32 v19, v11, v18
	v_mul_f32_e32 v13, v13, v10
	v_mul_f32_e32 v10, v12, v10
	s_waitcnt lgkmcnt(0)
	v_pk_add_f32 v[6:7], v[6:7], v[8:9]
	ds_bpermute_b32 v9, v75, v7
	ds_bpermute_b32 v8, v75, v6
	v_mul_f32_e32 v11, v69, v13
	v_mul_f32_e32 v10, v68, v10
	v_cvt_pk_fp8_f32 v19, v11, v10 op_sel:[0,0,1]
	v_or_b32_e32 v10, 25, v32
	s_waitcnt lgkmcnt(0)
	v_pk_add_f32 v[6:7], v[6:7], v[8:9]
	ds_bpermute_b32 v9, v76, v7
	ds_bpermute_b32 v8, v76, v6
	v_ashrrev_i32_e32 v11, 31, v10
	v_lshlrev_b64 v[10:11], 11, v[10:11]
	v_lshl_add_u64 v[10:11], v[16:17], 0, v[10:11]
	global_store_dword v[10:11], v19, off nt
	s_waitcnt lgkmcnt(0)
	v_pk_add_f32 v[6:7], v[6:7], v[8:9]
	s_nop 0
	v_pk_fma_f32 v[6:7], v[6:7], s[18:19], v[48:49] op_sel_hi:[1,0,0]
	s_nop 0
	v_mul_f32_e32 v8, 0x4b800000, v7
	v_cmp_gt_f32_e32 vcc, s33, v7
	s_nop 1
	v_cndmask_b32_e32 v7, v7, v8, vcc
	v_rsq_f32_e32 v7, v7
	v_or_b32_e32 v8, 26, v32
	v_ashrrev_i32_e32 v9, 31, v8
	v_mul_f32_e32 v10, 0x45800000, v7
	v_cndmask_b32_e32 v7, v7, v10, vcc
	v_mul_f32_e32 v4, v4, v7
	v_mul_f32_e32 v5, v5, v7
	v_mul_f32_e32 v4, v71, v4
	v_mul_f32_e32 v5, v70, v5
	v_mov_b32_e32 v10, 0
	v_cvt_pk_fp8_f32 v10, v4, v5
	v_mul_f32_e32 v1, v1, v7
	v_mul_f32_e32 v0, v0, v7
	v_mul_f32_e32 v1, v69, v1
	v_mul_f32_e32 v0, v68, v0
	v_cvt_pk_fp8_f32 v10, v1, v0 op_sel:[0,0,1]
	v_mul_f32_e32 v0, 0x4b800000, v6
	v_cmp_gt_f32_e32 vcc, s33, v6
	v_mov_b32_e32 v5, 0
	s_nop 0
	v_cndmask_b32_e32 v0, v6, v0, vcc
	v_rsq_f32_e32 v4, v0
	v_lshlrev_b64 v[0:1], 11, v[8:9]
	v_lshl_add_u64 v[0:1], v[16:17], 0, v[0:1]
	global_store_dword v[0:1], v10, off nt
	v_mul_f32_e32 v0, 0x45800000, v4
	v_cndmask_b32_e32 v0, v4, v0, vcc
	v_mul_f32_e32 v1, v14, v0
	v_mul_f32_e32 v4, v15, v0
	v_mul_f32_e32 v1, v71, v1
	v_mul_f32_e32 v4, v70, v4
	v_cvt_pk_fp8_f32 v5, v1, v4
	v_mul_f32_e32 v3, v3, v0
	v_mul_f32_e32 v0, v2, v0
	v_mul_f32_e32 v1, v69, v3
	v_mul_f32_e32 v0, v68, v0
	v_cvt_pk_fp8_f32 v5, v1, v0 op_sel:[0,0,1]
	v_or_b32_e32 v0, 27, v32
	v_ashrrev_i32_e32 v1, 31, v0
	v_lshlrev_b64 v[0:1], 11, v[0:1]
	v_lshl_add_u64 v[0:1], v[16:17], 0, v[0:1]
	global_store_dword v[0:1], v5, off nt
	s_barrier

.LBB0_932:
	s_or_b64 exec, exec, s[4:5]
	s_lshl_b32 s2, s69, 7
	s_ashr_i32 s3, s2, 31
	s_lshl_b64 s[4:5], s[2:3], 2
	s_add_u32 s4, s24, s4
	s_addc_u32 s5, s25, s5
	s_waitcnt lgkmcnt(0)
	v_lshl_add_u32 v77, v171, 4, s35
	v_ashrrev_i32_e32 v147, 31, v146
	v_lshl_add_u64 v[64:65], v[146:147], 2, s[4:5]
	global_load_dword v71, v[64:65], off offset:3072
	global_load_dword v70, v[64:65], off offset:3200
	global_load_dword v69, v[64:65], off offset:3328
	global_load_dword v68, v[64:65], off offset:3456
	ds_read_b128 v[78:81], v77
	v_and_b32_e32 v65, 64, v254
	v_xor_b32_e32 v64, 1, v254
	v_add_u32_e32 v76, 64, v65
	v_cmp_lt_i32_e32 vcc, v64, v76
	v_mov_b32_e32 v82, v0
	v_mov_b32_e32 v83, v48
	v_cndmask_b32_e32 v72, v254, v64, vcc
	ds_read_b128 v[64:67], v77 offset:32
	s_waitcnt lgkmcnt(1)
	v_rcp_f32_e32 v74, v78
	v_rcp_f32_e32 v0, v79
	v_mov_b32_e32 v86, v32
	v_mov_b32_e32 v87, v16
	v_mov_b32_e32 v48, v1
	v_pk_mul_f32 v[82:83], v[82:83], v[74:75] op_sel_hi:[1,0]
	v_pk_mul_f32 v[78:79], v[86:87], v[74:75] op_sel_hi:[1,0]
	v_pk_mul_f32 v[86:87], v[48:49], v[0:1] op_sel_hi:[1,0]
	v_mov_b32_e32 v16, v33
	v_pk_mul_f32 v[84:85], v[82:83], v[82:83]
	v_pk_mul_f32 v[48:49], v[86:87], v[86:87]
	v_pk_mul_f32 v[0:1], v[16:17], v[0:1] op_sel_hi:[1,0]
	v_pk_mul_f32 v[74:75], v[78:79], v[78:79]
	v_pk_mul_f32 v[16:17], v[0:1], v[0:1]
	v_mov_b32_e32 v32, v48
	v_mov_b32_e32 v33, v84
	v_mov_b32_e32 v84, v49
	v_pk_add_f32 v[32:33], v[32:33], v[84:85]
	v_mov_b32_e32 v48, v17
	v_mov_b32_e32 v49, v75
	v_pk_add_f32 v[32:33], v[48:49], v[32:33]
	v_mov_b32_e32 v17, v74
	v_lshlrev_b32_e32 v72, 2, v72
	v_pk_add_f32 v[16:17], v[16:17], v[32:33]
	ds_bpermute_b32 v33, v72, v17
	ds_bpermute_b32 v32, v72, v16
	v_xor_b32_e32 v48, 2, v254
	v_cmp_lt_i32_e32 vcc, v48, v76
	s_lshl_b64 s[24:25], s[26:27], 11
	s_add_u32 s22, s22, s24
	v_cndmask_b32_e32 v48, v254, v48, vcc
	v_lshlrev_b32_e32 v73, 2, v48
	s_waitcnt lgkmcnt(0)
	v_pk_add_f32 v[16:17], v[16:17], v[32:33]
	ds_bpermute_b32 v33, v73, v17
	ds_bpermute_b32 v32, v73, v16
	v_xor_b32_e32 v48, 4, v254
	v_cmp_lt_i32_e32 vcc, v48, v76
	s_addc_u32 s23, s23, s25
	s_add_u32 s2, s22, s2
	v_cndmask_b32_e32 v48, v254, v48, vcc
	v_lshlrev_b32_e32 v74, 2, v48
	s_waitcnt lgkmcnt(0)
	v_pk_add_f32 v[16:17], v[16:17], v[32:33]
	ds_bpermute_b32 v33, v74, v17
	ds_bpermute_b32 v32, v74, v16
	v_xor_b32_e32 v48, 8, v254
	v_cmp_lt_i32_e32 vcc, v48, v76
	s_addc_u32 s3, s23, s3
	v_mov_b32_e32 v90, 0
	v_cndmask_b32_e32 v48, v254, v48, vcc
	v_lshlrev_b32_e32 v75, 2, v48
	s_waitcnt lgkmcnt(0)
	v_pk_add_f32 v[16:17], v[16:17], v[32:33]
	ds_bpermute_b32 v33, v75, v17
	ds_bpermute_b32 v32, v75, v16
	v_xor_b32_e32 v48, 16, v254
	v_cmp_lt_i32_e32 vcc, v48, v76
	s_mov_b32 s26, 0
	s_waitcnt lgkmcnt(0)
	v_pk_add_f32 v[16:17], v[16:17], v[32:33]
	v_cndmask_b32_e32 v48, v254, v48, vcc
	v_lshlrev_b32_e32 v76, 2, v48
	ds_bpermute_b32 v33, v76, v17
	ds_bpermute_b32 v32, v76, v16
	v_lshlrev_b32_e32 v48, 2, v146
	v_ashrrev_i32_e32 v49, 31, v48
	v_lshl_add_u64 v[84:85], s[2:3], 0, v[48:49]
	v_mov_b64_e32 v[48:49], s[20:21]
	s_waitcnt lgkmcnt(0)
	v_pk_add_f32 v[16:17], v[16:17], v[32:33]
	v_lshl_or_b32 v32, v171, 2, s34
	v_pk_fma_f32 v[88:89], v[16:17], s[18:19], v[48:49] op_sel_hi:[1,0,0]
	v_ashrrev_i32_e32 v33, 31, v32
	v_mul_f32_e32 v16, 0x4b800000, v89
	v_cmp_gt_f32_e32 vcc, s67, v89
	s_nop 1
	v_cndmask_b32_e32 v16, v89, v16, vcc
	v_rsq_f32_e32 v89, v16
	v_lshl_add_u64 v[16:17], v[84:85], 0, s[14:15]
	v_mul_f32_e32 v84, 0x45800000, v89
	v_cndmask_b32_e32 v84, v89, v84, vcc
	v_mul_f32_e32 v82, v82, v84
	v_mul_f32_e32 v83, v83, v84
	s_waitcnt vmcnt(3)
	v_mul_f32_e32 v82, v71, v82
	s_waitcnt vmcnt(2)
	v_mul_f32_e32 v83, v70, v83
	v_cvt_pk_fp8_f32 v90, v82, v83
	v_mul_f32_e32 v79, v79, v84
	v_mul_f32_e32 v78, v78, v84
	s_waitcnt vmcnt(1)
	v_mul_f32_e32 v79, v69, v79
	s_waitcnt vmcnt(0)
	v_mul_f32_e32 v78, v68, v78
	v_cvt_pk_fp8_f32 v90, v79, v78 op_sel:[0,0,1]
	v_mul_f32_e32 v78, 0x4b800000, v88
	v_cmp_gt_f32_e32 vcc, s67, v88
	v_mov_b32_e32 v82, v2
	v_rcp_f32_e32 v2, v81
	v_cndmask_b32_e32 v79, v88, v78, vcc
	v_rcp_f32_e32 v78, v80
	v_mov_b32_e32 v83, v50
	v_mov_b32_e32 v50, v3
	v_mov_b32_e32 v88, v34
	v_pk_mul_f32 v[82:83], v[82:83], v[78:79] op_sel_hi:[1,0]
	v_mov_b32_e32 v89, v18
	v_pk_mul_f32 v[50:51], v[50:51], v[2:3] op_sel_hi:[1,0]
	v_mov_b32_e32 v18, v35
	v_rsq_f32_e32 v91, v79
	v_pk_mul_f32 v[84:85], v[82:83], v[82:83]
	v_pk_mul_f32 v[78:79], v[88:89], v[78:79] op_sel_hi:[1,0]
	v_pk_mul_f32 v[88:89], v[50:51], v[50:51]
	v_pk_mul_f32 v[2:3], v[18:19], v[2:3] op_sel_hi:[1,0]
	v_pk_mul_f32 v[80:81], v[78:79], v[78:79]
	v_pk_mul_f32 v[18:19], v[2:3], v[2:3]
	v_mov_b32_e32 v34, v88
	v_mov_b32_e32 v35, v84
	v_mov_b32_e32 v84, v89
	v_pk_add_f32 v[34:35], v[34:35], v[84:85]
	v_mov_b32_e32 v84, v19
	v_mov_b32_e32 v85, v81
	v_pk_add_f32 v[34:35], v[84:85], v[34:35]
	v_mov_b32_e32 v19, v80
	v_pk_add_f32 v[18:19], v[18:19], v[34:35]
	ds_bpermute_b32 v35, v72, v19
	ds_bpermute_b32 v34, v72, v18
	v_lshlrev_b64 v[80:81], 11, v[32:33]
	v_mul_f32_e32 v33, 0x45800000, v91
	v_lshl_add_u64 v[80:81], v[16:17], 0, v[80:81]
	v_cndmask_b32_e32 v33, v91, v33, vcc
	s_waitcnt lgkmcnt(0)
	v_pk_add_f32 v[18:19], v[18:19], v[34:35]
	ds_bpermute_b32 v35, v73, v19
	ds_bpermute_b32 v34, v73, v18
	global_store_dword v[80:81], v90, off nt
	v_mul_f32_e32 v80, v86, v33
	v_mul_f32_e32 v81, v87, v33
	v_mul_f32_e32 v80, v71, v80
	s_waitcnt lgkmcnt(0)
	v_pk_add_f32 v[18:19], v[18:19], v[34:35]
	ds_bpermute_b32 v35, v74, v19
	ds_bpermute_b32 v34, v74, v18
	v_mul_f32_e32 v81, v70, v81
	v_mov_b32_e32 v84, 0
	v_cvt_pk_fp8_f32 v84, v80, v81
	v_mul_f32_e32 v1, v1, v33
	s_waitcnt lgkmcnt(0)
	v_pk_add_f32 v[18:19], v[18:19], v[34:35]
	ds_bpermute_b32 v35, v75, v19
	ds_bpermute_b32 v34, v75, v18
	v_mul_f32_e32 v0, v0, v33
	v_mul_f32_e32 v1, v69, v1
	v_mul_f32_e32 v0, v68, v0
	v_cvt_pk_fp8_f32 v84, v1, v0 op_sel:[0,0,1]
	s_waitcnt lgkmcnt(0)
	v_pk_add_f32 v[0:1], v[18:19], v[34:35]
	ds_bpermute_b32 v19, v76, v1
	ds_bpermute_b32 v18, v76, v0
	v_or_b32_e32 v34, 1, v32
	v_ashrrev_i32_e32 v35, 31, v34
	v_lshlrev_b64 v[34:35], 11, v[34:35]
	v_lshl_add_u64 v[34:35], v[16:17], 0, v[34:35]
	s_waitcnt lgkmcnt(0)
	v_pk_add_f32 v[0:1], v[0:1], v[18:19]
	global_store_dword v[34:35], v84, off nt
	v_pk_fma_f32 v[0:1], v[0:1], s[18:19], v[48:49] op_sel_hi:[1,0,0]
	v_mov_b32_e32 v80, v36
	v_mul_f32_e32 v18, 0x4b800000, v1
	v_cmp_gt_f32_e32 vcc, s67, v1
	v_mov_b32_e32 v81, v20
	v_mov_b32_e32 v20, v37
	v_cndmask_b32_e32 v1, v1, v18, vcc
	v_rsq_f32_e32 v1, v1
	v_or_b32_e32 v18, 2, v32
	v_ashrrev_i32_e32 v19, 31, v18
	v_lshlrev_b64 v[18:19], 11, v[18:19]
	v_mul_f32_e32 v33, 0x45800000, v1
	v_cndmask_b32_e32 v1, v1, v33, vcc
	v_mul_f32_e32 v33, v82, v1
	v_mul_f32_e32 v34, v83, v1
	v_mul_f32_e32 v33, v71, v33
	v_mul_f32_e32 v34, v70, v34
	v_mov_b32_e32 v82, 0
	v_cvt_pk_fp8_f32 v82, v33, v34
	v_mul_f32_e32 v35, v79, v1
	v_mul_f32_e32 v1, v78, v1
	v_mul_f32_e32 v33, v69, v35
	v_mul_f32_e32 v1, v68, v1
	v_cvt_pk_fp8_f32 v82, v33, v1 op_sel:[0,0,1]
	v_mul_f32_e32 v1, 0x4b800000, v0
	v_cmp_gt_f32_e32 vcc, s67, v0
	v_mov_b32_e32 v34, v4
	v_rcp_f32_e32 v4, v65
	v_cndmask_b32_e32 v1, v0, v1, vcc
	v_rcp_f32_e32 v0, v64
	v_mov_b32_e32 v35, v52
	v_mov_b32_e32 v52, v5
	v_pk_mul_f32 v[52:53], v[52:53], v[4:5] op_sel_hi:[1,0]
	v_pk_mul_f32 v[34:35], v[34:35], v[0:1] op_sel_hi:[1,0]
	v_rsq_f32_e32 v33, v1
	v_pk_mul_f32 v[78:79], v[34:35], v[34:35]
	v_pk_mul_f32 v[0:1], v[80:81], v[0:1] op_sel_hi:[1,0]
	v_pk_mul_f32 v[80:81], v[52:53], v[52:53]
	v_pk_mul_f32 v[4:5], v[20:21], v[4:5] op_sel_hi:[1,0]
	v_pk_mul_f32 v[64:65], v[0:1], v[0:1]
	v_pk_mul_f32 v[20:21], v[4:5], v[4:5]
	v_mov_b32_e32 v36, v80
	v_mov_b32_e32 v37, v78
	v_mov_b32_e32 v78, v81
	v_pk_add_f32 v[36:37], v[36:37], v[78:79]
	v_mov_b32_e32 v78, v21
	v_mov_b32_e32 v79, v65
	v_pk_add_f32 v[36:37], v[78:79], v[36:37]
	v_mov_b32_e32 v21, v64
	v_pk_add_f32 v[20:21], v[20:21], v[36:37]
	ds_bpermute_b32 v37, v72, v21
	ds_bpermute_b32 v36, v72, v20
	v_lshl_add_u64 v[18:19], v[16:17], 0, v[18:19]
	global_store_dword v[18:19], v82, off nt
	v_mul_f32_e32 v64, 0x45800000, v33
	v_cndmask_b32_e32 v33, v33, v64, vcc
	s_waitcnt lgkmcnt(0)
	v_pk_add_f32 v[18:19], v[20:21], v[36:37]
	ds_bpermute_b32 v21, v73, v19
	ds_bpermute_b32 v20, v73, v18
	v_mul_f32_e32 v36, v50, v33
	v_mul_f32_e32 v37, v51, v33
	v_mul_f32_e32 v36, v71, v36
	v_mul_f32_e32 v37, v70, v37
	s_waitcnt lgkmcnt(0)
	v_pk_add_f32 v[18:19], v[18:19], v[20:21]
	ds_bpermute_b32 v21, v74, v19
	ds_bpermute_b32 v20, v74, v18
	v_mov_b32_e32 v50, 0
	v_cvt_pk_fp8_f32 v50, v36, v37
	v_mul_f32_e32 v3, v3, v33
	v_mul_f32_e32 v2, v2, v33
	s_waitcnt lgkmcnt(0)
	v_pk_add_f32 v[18:19], v[18:19], v[20:21]
	ds_bpermute_b32 v21, v75, v19
	ds_bpermute_b32 v20, v75, v18
	v_mul_f32_e32 v3, v69, v3
	v_mul_f32_e32 v2, v68, v2
	v_cvt_pk_fp8_f32 v50, v3, v2 op_sel:[0,0,1]
	v_mov_b32_e32 v33, 0
	s_waitcnt lgkmcnt(0)
	v_pk_add_f32 v[2:3], v[18:19], v[20:21]
	ds_bpermute_b32 v19, v76, v3
	ds_bpermute_b32 v18, v76, v2
	v_or_b32_e32 v20, 3, v32
	v_ashrrev_i32_e32 v21, 31, v20
	v_lshlrev_b64 v[20:21], 11, v[20:21]
	v_lshl_add_u64 v[20:21], v[16:17], 0, v[20:21]
	s_waitcnt lgkmcnt(0)
	v_pk_add_f32 v[2:3], v[2:3], v[18:19]
	global_store_dword v[20:21], v50, off nt
	v_pk_fma_f32 v[2:3], v[2:3], s[18:19], v[48:49] op_sel_hi:[1,0,0]
	v_or_b32_e32 v36, 8, v32
	v_mul_f32_e32 v18, 0x4b800000, v3
	v_cmp_gt_f32_e32 vcc, s67, v3
	v_ashrrev_i32_e32 v37, 31, v36
	s_nop 0
	v_cndmask_b32_e32 v3, v3, v18, vcc
	v_rsq_f32_e32 v3, v3
	s_nop 0
	v_mul_f32_e32 v18, 0x45800000, v3
	v_cndmask_b32_e32 v3, v3, v18, vcc
	v_mul_f32_e32 v18, v34, v3
	v_mul_f32_e32 v19, v35, v3
	v_mul_f32_e32 v18, v71, v18
	v_mul_f32_e32 v19, v70, v19
	v_cvt_pk_fp8_f32 v33, v18, v19
	v_mul_f32_e32 v1, v1, v3
	v_mul_f32_e32 v0, v0, v3
	v_mul_f32_e32 v1, v69, v1
	v_mul_f32_e32 v0, v68, v0
	v_cvt_pk_fp8_f32 v33, v1, v0 op_sel:[0,0,1]
	v_mul_f32_e32 v0, 0x4b800000, v2
	v_cmp_gt_f32_e32 vcc, s67, v2
	v_mov_b32_e32 v3, v54
	v_mov_b32_e32 v54, v7
	v_cndmask_b32_e32 v1, v2, v0, vcc
	v_rcp_f32_e32 v0, v66
	v_mov_b32_e32 v2, v6
	v_rcp_f32_e32 v6, v67
	v_mov_b32_e32 v18, v38
	v_pk_mul_f32 v[2:3], v[2:3], v[0:1] op_sel_hi:[1,0]
	v_mov_b32_e32 v19, v22
	v_pk_mul_f32 v[20:21], v[54:55], v[6:7] op_sel_hi:[1,0]
	v_mov_b32_e32 v22, v39
	v_rsq_f32_e32 v64, v1
	v_pk_mul_f32 v[34:35], v[2:3], v[2:3]
	v_pk_mul_f32 v[0:1], v[18:19], v[0:1] op_sel_hi:[1,0]
	v_pk_mul_f32 v[54:55], v[20:21], v[20:21]
	v_pk_mul_f32 v[18:19], v[22:23], v[6:7] op_sel_hi:[1,0]
	v_pk_mul_f32 v[50:51], v[0:1], v[0:1]
	v_pk_mul_f32 v[6:7], v[18:19], v[18:19]
	v_mov_b32_e32 v22, v54
	v_mov_b32_e32 v23, v34
	v_mov_b32_e32 v34, v55
	v_pk_add_f32 v[22:23], v[22:23], v[34:35]
	v_mov_b32_e32 v34, v7
	v_mov_b32_e32 v35, v51
	v_pk_add_f32 v[22:23], v[34:35], v[22:23]
	v_mov_b32_e32 v7, v50
	v_pk_add_f32 v[6:7], v[6:7], v[22:23]
	ds_bpermute_b32 v23, v72, v7
	ds_bpermute_b32 v22, v72, v6
	v_lshlrev_b64 v[34:35], 11, v[36:37]
	v_lshl_add_u64 v[34:35], v[16:17], 0, v[34:35]
	global_store_dword v[34:35], v33, off nt
	v_mul_f32_e32 v33, 0x45800000, v64
	s_waitcnt lgkmcnt(0)
	v_pk_add_f32 v[6:7], v[6:7], v[22:23]
	ds_bpermute_b32 v23, v73, v7
	ds_bpermute_b32 v22, v73, v6
	v_cndmask_b32_e32 v33, v64, v33, vcc
	v_mul_f32_e32 v34, v52, v33
	v_mul_f32_e32 v35, v53, v33
	v_mul_f32_e32 v34, v71, v34
	s_waitcnt lgkmcnt(0)
	v_pk_add_f32 v[6:7], v[6:7], v[22:23]
	ds_bpermute_b32 v23, v74, v7
	ds_bpermute_b32 v22, v74, v6
	v_mul_f32_e32 v35, v70, v35
	v_mov_b32_e32 v36, 0
	v_cvt_pk_fp8_f32 v36, v34, v35
	v_mul_f32_e32 v5, v5, v33
	s_waitcnt lgkmcnt(0)
	v_pk_add_f32 v[6:7], v[6:7], v[22:23]
	ds_bpermute_b32 v23, v75, v7
	ds_bpermute_b32 v22, v75, v6
	v_mul_f32_e32 v4, v4, v33
	v_mul_f32_e32 v5, v69, v5
	v_mul_f32_e32 v4, v68, v4
	v_cvt_pk_fp8_f32 v36, v5, v4 op_sel:[0,0,1]
	s_waitcnt lgkmcnt(0)
	v_pk_add_f32 v[4:5], v[6:7], v[22:23]
	ds_bpermute_b32 v7, v76, v5
	ds_bpermute_b32 v6, v76, v4
	v_mov_b32_e32 v33, 0
	v_or_b32_e32 v22, 9, v32
	v_ashrrev_i32_e32 v23, 31, v22
	v_lshlrev_b64 v[22:23], 11, v[22:23]
	s_waitcnt lgkmcnt(0)
	v_pk_add_f32 v[4:5], v[4:5], v[6:7]
	v_lshl_add_u64 v[22:23], v[16:17], 0, v[22:23]
	v_pk_fma_f32 v[34:35], v[4:5], s[18:19], v[48:49] op_sel_hi:[1,0,0]
	v_mov_b32_e32 v38, v40
	v_mul_f32_e32 v4, 0x4b800000, v35
	v_cmp_gt_f32_e32 vcc, s67, v35
	v_mov_b32_e32 v39, v24
	v_mov_b32_e32 v24, v41
	v_cndmask_b32_e32 v4, v35, v4, vcc
	v_rsq_f32_e32 v4, v4
	v_mov_b32_e32 v35, v56
	v_mov_b32_e32 v56, v9
	global_store_dword v[22:23], v36, off nt
	v_mul_f32_e32 v5, 0x45800000, v4
	v_cndmask_b32_e32 v4, v4, v5, vcc
	v_mul_f32_e32 v2, v2, v4
	v_mul_f32_e32 v3, v3, v4
	v_mul_f32_e32 v2, v71, v2
	v_mul_f32_e32 v3, v70, v3
	v_cvt_pk_fp8_f32 v33, v2, v3
	v_mul_f32_e32 v1, v1, v4
	v_mul_f32_e32 v0, v0, v4
	ds_read_b128 v[4:7], v77 offset:64
	v_mul_f32_e32 v1, v69, v1
	v_mul_f32_e32 v0, v68, v0
	v_cvt_pk_fp8_f32 v33, v1, v0 op_sel:[0,0,1]
	v_mul_f32_e32 v0, 0x4b800000, v34
	v_cmp_gt_f32_e32 vcc, s67, v34
	v_or_b32_e32 v22, 10, v32
	v_ashrrev_i32_e32 v23, 31, v22
	v_cndmask_b32_e32 v34, v34, v0, vcc
	ds_read_b128 v[0:3], v77 offset:96
	s_waitcnt lgkmcnt(1)
	v_rcp_f32_e32 v4, v4
	v_rsq_f32_e32 v54, v34
	v_mov_b32_e32 v34, v8
	v_rcp_f32_e32 v8, v5
	v_pk_mul_f32 v[34:35], v[34:35], v[4:5] op_sel_hi:[1,0]
	v_pk_mul_f32 v[4:5], v[38:39], v[4:5] op_sel_hi:[1,0]
	v_pk_mul_f32 v[36:37], v[34:35], v[34:35]
	v_pk_mul_f32 v[50:51], v[56:57], v[8:9] op_sel_hi:[1,0]
	v_pk_mul_f32 v[8:9], v[24:25], v[8:9] op_sel_hi:[1,0]
	v_pk_mul_f32 v[52:53], v[50:51], v[50:51]
	v_pk_mul_f32 v[38:39], v[4:5], v[4:5]
	v_pk_mul_f32 v[24:25], v[8:9], v[8:9]
	v_mov_b32_e32 v40, v52
	v_mov_b32_e32 v41, v36
	v_mov_b32_e32 v36, v53
	v_pk_add_f32 v[36:37], v[40:41], v[36:37]
	v_mov_b32_e32 v40, v25
	v_mov_b32_e32 v41, v39
	v_pk_add_f32 v[36:37], v[40:41], v[36:37]
	v_mov_b32_e32 v25, v38
	v_pk_add_f32 v[24:25], v[24:25], v[36:37]
	ds_bpermute_b32 v37, v72, v25
	ds_bpermute_b32 v36, v72, v24
	v_lshlrev_b64 v[22:23], 11, v[22:23]
	v_lshl_add_u64 v[22:23], v[16:17], 0, v[22:23]
	global_store_dword v[22:23], v33, off nt
	v_mul_f32_e32 v33, 0x45800000, v54
	s_waitcnt lgkmcnt(0)
	v_pk_add_f32 v[22:23], v[24:25], v[36:37]
	ds_bpermute_b32 v25, v73, v23
	ds_bpermute_b32 v24, v73, v22
	v_cndmask_b32_e32 v33, v54, v33, vcc
	v_mul_f32_e32 v20, v20, v33
	v_mul_f32_e32 v36, v71, v20
	v_mul_f32_e32 v37, v21, v33
	s_waitcnt lgkmcnt(0)
	v_pk_add_f32 v[20:21], v[22:23], v[24:25]
	ds_bpermute_b32 v23, v74, v21
	ds_bpermute_b32 v22, v74, v20
	v_mul_f32_e32 v24, v70, v37
	v_mov_b32_e32 v25, 0
	v_cvt_pk_fp8_f32 v25, v36, v24
	v_mul_f32_e32 v19, v19, v33
	s_waitcnt lgkmcnt(0)
	v_pk_add_f32 v[20:21], v[20:21], v[22:23]
	ds_bpermute_b32 v23, v75, v21
	ds_bpermute_b32 v22, v75, v20
	v_mul_f32_e32 v18, v18, v33
	v_mul_f32_e32 v19, v69, v19
	v_mul_f32_e32 v18, v68, v18
	v_cvt_pk_fp8_f32 v25, v19, v18 op_sel:[0,0,1]
	s_waitcnt lgkmcnt(0)
	v_pk_add_f32 v[18:19], v[20:21], v[22:23]
	ds_bpermute_b32 v21, v76, v19
	ds_bpermute_b32 v20, v76, v18
	v_or_b32_e32 v22, 11, v32
	v_ashrrev_i32_e32 v23, 31, v22
	v_lshlrev_b64 v[22:23], 11, v[22:23]
	v_lshl_add_u64 v[22:23], v[16:17], 0, v[22:23]
	s_waitcnt lgkmcnt(0)
	v_pk_add_f32 v[18:19], v[18:19], v[20:21]
	global_store_dword v[22:23], v25, off nt
	v_pk_fma_f32 v[18:19], v[18:19], s[18:19], v[48:49] op_sel_hi:[1,0,0]
	v_mov_b32_e32 v33, 0
	v_mul_f32_e32 v20, 0x4b800000, v19
	v_cmp_gt_f32_e32 vcc, s67, v19
	v_mov_b32_e32 v24, v42
	v_mov_b32_e32 v25, v26
	v_cndmask_b32_e32 v19, v19, v20, vcc
	v_rsq_f32_e32 v19, v19
	v_mov_b32_e32 v26, v43
	v_or_b32_e32 v20, 16, v32
	v_ashrrev_i32_e32 v21, 31, v20
	v_mul_f32_e32 v22, 0x45800000, v19
	v_cndmask_b32_e32 v19, v19, v22, vcc
	v_mul_f32_e32 v22, v34, v19
	v_mul_f32_e32 v23, v35, v19
	v_mul_f32_e32 v22, v71, v22
	v_mul_f32_e32 v23, v70, v23
	v_cvt_pk_fp8_f32 v33, v22, v23
	v_mul_f32_e32 v5, v5, v19
	v_mul_f32_e32 v4, v4, v19
	v_mul_f32_e32 v5, v69, v5
	v_mul_f32_e32 v4, v68, v4
	v_cvt_pk_fp8_f32 v33, v5, v4 op_sel:[0,0,1]
	v_mul_f32_e32 v4, 0x4b800000, v18
	v_cmp_gt_f32_e32 vcc, s67, v18
	v_mov_b32_e32 v19, v58
	v_mov_b32_e32 v58, v11
	v_cndmask_b32_e32 v5, v18, v4, vcc
	v_rcp_f32_e32 v4, v6
	v_rcp_f32_e32 v6, v7
	v_mov_b32_e32 v18, v10
	v_rsq_f32_e32 v38, v5
	v_pk_mul_f32 v[18:19], v[18:19], v[4:5] op_sel_hi:[1,0]
	v_pk_mul_f32 v[10:11], v[58:59], v[6:7] op_sel_hi:[1,0]
	v_pk_mul_f32 v[22:23], v[18:19], v[18:19]
	v_pk_mul_f32 v[4:5], v[24:25], v[4:5] op_sel_hi:[1,0]
	v_pk_mul_f32 v[34:35], v[10:11], v[10:11]
	v_pk_mul_f32 v[6:7], v[26:27], v[6:7] op_sel_hi:[1,0]
	v_pk_mul_f32 v[24:25], v[4:5], v[4:5]
	v_pk_mul_f32 v[26:27], v[6:7], v[6:7]
	v_mov_b32_e32 v36, v34
	v_mov_b32_e32 v37, v22
	v_mov_b32_e32 v22, v35
	v_pk_add_f32 v[22:23], v[36:37], v[22:23]
	v_mov_b32_e32 v34, v27
	v_mov_b32_e32 v35, v25
	v_pk_add_f32 v[22:23], v[34:35], v[22:23]
	v_mov_b32_e32 v27, v24
	v_pk_add_f32 v[22:23], v[26:27], v[22:23]
	ds_bpermute_b32 v25, v72, v23
	ds_bpermute_b32 v24, v72, v22
	v_lshlrev_b64 v[20:21], 11, v[20:21]
	v_lshl_add_u64 v[20:21], v[16:17], 0, v[20:21]
	global_store_dword v[20:21], v33, off nt
	v_mul_f32_e32 v26, 0x45800000, v38
	s_waitcnt lgkmcnt(0)
	v_pk_add_f32 v[20:21], v[22:23], v[24:25]
	ds_bpermute_b32 v23, v73, v21
	ds_bpermute_b32 v22, v73, v20
	v_cndmask_b32_e32 v24, v38, v26, vcc
	v_mul_f32_e32 v25, v50, v24
	v_mul_f32_e32 v26, v51, v24
	v_mul_f32_e32 v25, v71, v25
	s_waitcnt lgkmcnt(0)
	v_pk_add_f32 v[20:21], v[20:21], v[22:23]
	ds_bpermute_b32 v23, v74, v21
	ds_bpermute_b32 v22, v74, v20
	v_mul_f32_e32 v26, v70, v26
	v_mov_b32_e32 v27, 0
	v_cvt_pk_fp8_f32 v27, v25, v26
	v_mul_f32_e32 v9, v9, v24
	s_waitcnt lgkmcnt(0)
	v_pk_add_f32 v[20:21], v[20:21], v[22:23]
	ds_bpermute_b32 v23, v75, v21
	ds_bpermute_b32 v22, v75, v20
	v_mul_f32_e32 v8, v8, v24
	v_mul_f32_e32 v9, v69, v9
	v_mul_f32_e32 v8, v68, v8
	v_cvt_pk_fp8_f32 v27, v9, v8 op_sel:[0,0,1]
	s_waitcnt lgkmcnt(0)
	v_pk_add_f32 v[8:9], v[20:21], v[22:23]
	ds_bpermute_b32 v21, v76, v9
	ds_bpermute_b32 v20, v76, v8
	v_or_b32_e32 v22, 17, v32
	v_ashrrev_i32_e32 v23, 31, v22
	v_lshlrev_b64 v[22:23], 11, v[22:23]
	v_lshl_add_u64 v[22:23], v[16:17], 0, v[22:23]
	s_waitcnt lgkmcnt(0)
	v_pk_add_f32 v[8:9], v[8:9], v[20:21]
	global_store_dword v[22:23], v27, off nt
	v_pk_fma_f32 v[8:9], v[8:9], s[18:19], v[48:49] op_sel_hi:[1,0,0]
	v_mov_b32_e32 v33, 0
	v_mul_f32_e32 v20, 0x4b800000, v9
	v_cmp_gt_f32_e32 vcc, s67, v9
	v_rcp_f32_e32 v0, v0
	s_nop 0
	v_cndmask_b32_e32 v9, v9, v20, vcc
	v_rsq_f32_e32 v9, v9
	v_or_b32_e32 v20, 18, v32
	v_ashrrev_i32_e32 v21, 31, v20
	v_lshlrev_b64 v[20:21], 11, v[20:21]
	v_mul_f32_e32 v22, 0x45800000, v9
	v_cndmask_b32_e32 v9, v9, v22, vcc
	v_mul_f32_e32 v18, v18, v9
	v_mul_f32_e32 v19, v19, v9
	v_mul_f32_e32 v18, v71, v18
	v_mul_f32_e32 v19, v70, v19
	v_cvt_pk_fp8_f32 v33, v18, v19
	v_mul_f32_e32 v5, v5, v9
	v_mul_f32_e32 v4, v4, v9
	v_mul_f32_e32 v5, v69, v5
	v_mul_f32_e32 v4, v68, v4
	v_cvt_pk_fp8_f32 v33, v5, v4 op_sel:[0,0,1]
	v_mul_f32_e32 v4, 0x4b800000, v8
	v_cmp_gt_f32_e32 vcc, s67, v8
	v_mov_b32_e32 v5, v60
	v_mov_b32_e32 v60, v13
	v_cndmask_b32_e32 v4, v8, v4, vcc
	v_rsq_f32_e32 v34, v4
	v_mov_b32_e32 v4, v12
	v_rcp_f32_e32 v12, v1
	v_pk_mul_f32 v[4:5], v[4:5], v[0:1] op_sel_hi:[1,0]
	v_mov_b32_e32 v18, v44
	v_mov_b32_e32 v19, v28
	v_pk_mul_f32 v[22:23], v[60:61], v[12:13] op_sel_hi:[1,0]
	v_mov_b32_e32 v28, v45
	v_pk_mul_f32 v[8:9], v[4:5], v[4:5]
	v_pk_mul_f32 v[0:1], v[18:19], v[0:1] op_sel_hi:[1,0]
	v_pk_mul_f32 v[24:25], v[22:23], v[22:23]
	v_pk_mul_f32 v[12:13], v[28:29], v[12:13] op_sel_hi:[1,0]
	v_pk_mul_f32 v[18:19], v[0:1], v[0:1]
	v_pk_mul_f32 v[26:27], v[12:13], v[12:13]
	v_mov_b32_e32 v28, v24
	v_mov_b32_e32 v29, v8
	v_mov_b32_e32 v8, v25
	v_pk_add_f32 v[8:9], v[28:29], v[8:9]
	v_mov_b32_e32 v24, v27
	v_mov_b32_e32 v25, v19
	v_pk_add_f32 v[8:9], v[24:25], v[8:9]
	v_mov_b32_e32 v27, v18
	v_pk_add_f32 v[8:9], v[26:27], v[8:9]
	ds_bpermute_b32 v19, v72, v9
	ds_bpermute_b32 v18, v72, v8
	v_lshl_add_u64 v[20:21], v[16:17], 0, v[20:21]
	global_store_dword v[20:21], v33, off nt
	v_mul_f32_e32 v20, 0x45800000, v34
	v_cndmask_b32_e32 v20, v34, v20, vcc
	s_waitcnt lgkmcnt(0)
	v_pk_add_f32 v[8:9], v[8:9], v[18:19]
	ds_bpermute_b32 v19, v73, v9
	ds_bpermute_b32 v18, v73, v8
	v_mul_f32_e32 v10, v10, v20
	v_mul_f32_e32 v21, v71, v10
	v_mul_f32_e32 v24, v11, v20
	v_mul_f32_e32 v7, v7, v20
	s_waitcnt lgkmcnt(0)
	v_pk_add_f32 v[8:9], v[8:9], v[18:19]
	ds_bpermute_b32 v11, v74, v9
	ds_bpermute_b32 v10, v74, v8
	v_mul_f32_e32 v18, v70, v24
	v_mov_b32_e32 v19, 0
	v_cvt_pk_fp8_f32 v19, v21, v18
	v_mul_f32_e32 v6, v6, v20
	s_waitcnt lgkmcnt(0)
	v_pk_add_f32 v[8:9], v[8:9], v[10:11]
	ds_bpermute_b32 v11, v75, v9
	ds_bpermute_b32 v10, v75, v8
	v_mul_f32_e32 v7, v69, v7
	v_mul_f32_e32 v6, v68, v6
	v_cvt_pk_fp8_f32 v19, v7, v6 op_sel:[0,0,1]
	v_mov_b32_e32 v26, 0
	s_waitcnt lgkmcnt(0)
	v_pk_add_f32 v[6:7], v[8:9], v[10:11]
	ds_bpermute_b32 v9, v76, v7
	ds_bpermute_b32 v8, v76, v6
	v_or_b32_e32 v10, 19, v32
	v_ashrrev_i32_e32 v11, 31, v10
	v_lshlrev_b64 v[10:11], 11, v[10:11]
	v_lshl_add_u64 v[10:11], v[16:17], 0, v[10:11]
	s_waitcnt lgkmcnt(0)
	v_pk_add_f32 v[6:7], v[6:7], v[8:9]
	global_store_dword v[10:11], v19, off nt
	v_pk_fma_f32 v[6:7], v[6:7], s[18:19], v[48:49] op_sel_hi:[1,0,0]
	v_mov_b32_e32 v11, v30
	v_mul_f32_e32 v8, 0x4b800000, v7
	v_cmp_gt_f32_e32 vcc, s67, v7
	v_mov_b32_e32 v30, v47
	s_nop 0
	v_cndmask_b32_e32 v7, v7, v8, vcc
	v_rsq_f32_e32 v7, v7
	v_or_b32_e32 v8, 24, v32
	v_ashrrev_i32_e32 v9, 31, v8
	v_lshlrev_b64 v[8:9], 11, v[8:9]
	v_mul_f32_e32 v10, 0x45800000, v7
	v_cndmask_b32_e32 v7, v7, v10, vcc
	v_mul_f32_e32 v4, v4, v7
	v_mul_f32_e32 v5, v5, v7
	v_mul_f32_e32 v4, v71, v4
	v_mul_f32_e32 v5, v70, v5
	v_cvt_pk_fp8_f32 v26, v4, v5
	v_mul_f32_e32 v1, v1, v7
	v_mul_f32_e32 v0, v0, v7
	v_mul_f32_e32 v1, v69, v1
	v_mul_f32_e32 v0, v68, v0
	v_cvt_pk_fp8_f32 v26, v1, v0 op_sel:[0,0,1]
	v_mul_f32_e32 v0, 0x4b800000, v6
	v_cmp_gt_f32_e32 vcc, s67, v6
	v_mov_b32_e32 v4, v14
	v_mov_b32_e32 v5, v62
	v_cndmask_b32_e32 v1, v6, v0, vcc
	v_rcp_f32_e32 v0, v2
	v_rcp_f32_e32 v2, v3
	v_mov_b32_e32 v62, v15
	v_mov_b32_e32 v10, v46
	v_pk_mul_f32 v[4:5], v[4:5], v[0:1] op_sel_hi:[1,0]
	v_pk_mul_f32 v[14:15], v[62:63], v[2:3] op_sel_hi:[1,0]
	v_rsq_f32_e32 v27, v1
	v_pk_mul_f32 v[6:7], v[4:5], v[4:5]
	v_pk_mul_f32 v[0:1], v[10:11], v[0:1] op_sel_hi:[1,0]
	v_pk_mul_f32 v[18:19], v[14:15], v[14:15]
	v_pk_mul_f32 v[2:3], v[30:31], v[2:3] op_sel_hi:[1,0]
	v_pk_mul_f32 v[10:11], v[0:1], v[0:1]
	v_pk_mul_f32 v[20:21], v[2:3], v[2:3]
	v_mov_b32_e32 v24, v18
	v_mov_b32_e32 v25, v6
	v_mov_b32_e32 v6, v19
	v_pk_add_f32 v[6:7], v[24:25], v[6:7]
	v_mov_b32_e32 v18, v21
	v_mov_b32_e32 v19, v11
	v_pk_add_f32 v[6:7], v[18:19], v[6:7]
	v_mov_b32_e32 v21, v10
	v_pk_add_f32 v[6:7], v[20:21], v[6:7]
	ds_bpermute_b32 v11, v72, v7
	ds_bpermute_b32 v10, v72, v6
	v_lshl_add_u64 v[8:9], v[16:17], 0, v[8:9]
	global_store_dword v[8:9], v26, off nt
	v_mul_f32_e32 v18, 0x45800000, v27
	v_mov_b32_e32 v19, 0
	s_waitcnt lgkmcnt(0)
	v_pk_add_f32 v[6:7], v[6:7], v[10:11]
	ds_bpermute_b32 v9, v73, v7
	ds_bpermute_b32 v8, v73, v6
	v_cndmask_b32_e32 v10, v27, v18, vcc
	v_mul_f32_e32 v11, v22, v10
	v_mul_f32_e32 v18, v23, v10
	v_mul_f32_e32 v11, v71, v11
	s_waitcnt lgkmcnt(0)
	v_pk_add_f32 v[6:7], v[6:7], v[8:9]
	ds_bpermute_b32 v9, v74, v7
	ds_bpermute_b32 v8, v74, v6
	v_mul_f32_e32 v18, v70, v18
	v_cvt_pk_fp8_f32 v19, v11, v18
	v_mul_f32_e32 v13, v13, v10
	v_mul_f32_e32 v10, v12, v10
	s_waitcnt lgkmcnt(0)
	v_pk_add_f32 v[6:7], v[6:7], v[8:9]
	ds_bpermute_b32 v9, v75, v7
	ds_bpermute_b32 v8, v75, v6
	v_mul_f32_e32 v11, v69, v13
	v_mul_f32_e32 v10, v68, v10
	v_cvt_pk_fp8_f32 v19, v11, v10 op_sel:[0,0,1]
	v_or_b32_e32 v10, 25, v32
	s_waitcnt lgkmcnt(0)
	v_pk_add_f32 v[6:7], v[6:7], v[8:9]
	ds_bpermute_b32 v9, v76, v7
	ds_bpermute_b32 v8, v76, v6
	v_ashrrev_i32_e32 v11, 31, v10
	v_lshlrev_b64 v[10:11], 11, v[10:11]
	v_lshl_add_u64 v[10:11], v[16:17], 0, v[10:11]
	global_store_dword v[10:11], v19, off nt
	s_waitcnt lgkmcnt(0)
	v_pk_add_f32 v[6:7], v[6:7], v[8:9]
	s_nop 0
	v_pk_fma_f32 v[6:7], v[6:7], s[18:19], v[48:49] op_sel_hi:[1,0,0]
	s_nop 0
	v_mul_f32_e32 v8, 0x4b800000, v7
	v_cmp_gt_f32_e32 vcc, s67, v7
	s_nop 1
	v_cndmask_b32_e32 v7, v7, v8, vcc
	v_rsq_f32_e32 v7, v7
	v_or_b32_e32 v8, 26, v32
	v_ashrrev_i32_e32 v9, 31, v8
	v_mul_f32_e32 v10, 0x45800000, v7
	v_cndmask_b32_e32 v7, v7, v10, vcc
	v_mul_f32_e32 v4, v4, v7
	v_mul_f32_e32 v5, v5, v7
	v_mul_f32_e32 v4, v71, v4
	v_mul_f32_e32 v5, v70, v5
	v_mov_b32_e32 v10, 0
	v_cvt_pk_fp8_f32 v10, v4, v5
	v_mul_f32_e32 v1, v1, v7
	v_mul_f32_e32 v0, v0, v7
	v_mul_f32_e32 v1, v69, v1
	v_mul_f32_e32 v0, v68, v0
	v_cvt_pk_fp8_f32 v10, v1, v0 op_sel:[0,0,1]
	v_mul_f32_e32 v0, 0x4b800000, v6
	v_cmp_gt_f32_e32 vcc, s67, v6
	v_mov_b32_e32 v5, 0
	s_nop 0
	v_cndmask_b32_e32 v0, v6, v0, vcc
	v_rsq_f32_e32 v4, v0
	v_lshlrev_b64 v[0:1], 11, v[8:9]
	v_lshl_add_u64 v[0:1], v[16:17], 0, v[0:1]
	global_store_dword v[0:1], v10, off nt
	v_mul_f32_e32 v0, 0x45800000, v4
	v_cndmask_b32_e32 v0, v4, v0, vcc
	v_mul_f32_e32 v1, v14, v0
	v_mul_f32_e32 v4, v15, v0
	v_mul_f32_e32 v1, v71, v1
	v_mul_f32_e32 v4, v70, v4
	v_cvt_pk_fp8_f32 v5, v1, v4
	v_mul_f32_e32 v3, v3, v0
	v_mul_f32_e32 v0, v2, v0
	v_mul_f32_e32 v1, v69, v3
	v_mul_f32_e32 v0, v68, v0
	v_cvt_pk_fp8_f32 v5, v1, v0 op_sel:[0,0,1]
	v_or_b32_e32 v0, 27, v32
	v_ashrrev_i32_e32 v1, 31, v0
	v_lshlrev_b64 v[0:1], 11, v[0:1]
	v_lshl_add_u64 v[0:1], v[16:17], 0, v[0:1]
	global_store_dword v[0:1], v5, off nt
	s_barrier

.LBB0_973:
	s_or_b64 exec, exec, s[2:3]
	v_ashrrev_i32_e32 v10, 3, v108
	v_ashrrev_i32_e32 v11, 31, v10
	v_lshl_add_u64 v[0:1], s[40:41], 0, v[10:11]
	v_lshlrev_b64 v[2:3], 13, v[0:1]
	v_lshl_add_u64 v[2:3], s[24:25], 0, v[2:3]
	s_mov_b32 s5, s23
	v_lshl_add_u64 v[2:3], v[2:3], 0, s[4:5]
	v_lshlrev_b32_e32 v4, 1, v64
	v_mov_b32_e32 v5, v65
	v_lshl_add_u64 v[6:7], v[2:3], 0, v[4:5]
	v_add_co_u32_e32 v2, vcc, s50, v6
	s_waitcnt lgkmcnt(0)
	s_nop 0
	v_addc_co_u32_e32 v3, vcc, 0, v7, vcc
	s_barrier
	global_load_dwordx4 v[2:5], v[2:3], off offset:2944
	s_lshl_b32 s2, s22, 2
	s_add_u32 s2, s48, s2
	v_lshl_add_u64 v[6:7], v[6:7], 0, s[38:39]
	v_lshlrev_b32_e32 v42, 2, v64
	v_and_b32_e32 v11, 64, v254
	s_addc_u32 s3, s49, 0
	global_load_dwordx4 v[6:9], v[6:7], off offset:16
	v_mul_lo_u32 v19, v10, s68
	v_add_u32_e32 v43, 64, v11
	global_load_dwordx4 v[10:13], v42, s[2:3] offset:16
	global_load_dwordx4 v[14:17], v42, s[2:3]
	v_xor_b32_e32 v18, 1, v254
	v_add3_u32 v30, s67, v19, v42
	v_cmp_lt_i32_e32 vcc, v18, v43
	v_lshlrev_b64 v[0:1], 11, v[0:1]
	v_lshl_add_u64 v[0:1], s[18:19], 0, v[0:1]
	v_cndmask_b32_e32 v34, v254, v18, vcc
	ds_read_b128 v[18:21], v30
	ds_read_b128 v[22:25], v30 offset:32
	ds_read_b128 v[26:29], v30 offset:16
	ds_read_b128 v[30:33], v30 offset:48
	v_lshlrev_b32_e32 v44, 2, v34
	s_waitcnt lgkmcnt(3)
	v_mul_f32_e32 v45, v19, v19
	v_fmac_f32_e32 v45, v18, v18
	v_fmac_f32_e32 v45, v20, v20
	v_fmac_f32_e32 v45, v21, v21
	s_waitcnt lgkmcnt(1)
	v_fmac_f32_e32 v45, v26, v26
	v_fmac_f32_e32 v45, v27, v27
	v_fmac_f32_e32 v45, v28, v28
	v_pk_mul_f32 v[34:35], v[22:23], v[22:23]
	v_fmac_f32_e32 v45, v29, v29
	v_add_f32_e32 v34, v45, v34
	v_pk_mul_f32 v[36:37], v[24:25], v[24:25]
	v_add_f32_e32 v34, v34, v35
	v_add_f32_e32 v34, v34, v36
	s_waitcnt lgkmcnt(0)
	v_pk_mul_f32 v[38:39], v[30:31], v[30:31]
	v_add_f32_e32 v34, v34, v37
	v_add_f32_e32 v34, v34, v38
	v_pk_mul_f32 v[40:41], v[32:33], v[32:33]
	v_add_f32_e32 v34, v34, v39
	v_add_f32_e32 v34, v34, v40
	v_add_f32_e32 v34, v34, v41
	ds_bpermute_b32 v35, v44, v34
	v_xor_b32_e32 v36, 2, v254
	v_cmp_lt_i32_e32 vcc, v36, v43
	v_lshl_add_u64 v[0:1], v[0:1], 0, s[22:23]
	v_lshl_add_u64 v[0:1], v[0:1], 0, v[64:65]
	v_cndmask_b32_e32 v36, v254, v36, vcc
	v_lshlrev_b32_e32 v36, 2, v36
	s_waitcnt lgkmcnt(0)
	v_add_f32_e32 v34, v34, v35
	ds_bpermute_b32 v35, v36, v34
	v_xor_b32_e32 v36, 4, v254
	v_cmp_lt_i32_e32 vcc, v36, v43
	s_add_i32 s1, s1, s0
	s_add_i32 s16, s16, -1
	v_cndmask_b32_e32 v36, v254, v36, vcc
	v_lshlrev_b32_e32 v36, 2, v36
	s_waitcnt lgkmcnt(0)
	v_add_f32_e32 v34, v34, v35
	ds_bpermute_b32 v35, v36, v34
	s_cmp_lg_u32 s16, 0
	s_waitcnt lgkmcnt(0)
	v_add_f32_e32 v34, v34, v35
	v_fmamk_f32 v34, v34, 0x3c000000, v104
	v_mul_f32_e32 v35, 0x4b800000, v34
	v_cmp_gt_f32_e32 vcc, s69, v34
	s_waitcnt vmcnt(3)
	v_lshlrev_b32_e32 v44, 16, v3
	v_cndmask_b32_e32 v34, v34, v35, vcc
	v_rsq_f32_e32 v43, v34
	global_load_dwordx4 v[34:37], v42, s[2:3] offset:48
	global_load_dwordx4 v[38:41], v42, s[2:3] offset:32
	v_and_b32_e32 v3, 0xffff0000, v3
	v_mul_f32_e32 v3, 0xbfb8aa3b, v3
	v_mul_f32_e32 v42, 0x45800000, v43
	v_cndmask_b32_e32 v42, v43, v42, vcc
	v_lshlrev_b32_e32 v43, 16, v2
	v_and_b32_e32 v2, 0xffff0000, v2
	v_mul_f32_e32 v2, 0xbfb8aa3b, v2
	v_exp_f32_e32 v2, v2
	v_mul_f32_e32 v18, v18, v42
	s_waitcnt vmcnt(2)
	v_mul_f32_e32 v14, v14, v18
	v_mul_f32_e32 v18, v19, v42
	v_add_f32_e32 v2, 1.0, v2
	v_rcp_f32_e32 v2, v2
	v_mul_f32_e32 v15, v15, v18
	v_exp_f32_e32 v3, v3
	v_mul_f32_e32 v18, v20, v42
	v_mul_f32_e32 v15, v2, v15
	v_mul_f32_e32 v2, 0xbfb8aa3b, v44
	v_exp_f32_e32 v2, v2
	v_add_f32_e32 v3, 1.0, v3
	v_rcp_f32_e32 v3, v3
	v_mul_f32_e32 v16, v16, v18
	v_add_f32_e32 v2, 1.0, v2
	v_rcp_f32_e32 v2, v2
	v_lshlrev_b32_e32 v45, 16, v4
	v_and_b32_e32 v4, 0xffff0000, v4
	v_mul_f32_e32 v4, 0xbfb8aa3b, v4
	v_mul_f32_e32 v16, v2, v16
	v_mul_f32_e32 v2, v21, v42
	v_mul_f32_e32 v2, v17, v2
	v_mul_f32_e32 v17, v3, v2
	v_mul_f32_e32 v2, 0xbfb8aa3b, v45
	v_exp_f32_e32 v2, v2
	v_exp_f32_e32 v4, v4
	v_mul_f32_e32 v3, v26, v42
	v_mul_f32_e32 v3, v10, v3
	v_add_f32_e32 v2, 1.0, v2
	v_rcp_f32_e32 v2, v2
	v_add_f32_e32 v4, 1.0, v4
	v_rcp_f32_e32 v4, v4
	v_lshlrev_b32_e32 v46, 16, v5
	v_mul_f32_e32 v10, v2, v3
	v_mul_f32_e32 v2, v27, v42
	v_mul_f32_e32 v2, v11, v2
	v_mul_f32_e32 v4, v4, v2
	v_mul_f32_e32 v2, 0xbfb8aa3b, v46
	v_and_b32_e32 v5, 0xffff0000, v5
	v_exp_f32_e32 v2, v2
	v_mul_f32_e32 v5, 0xbfb8aa3b, v5
	v_exp_f32_e32 v5, v5
	v_mul_f32_e32 v3, v28, v42
	v_add_f32_e32 v2, 1.0, v2
	v_rcp_f32_e32 v2, v2
	v_add_f32_e32 v5, 1.0, v5
	v_rcp_f32_e32 v5, v5
	v_mul_f32_e32 v3, v12, v3
	v_mul_f32_e32 v11, v2, v3
	v_mul_f32_e32 v2, v29, v42
	v_lshlrev_b32_e32 v47, 16, v6
	v_mul_f32_e32 v2, v2, v13
	v_mul_f32_e32 v12, v5, v2
	v_mul_f32_e32 v2, 0xbfb8aa3b, v47
	v_and_b32_e32 v6, 0xffff0000, v6
	v_exp_f32_e32 v2, v2
	v_mul_f32_e32 v5, 0xbfb8aa3b, v6
	v_exp_f32_e32 v5, v5
	v_mul_f32_e32 v3, v22, v42
	v_add_f32_e32 v2, 1.0, v2
	v_rcp_f32_e32 v2, v2
	v_add_f32_e32 v5, 1.0, v5
	v_rcp_f32_e32 v5, v5
	v_lshlrev_b32_e32 v48, 16, v7
	v_and_b32_e32 v7, 0xffff0000, v7
	v_mul_f32_e32 v7, 0xbfb8aa3b, v7
	v_exp_f32_e32 v7, v7
	v_lshlrev_b32_e32 v49, 16, v8
	v_and_b32_e32 v8, 0xffff0000, v8
	v_mul_f32_e32 v8, 0xbfb8aa3b, v8
	v_add_f32_e32 v7, 1.0, v7
	s_waitcnt vmcnt(0)
	v_mul_f32_e32 v3, v3, v38
	v_mul_f32_e32 v6, v2, v3
	v_mul_f32_e32 v2, v23, v42
	v_mul_f32_e32 v2, v2, v39
	v_mul_f32_e32 v5, v5, v2
	v_mul_f32_e32 v2, 0xbfb8aa3b, v48
	v_exp_f32_e32 v2, v2
	v_mul_f32_e32 v3, v24, v42
	v_rcp_f32_e32 v7, v7
	v_mul_f32_e32 v3, v3, v40
	v_add_f32_e32 v2, 1.0, v2
	v_rcp_f32_e32 v2, v2
	v_exp_f32_e32 v8, v8
	v_lshlrev_b32_e32 v50, 16, v9
	v_and_b32_e32 v9, 0xffff0000, v9
	v_mul_f32_e32 v13, v2, v3
	v_mul_f32_e32 v2, v25, v42
	v_mul_f32_e32 v2, v2, v41
	v_mul_f32_e32 v7, v7, v2
	v_mul_f32_e32 v2, 0xbfb8aa3b, v49
	v_exp_f32_e32 v2, v2
	v_add_f32_e32 v8, 1.0, v8
	v_mul_f32_e32 v3, v30, v42
	v_rcp_f32_e32 v8, v8
	v_add_f32_e32 v2, 1.0, v2
	v_rcp_f32_e32 v2, v2
	v_mul_f32_e32 v3, v3, v34
	v_mul_f32_e32 v43, 0xbfb8aa3b, v43
	v_mul_f32_e32 v9, 0xbfb8aa3b, v9
	v_mul_f32_e32 v18, v2, v3
	v_mul_f32_e32 v2, v31, v42
	v_mul_f32_e32 v2, v2, v35
	v_mul_f32_e32 v8, v8, v2
	v_mul_f32_e32 v2, 0xbfb8aa3b, v50
	v_exp_f32_e32 v2, v2
	v_exp_f32_e32 v43, v43
	v_exp_f32_e32 v9, v9
	v_mul_f32_e32 v3, v32, v42
	v_add_f32_e32 v2, 1.0, v2
	v_rcp_f32_e32 v2, v2
	v_add_f32_e32 v43, 1.0, v43
	v_add_f32_e32 v9, 1.0, v9
	v_rcp_f32_e32 v43, v43
	v_rcp_f32_e32 v9, v9
	v_mul_f32_e32 v3, v3, v36
	v_mul_f32_e32 v19, v2, v3
	v_mul_f32_e32 v2, v33, v42
	v_mov_b32_e32 v3, v65
	v_mul_f32_e32 v2, v2, v37
	v_cvt_pk_fp8_f32 v3, v10, v4
	v_mov_b32_e32 v4, v65
	v_mul_f32_e32 v14, v43, v14
	v_mul_f32_e32 v9, v9, v2
	v_mov_b32_e32 v2, v65
	v_cvt_pk_fp8_f32 v4, v6, v5
	v_mov_b32_e32 v5, v65
	v_cvt_pk_fp8_f32 v2, v14, v15
	v_cvt_pk_fp8_f32 v5, v18, v8
	v_cvt_pk_fp8_f32 v3, v11, v12 op_sel:[0,0,1]
	v_cvt_pk_fp8_f32 v4, v13, v7 op_sel:[0,0,1]
	v_cvt_pk_fp8_f32 v2, v16, v17 op_sel:[0,0,1]
	v_cvt_pk_fp8_f32 v5, v19, v9 op_sel:[0,0,1]
	v_add_co_u32_e32 v0, vcc, 0x3c560000, v0
	s_nop 1
	v_addc_co_u32_e32 v1, vcc, 0, v1, vcc
	global_store_dwordx4 v[0:1], v[2:5], off offset:2048 nt
	s_barrier
	s_cbranch_scc0 .LBB0_1052

.LBB0_1717:
	s_or_b64 exec, exec, s[2:3]
	v_and_b32_e32 v68, 63, v70
	v_ashrrev_i32_e32 v40, 8, v70
	v_bfe_u32 v41, v70, 6, 2
	s_waitcnt vmcnt(0)
	v_lshl_add_u32 v0, v68, 6, 0
	v_lshlrev_b32_e32 v1, 5, v40
	v_lshlrev_b32_e32 v2, 2, v41
	v_add3_u32 v0, v0, v1, v2
	s_waitcnt lgkmcnt(0)
	s_barrier
	ds_read2_b32 v[2:3], v0 offset1:4
	s_mov_b32 s2, 0xbfb8aa3b
	v_and_b32_e32 v71, 64, v254
	v_cmp_gt_u32_e64 s[6:7], s31, v70
	s_ashr_i32 s30, s18, 6
	s_waitcnt lgkmcnt(0)
	v_mul_f32_e64 v0, |v3|, s2
	v_exp_f32_e32 v4, v0
	v_max_f32_e32 v0, v3, v3
	v_min_f32_e32 v3, 0, v0
	s_mov_b32 s2, 0x3f2aaaab
	v_add_f32_e32 v5, 1.0, v4
	v_add_f32_e32 v0, -1.0, v5
	v_sub_f32_e32 v1, v0, v5
	v_add_f32_e32 v1, 1.0, v1
	v_sub_f32_e32 v0, v4, v0
	v_add_f32_e32 v6, v0, v1
	v_frexp_mant_f32_e32 v7, v5
	v_cvt_f64_f32_e32 v[0:1], v5
	v_frexp_exp_i32_f64_e32 v0, v[0:1]
	v_cmp_gt_f32_e32 vcc, s2, v7
	s_mov_b32 s2, 0x3f317218
	s_and_b32 s16, s18, 63
	v_subbrev_co_u32_e32 v0, vcc, 0, v0, vcc
	v_sub_u32_e32 v1, 0, v0
	v_ldexp_f32 v5, v5, v1
	v_ldexp_f32 v1, v6, v1
	v_add_f32_e32 v6, -1.0, v5
	v_add_f32_e32 v9, 1.0, v5
	v_add_f32_e32 v7, 1.0, v6
	v_add_f32_e32 v10, -1.0, v9
	v_sub_f32_e32 v7, v5, v7
	v_sub_f32_e32 v5, v5, v10
	v_add_f32_e32 v7, v1, v7
	v_add_f32_e32 v1, v1, v5
	v_add_f32_e32 v5, v9, v1
	v_rcp_f32_e32 v10, v5
	v_add_f32_e32 v8, v6, v7
	v_sub_f32_e32 v6, v8, v6
	v_sub_f32_e32 v6, v7, v6
	v_sub_f32_e32 v7, v5, v9
	v_sub_f32_e32 v1, v1, v7
	v_mul_f32_e32 v7, v8, v10
	v_mul_f32_e32 v9, v5, v7
	v_fma_f32 v11, v7, v5, -v9
	v_fmac_f32_e32 v11, v7, v1
	v_add_f32_e32 v12, v9, v11
	v_sub_f32_e32 v13, v8, v12
	v_sub_f32_e32 v8, v8, v13
	v_sub_f32_e32 v9, v12, v9
	v_sub_f32_e32 v8, v8, v12
	v_add_f32_e32 v6, v6, v8
	v_sub_f32_e32 v8, v9, v11
	v_add_f32_e32 v6, v8, v6
	v_add_f32_e32 v8, v13, v6
	v_mul_f32_e32 v9, v10, v8
	v_mul_f32_e32 v11, v5, v9
	v_fma_f32 v5, v9, v5, -v11
	v_fmac_f32_e32 v5, v9, v1
	v_sub_f32_e32 v1, v13, v8
	v_add_f32_e32 v1, v6, v1
	v_add_f32_e32 v6, v11, v5
	v_sub_f32_e32 v12, v8, v6
	v_sub_f32_e32 v8, v8, v12
	v_sub_f32_e32 v11, v6, v11
	v_sub_f32_e32 v6, v8, v6
	v_add_f32_e32 v1, v1, v6
	v_sub_f32_e32 v5, v11, v5
	v_cvt_f32_i32_e32 v0, v0
	v_add_f32_e32 v1, v5, v1
	v_add_f32_e32 v5, v7, v9
	v_add_f32_e32 v1, v12, v1
	v_sub_f32_e32 v6, v5, v7
	v_mul_f32_e32 v1, v10, v1
	v_sub_f32_e32 v6, v9, v6
	v_add_f32_e32 v1, v6, v1
	v_mul_f32_e32 v9, 0x3f317218, v0
	v_add_f32_e32 v6, v5, v1
	v_fma_f32 v10, v0, s2, -v9
	v_mul_f32_e32 v7, v6, v6
	v_fmac_f32_e32 v10, 0xb102e308, v0
	v_sub_f32_e32 v0, v6, v5
	v_fmamk_f32 v8, v7, 0x3e9b6dac, v69
	v_sub_f32_e32 v0, v1, v0
	v_add_f32_e32 v1, v9, v10
	v_fmaak_f32 v8, v7, v8, 0x3f2aaada
	v_sub_f32_e32 v5, v1, v9
	v_ldexp_f32 v9, v6, 1
	v_mul_f32_e32 v6, v6, v7
	v_mul_f32_e32 v6, v6, v8
	v_add_f32_e32 v7, v9, v6
	v_sub_f32_e32 v8, v7, v9
	v_ldexp_f32 v0, v0, 1
	v_sub_f32_e32 v6, v6, v8
	v_add_f32_e32 v0, v0, v6
	v_add_f32_e32 v6, v7, v0
	v_sub_f32_e32 v7, v6, v7
	v_sub_f32_e32 v0, v0, v7
	v_add_f32_e32 v7, v1, v6
	v_sub_f32_e32 v8, v7, v1
	v_sub_f32_e32 v9, v7, v8
	v_sub_f32_e32 v5, v10, v5
	v_sub_f32_e32 v1, v1, v9
	v_sub_f32_e32 v6, v6, v8
	v_add_f32_e32 v1, v6, v1
	v_add_f32_e32 v6, v5, v0
	v_sub_f32_e32 v8, v6, v5
	v_sub_f32_e32 v9, v6, v8
	v_sub_f32_e32 v5, v5, v9
	v_sub_f32_e32 v0, v0, v8
	v_add_f32_e32 v1, v6, v1
	v_add_f32_e32 v0, v0, v5
	v_add_f32_e32 v5, v7, v1
	v_sub_f32_e32 v6, v5, v7
	v_sub_f32_e32 v1, v1, v6
	v_add_f32_e32 v0, v0, v1
	s_mov_b32 s2, 0x7f800000
	v_add_f32_e32 v0, v5, v0
	v_cmp_neq_f32_e32 vcc, s2, v4
	s_mov_b32 s2, 0x33800000
	s_nop 0
	v_cndmask_b32_e32 v0, v86, v0, vcc
	v_cmp_ngt_f32_e32 vcc, -1.0, v4
	s_nop 1
	v_cndmask_b32_e32 v0, v87, v0, vcc
	v_cmp_neq_f32_e32 vcc, -1.0, v4
	s_nop 1
	v_cndmask_b32_e32 v0, v88, v0, vcc
	v_cmp_lt_f32_e64 vcc, |v4|, s2
	s_nop 1
	v_cndmask_b32_e32 v0, v0, v4, vcc
	v_sub_f32_e32 v1, v3, v0
	v_add_u32_e32 v0, -1, v254
	v_cmp_lt_i32_e32 vcc, v0, v71
	v_add_u32_e32 v3, -2, v254
	v_cmp_lt_i32_e64 s[2:3], v3, v71
	v_cndmask_b32_e32 v0, v0, v254, vcc
	v_lshlrev_b32_e32 v0, 2, v0
	ds_bpermute_b32 v0, v0, v1
	v_cmp_eq_u32_e32 vcc, 0, v68
	v_cndmask_b32_e64 v3, v3, v254, s[2:3]
	v_lshlrev_b32_e32 v3, 2, v3
	v_cmp_gt_u32_e64 s[2:3], 2, v68
	s_waitcnt lgkmcnt(0)
	v_add_f32_e32 v0, v1, v0
	v_cndmask_b32_e32 v0, v0, v1, vcc
	ds_bpermute_b32 v3, v3, v0
	s_waitcnt lgkmcnt(0)
	v_add_f32_e32 v3, v0, v3
	v_cndmask_b32_e64 v0, v3, v0, s[2:3]
	v_add_u32_e32 v3, -4, v254
	v_cmp_lt_i32_e64 s[2:3], v3, v71
	s_nop 1
	v_cndmask_b32_e64 v3, v3, v254, s[2:3]
	v_lshlrev_b32_e32 v3, 2, v3
	ds_bpermute_b32 v3, v3, v0
	v_cmp_gt_u32_e64 s[2:3], 4, v68
	s_waitcnt lgkmcnt(0)
	v_add_f32_e32 v3, v0, v3
	v_cndmask_b32_e64 v0, v3, v0, s[2:3]
	v_add_u32_e32 v3, -8, v254
	v_cmp_lt_i32_e64 s[2:3], v3, v71
	s_nop 1
	v_cndmask_b32_e64 v3, v3, v254, s[2:3]
	v_lshlrev_b32_e32 v3, 2, v3
	ds_bpermute_b32 v3, v3, v0
	v_cmp_gt_u32_e64 s[2:3], 8, v68
	s_waitcnt lgkmcnt(0)
	v_add_f32_e32 v3, v0, v3
	v_cndmask_b32_e64 v0, v3, v0, s[2:3]
	v_add_u32_e32 v3, -16, v254
	v_cmp_lt_i32_e64 s[2:3], v3, v71
	s_nop 1
	v_cndmask_b32_e64 v3, v3, v254, s[2:3]
	v_lshlrev_b32_e32 v3, 2, v3
	ds_bpermute_b32 v3, v3, v0
	v_cmp_gt_u32_e64 s[2:3], 16, v68
	s_waitcnt lgkmcnt(0)
	v_add_f32_e32 v3, v0, v3
	v_cndmask_b32_e64 v0, v3, v0, s[2:3]
	v_subrev_u32_e32 v3, 32, v254
	v_cmp_lt_i32_e64 s[4:5], v3, v71
	s_nop 1
	v_cndmask_b32_e64 v3, v3, v254, s[4:5]
	v_lshlrev_b32_e32 v3, 2, v3
	ds_bpermute_b32 v3, v3, v0
	v_cmp_gt_u32_e64 s[4:5], 32, v68
	s_waitcnt lgkmcnt(0)
	v_add_f32_e32 v3, v0, v3
	v_cndmask_b32_e64 v3, v3, v0, s[4:5]
	ds_bpermute_b32 v0, v84, v3
	s_waitcnt lgkmcnt(0)
	v_sub_f32_e32 v4, v0, v3
	v_add_f32_e32 v1, v1, v4
	v_cndmask_b32_e64 v1, v1, v3, s[6:7]
	v_sub_f32_e32 v1, v0, v1
	v_add_f32_e32 v1, v2, v1
	v_mov_b32_e32 v2, 0xff7fffff
	v_mov_b32_e32 v3, 0xff7fffff
	s_nop 0
	v_mov_b32_dpp v2, v1 quad_perm:[1,0,3,2] row_mask:0xf bank_mask:0xf
	v_max_f32_e32 v2, v2, v2
	v_max_f32_e32 v2, v1, v2
	s_nop 1
	v_mov_b32_dpp v3, v2 quad_perm:[2,3,0,1] row_mask:0xf bank_mask:0xf
	v_max_f32_e32 v3, v3, v3
	v_max_f32_e32 v2, v2, v3
	v_mov_b32_e32 v3, 0xff7fffff
	s_nop 1
	v_mov_b32_dpp v3, v2 row_half_mirror row_mask:0xf bank_mask:0xf
	v_max_f32_e32 v3, v3, v3
	v_max_f32_e32 v2, v2, v3
	v_mov_b32_e32 v3, 0xff7fffff
	s_nop 1
	v_mov_b32_dpp v3, v2 row_mirror row_mask:0xf bank_mask:0xf
	v_max_f32_e32 v3, v3, v3
	v_max_f32_e32 v2, v2, v3
	v_mov_b32_e32 v3, 0xff7fffff
	s_nop 1
	v_mov_b32_dpp v3, v2 row_bcast:15 row_mask:0xa bank_mask:0xf
	v_max_f32_e32 v3, v3, v3
	v_max_f32_e32 v2, v2, v3
	v_mov_b32_e32 v3, 0xff7fffff
	s_nop 1
	v_mov_b32_dpp v3, v2 row_bcast:31 row_mask:0xc bank_mask:0xf
	v_max_f32_e32 v3, v3, v3
	v_max_f32_e32 v2, v2, v3
	s_nop 0
	v_readlane_b32 s10, v2, 63
	v_lshl_add_u32 v2, v70, 2, 0
	s_nop 0
	v_subrev_f32_e32 v1, s10, v1
	v_mul_f32_e32 v1, 0x3fb8aa3b, v1
	v_exp_f32_e32 v1, v1
	ds_write_b32 v2, v1 offset:4096
	s_and_saveexec_b64 s[8:9], vcc
	s_cbranch_execz .LBB0_1719
	s_lshl_b32 s11, s30, 10
	v_lshl_add_u32 v1, v40, 7, s11
	s_lshl_b32 s11, s16, 1
	s_xor_b32 s28, s11, 0x7e
	v_mov_b32_e32 v2, s28
	v_mov_b32_e32 v3, s11
	v_cndmask_b32_e64 v2, v2, v3, s[6:7]
	v_or_b32_e32 v1, v1, v2
	v_lshl_add_u32 v2, v41, 8, v1
	v_readlane_b32 s28, v255, 11
	v_ashrrev_i32_e32 v3, 31, v2
	v_readlane_b32 s29, v255, 12
	v_mov_b32_e32 v1, s10
	s_nop 0
	v_lshl_add_u64 v[2:3], v[2:3], 2, s[28:29]
	global_store_dwordx2 v[2:3], v[0:1], off nt

.LBB0_1794:
	s_and_saveexec_b64 s[28:29], s[8:9]
	s_xor_b64 s[8:9], exec, s[28:29]
	s_lshl_b32 s10, s30, 3
	s_or_saveexec_b64 s[8:9], s[8:9]
	v_mov_b32_e32 v2, s10
	s_xor_b64 exec, exec, s[8:9]
	s_cbranch_execz .LBB0_1798
	s_lshl_b32 s10, s30, 3
	v_lshl_add_u32 v4, v1, 1, s10
	v_ashrrev_i32_e32 v5, 31, v4
	v_or_b32_e32 v6, 1, v4
	v_lshlrev_b64 v[4:5], 15, v[4:5]
	v_and_b32_e32 v3, 0x7e, v0
	v_lshl_add_u64 v[4:5], s[48:49], 0, v[4:5]
	s_lshl_b32 s78, s16, 9
	v_lshl_add_u64 v[4:5], v[4:5], 0, s[78:79]
	v_lshlrev_b32_e32 v64, 2, v3
	v_lshl_add_u64 v[4:5], v[4:5], 0, v[64:65]
	v_ashrrev_i32_e32 v7, 31, v6
	global_store_dwordx2 v[4:5], v[14:15], off nt
	v_lshlrev_b64 v[4:5], 15, v[6:7]
	v_lshl_add_u64 v[4:5], s[48:49], 0, v[4:5]
	s_xor_b32 s78, s78, 0x7e00
	v_lshl_add_u64 v[4:5], v[4:5], 0, s[78:79]
	v_mov_b32_e32 v2, s10
	v_lshl_add_u64 v[4:5], v[4:5], 0, v[64:65]
	global_store_dwordx2 v[4:5], v[18:19], off nt

.LBB0_1799:
	v_lshl_add_u64 v[0:1], s[12:13], 0, v[74:75]
	global_load_dwordx4 v[0:3], v[0:1], off
	v_lshl_add_u64 v[4:5], s[12:13], 0, v[76:77]
	global_load_dwordx4 v[4:7], v[4:5], off
	v_add_u32_e32 v19, s9, v94
	ds_read_b32 v8, v19
	ds_read_b32 v10, v19 offset:1024
	v_add_u32_e32 v32, s8, v92
	v_add_u32_e32 v33, s33, v92
	v_add_u32_e32 v34, s8, v93
	v_add_u32_e32 v35, s33, v93
	s_waitcnt vmcnt(1)
	v_lshlrev_b32_e32 v12, 16, v0
	v_and_b32_e32 v13, 0xffff0000, v0
	v_lshlrev_b32_e32 v0, 16, v1
	v_and_b32_e32 v1, 0xffff0000, v1
	v_lshlrev_b32_e32 v14, 16, v2
	v_and_b32_e32 v15, 0xffff0000, v2
	v_lshlrev_b32_e32 v2, 16, v3
	v_and_b32_e32 v3, 0xffff0000, v3
	s_waitcnt lgkmcnt(1)
	v_pk_mul_f32 v[20:21], v[8:9], v[12:13] op_sel_hi:[0,1]
	v_pk_mul_f32 v[22:23], v[8:9], v[0:1] op_sel_hi:[0,1]
	v_pk_mul_f32 v[26:27], v[8:9], v[14:15] op_sel_hi:[0,1]
	v_pk_mul_f32 v[28:29], v[8:9], v[2:3] op_sel_hi:[0,1]
	s_waitcnt lgkmcnt(0)
	v_pk_mul_f32 v[12:13], v[10:11], v[12:13] op_sel_hi:[0,1]
	v_pk_mul_f32 v[24:25], v[10:11], v[0:1] op_sel_hi:[0,1]
	v_pk_mul_f32 v[14:15], v[10:11], v[14:15] op_sel_hi:[0,1]
	v_pk_mul_f32 v[30:31], v[10:11], v[2:3] op_sel_hi:[0,1]
	v_cvt_pk_bf16_f32 v0, v20, v21
	v_cvt_pk_bf16_f32 v1, v22, v23
	v_cvt_pk_bf16_f32 v2, v26, v27
	v_cvt_pk_bf16_f32 v3, v28, v29
	v_cvt_pk_bf16_f32 v8, v12, v13
	v_cvt_pk_bf16_f32 v9, v24, v25
	v_cvt_pk_bf16_f32 v10, v14, v15
	v_cvt_pk_bf16_f32 v11, v30, v31
	ds_write_b128 v32, v[0:3]
	ds_write_b128 v33, v[8:11]
	ds_read_b32 v0, v19 offset:128
	ds_read_b32 v2, v19 offset:1152
	s_waitcnt vmcnt(0)
	v_lshlrev_b32_e32 v16, 16, v4
	v_and_b32_e32 v17, 0xffff0000, v4
	v_lshlrev_b32_e32 v4, 16, v5
	v_and_b32_e32 v5, 0xffff0000, v5
	v_lshlrev_b32_e32 v18, 16, v6
	v_and_b32_e32 v19, 0xffff0000, v6
	v_lshlrev_b32_e32 v6, 16, v7
	v_and_b32_e32 v7, 0xffff0000, v7
	s_waitcnt lgkmcnt(1)
	v_pk_mul_f32 v[8:9], v[0:1], v[16:17] op_sel_hi:[0,1]
	s_waitcnt lgkmcnt(0)
	v_pk_mul_f32 v[10:11], v[2:3], v[16:17] op_sel_hi:[0,1]
	v_pk_mul_f32 v[12:13], v[0:1], v[4:5] op_sel_hi:[0,1]
	v_pk_mul_f32 v[16:17], v[0:1], v[18:19] op_sel_hi:[0,1]
	v_pk_mul_f32 v[20:21], v[0:1], v[6:7] op_sel_hi:[0,1]
	v_pk_mul_f32 v[14:15], v[2:3], v[4:5] op_sel_hi:[0,1]
	v_pk_mul_f32 v[18:19], v[2:3], v[18:19] op_sel_hi:[0,1]
	v_pk_mul_f32 v[22:23], v[2:3], v[6:7] op_sel_hi:[0,1]
	v_cvt_pk_bf16_f32 v0, v8, v9
	v_cvt_pk_bf16_f32 v1, v12, v13
	v_cvt_pk_bf16_f32 v2, v16, v17
	v_cvt_pk_bf16_f32 v3, v20, v21
	v_cvt_pk_bf16_f32 v4, v10, v11
	v_cvt_pk_bf16_f32 v5, v14, v15
	v_cvt_pk_bf16_f32 v6, v18, v19
	v_cvt_pk_bf16_f32 v7, v22, v23
	ds_write_b128 v34, v[0:3]
	ds_write_b128 v35, v[4:7]
	s_waitcnt lgkmcnt(0)
	s_barrier
	ds_read_b64_tr_b16 v[48:49], v64 offset:0
	ds_read_b64_tr_b16 v[50:51], v64 offset:0x800
	ds_read_b64_tr_b16 v[0:1], v95 offset:0
	ds_read_b64_tr_b16 v[2:3], v95 offset:0x800
	ds_read_b64_tr_b16 v[16:17], v95 offset:0x200
	ds_read_b64_tr_b16 v[18:19], v95 offset:0xa00
	ds_read_b64_tr_b16 v[32:33], v95 offset:0x400
	ds_read_b64_tr_b16 v[34:35], v95 offset:0xc00
	ds_read_b64_tr_b16 v[52:53], v95 offset:0x600
	ds_read_b64_tr_b16 v[54:55], v95 offset:0xe00
	s_waitcnt lgkmcnt(0)
	ds_read_b64_tr_b16 v[80:81], v64 offset:0x1000
	ds_read_b64_tr_b16 v[82:83], v64 offset:0x1800
	ds_read_b64_tr_b16 v[96:97], v95 offset:0x1000
	ds_read_b64_tr_b16 v[98:99], v95 offset:0x1800
	ds_read_b64_tr_b16 v[100:101], v95 offset:0x1200
	ds_read_b64_tr_b16 v[102:103], v95 offset:0x1a00
	ds_read_b64_tr_b16 v[104:105], v95 offset:0x1400
	ds_read_b64_tr_b16 v[106:107], v95 offset:0x1c00
	ds_read_b64_tr_b16 v[108:109], v95 offset:0x1600
	ds_read_b64_tr_b16 v[110:111], v95 offset:0x1e00
	s_waitcnt lgkmcnt(0)
	s_nop 0
	v_mfma_f32_32x32x16_bf16 v[0:15], v[48:51], v[0:3], 0
	v_mfma_f32_32x32x16_bf16 v[16:31], v[48:51], v[16:19], 0
	v_mfma_f32_32x32x16_bf16 v[32:47], v[48:51], v[32:35], 0
	v_mfma_f32_32x32x16_bf16 v[48:63], v[48:51], v[52:55], 0
	v_mfma_f32_32x32x16_bf16 v[0:15], v[80:83], v[96:99], v[0:15]
	ds_read_b64_tr_b16 v[96:97], v64 offset:0x2000
	ds_read_b64_tr_b16 v[98:99], v64 offset:0x2800
	v_mfma_f32_32x32x16_bf16 v[16:31], v[80:83], v[100:103], v[16:31]
	ds_read_b64_tr_b16 v[100:101], v95 offset:0x2000
	ds_read_b64_tr_b16 v[102:103], v95 offset:0x2800
	v_mfma_f32_32x32x16_bf16 v[32:47], v[80:83], v[104:107], v[32:47]
	ds_read_b64_tr_b16 v[104:105], v95 offset:0x2200
	ds_read_b64_tr_b16 v[106:107], v95 offset:0x2a00
	ds_read_b64_tr_b16 v[112:113], v95 offset:0x2400
	ds_read_b64_tr_b16 v[114:115], v95 offset:0x2c00
	ds_read_b64_tr_b16 v[116:117], v95 offset:0x2600
	ds_read_b64_tr_b16 v[118:119], v95 offset:0x2e00
	s_waitcnt lgkmcnt(0)
	v_mfma_f32_32x32x16_bf16 v[48:63], v[80:83], v[108:111], v[48:63]
	ds_read_b64_tr_b16 v[80:81], v64 offset:0x3000
	ds_read_b64_tr_b16 v[82:83], v64 offset:0x3800
	v_mfma_f32_32x32x16_bf16 v[0:15], v[96:99], v[100:103], v[0:15]
	ds_read_b64_tr_b16 v[100:101], v95 offset:0x3000
	ds_read_b64_tr_b16 v[102:103], v95 offset:0x3800
	v_mfma_f32_32x32x16_bf16 v[16:31], v[96:99], v[104:107], v[16:31]
	ds_read_b64_tr_b16 v[104:105], v95 offset:0x3200
	ds_read_b64_tr_b16 v[106:107], v95 offset:0x3a00
	ds_read_b64_tr_b16 v[108:109], v95 offset:0x3400
	ds_read_b64_tr_b16 v[110:111], v95 offset:0x3c00
	v_mfma_f32_32x32x16_bf16 v[32:47], v[96:99], v[112:115], v[32:47]
	ds_read_b64_tr_b16 v[112:113], v95 offset:0x3600
	ds_read_b64_tr_b16 v[114:115], v95 offset:0x3e00
	s_waitcnt lgkmcnt(0)
	v_mfma_f32_32x32x16_bf16 v[48:63], v[96:99], v[116:119], v[48:63]
	v_mfma_f32_32x32x16_bf16 v[0:15], v[80:83], v[100:103], v[0:15]
	s_mov_b32 s6, 0x53360000
	s_addk_i32 s9, 0x100
	v_lshl_add_u64 v[74:75], v[74:75], 0, s[86:87]
	v_lshl_add_u64 v[76:77], v[76:77], 0, s[86:87]
	v_add_u32_e32 v95, 0x4000, v95
	s_cmpk_eq_i32 s9, 0x400
	v_mfma_f32_32x32x16_bf16 v[16:31], v[80:83], v[104:107], v[16:31]
	v_mfma_f32_32x32x16_bf16 v[32:47], v[80:83], v[108:111], v[32:47]
	s_nop 10
	v_cvt_pk_bf16_f32 v0, v0, v16
	v_mfma_f32_32x32x16_bf16 v[48:63], v[80:83], v[112:115], v[48:63]
	v_lshl_add_u64 v[80:81], s[12:13], 0, v[78:79]
	v_add_co_u32_e64 v82, s[6:7], s6, v80
	s_nop 1
	v_addc_co_u32_e64 v83, s[6:7], 0, v81, s[6:7]
	s_mov_b32 s6, 0x53361000
	s_nop 5
	v_cvt_pk_bf16_f32 v16, v32, v48
	v_mov_b32_e32 v48, 0
	v_mov_b32_e32 v32, 0
	s_nop 0
	v_mov_b32_dpp v48, v16 quad_perm:[1,0,3,2] row_mask:0xf bank_mask:0xf
	v_mov_b32_dpp v32, v0 quad_perm:[1,0,3,2] row_mask:0xf bank_mask:0xf
	v_cndmask_b32_e32 v0, v48, v0, vcc
	v_cndmask_b32_e32 v16, v16, v32, vcc
	v_and_b32_e32 v32, 0xffff, v0
	v_lshrrev_b32_e32 v0, 16, v0
	v_and_or_b32 v0, v16, s17, v0
	v_lshl_or_b32 v32, v16, 16, v32
	global_store_dword v[82:83], v0, off offset:576 nt
	v_cvt_pk_bf16_f32 v0, v1, v17
	v_mov_b32_e32 v16, 0
	v_cvt_pk_bf16_f32 v1, v33, v49
	v_mov_b32_e32 v17, 0
	v_mov_b32_dpp v16, v0 quad_perm:[1,0,3,2] row_mask:0xf bank_mask:0xf
	global_store_dword v[82:83], v32, off offset:512 nt
	v_mov_b32_dpp v17, v1 quad_perm:[1,0,3,2] row_mask:0xf bank_mask:0xf
	v_cndmask_b32_e32 v1, v1, v16, vcc
	v_cndmask_b32_e32 v0, v17, v0, vcc
	v_lshlrev_b32_e32 v16, 16, v1
	v_and_or_b32 v16, v0, s0, v16
	v_lshrrev_b32_e32 v0, 16, v0
	v_and_or_b32 v0, v1, s17, v0
	global_store_dword v[82:83], v0, off offset:832 nt
	v_cvt_pk_bf16_f32 v0, v2, v18
	v_mov_b32_e32 v2, 0
	global_store_dword v[82:83], v16, off offset:768 nt
	v_cvt_pk_bf16_f32 v1, v34, v50
	v_mov_b32_dpp v2, v0 quad_perm:[1,0,3,2] row_mask:0xf bank_mask:0xf
	v_mov_b32_e32 v16, 0
	s_nop 1
	v_mov_b32_dpp v16, v1 quad_perm:[1,0,3,2] row_mask:0xf bank_mask:0xf
	v_cndmask_b32_e32 v1, v1, v2, vcc
	v_cndmask_b32_e32 v0, v16, v0, vcc
	v_lshlrev_b32_e32 v2, 16, v1
	v_and_or_b32 v2, v0, s0, v2
	v_lshrrev_b32_e32 v0, 16, v0
	v_and_or_b32 v0, v1, s17, v0
	global_store_dword v[82:83], v2, off offset:1024 nt
	global_store_dword v[82:83], v0, off offset:1088 nt
	v_cvt_pk_bf16_f32 v0, v3, v19
	v_mov_b32_e32 v2, 0
	v_cvt_pk_bf16_f32 v1, v35, v51
	v_mov_b32_e32 v3, 0
	v_mov_b32_dpp v2, v0 quad_perm:[1,0,3,2] row_mask:0xf bank_mask:0xf
	s_nop 0
	v_mov_b32_dpp v3, v1 quad_perm:[1,0,3,2] row_mask:0xf bank_mask:0xf
	v_cndmask_b32_e32 v1, v1, v2, vcc
	v_cndmask_b32_e32 v0, v3, v0, vcc
	v_lshlrev_b32_e32 v2, 16, v1
	v_and_or_b32 v2, v0, s0, v2
	v_lshrrev_b32_e32 v0, 16, v0
	v_and_or_b32 v0, v1, s17, v0
	global_store_dword v[82:83], v2, off offset:1280 nt
	global_store_dword v[82:83], v0, off offset:1344 nt
	v_cvt_pk_bf16_f32 v0, v4, v20
	v_mov_b32_e32 v2, 0
	v_cvt_pk_bf16_f32 v1, v36, v52
	v_mov_b32_e32 v3, 0
	v_mov_b32_dpp v2, v0 quad_perm:[1,0,3,2] row_mask:0xf bank_mask:0xf
	s_nop 0
	v_mov_b32_dpp v3, v1 quad_perm:[1,0,3,2] row_mask:0xf bank_mask:0xf
	v_cndmask_b32_e32 v1, v1, v2, vcc
	v_cndmask_b32_e32 v0, v3, v0, vcc
	v_lshlrev_b32_e32 v2, 16, v1
	v_and_or_b32 v2, v0, s0, v2
	v_lshrrev_b32_e32 v0, 16, v0
	v_and_or_b32 v0, v1, s17, v0
	global_store_dword v[82:83], v2, off offset:2560 nt
	global_store_dword v[82:83], v0, off offset:2624 nt
	v_cvt_pk_bf16_f32 v0, v5, v21
	v_mov_b32_e32 v2, 0
	v_cvt_pk_bf16_f32 v1, v37, v53
	v_mov_b32_e32 v3, 0
	v_mov_b32_dpp v2, v0 quad_perm:[1,0,3,2] row_mask:0xf bank_mask:0xf
	v_mov_b32_e32 v5, 0
	v_mov_b32_dpp v3, v1 quad_perm:[1,0,3,2] row_mask:0xf bank_mask:0xf
	v_cndmask_b32_e32 v1, v1, v2, vcc
	v_cndmask_b32_e32 v0, v3, v0, vcc
	v_lshlrev_b32_e32 v2, 16, v1
	v_and_or_b32 v2, v0, s0, v2
	v_lshrrev_b32_e32 v0, 16, v0
	v_and_or_b32 v0, v1, s17, v0
	global_store_dword v[82:83], v2, off offset:2816 nt
	global_store_dword v[82:83], v0, off offset:2880 nt
	v_cvt_pk_bf16_f32 v0, v6, v22
	v_mov_b32_e32 v2, 0
	v_cvt_pk_bf16_f32 v1, v38, v54
	v_mov_b32_e32 v3, 0
	v_mov_b32_dpp v2, v0 quad_perm:[1,0,3,2] row_mask:0xf bank_mask:0xf
	s_nop 0
	v_mov_b32_dpp v3, v1 quad_perm:[1,0,3,2] row_mask:0xf bank_mask:0xf
	v_cndmask_b32_e32 v1, v1, v2, vcc
	v_cndmask_b32_e32 v0, v3, v0, vcc
	v_lshlrev_b32_e32 v2, 16, v1
	v_and_or_b32 v2, v0, s0, v2
	v_lshrrev_b32_e32 v0, 16, v0
	v_and_or_b32 v0, v1, s17, v0
	global_store_dword v[82:83], v2, off offset:3072 nt
	global_store_dword v[82:83], v0, off offset:3136 nt
	v_cvt_pk_bf16_f32 v0, v7, v23
	v_mov_b32_e32 v2, 0
	v_cvt_pk_bf16_f32 v1, v39, v55
	v_mov_b32_e32 v3, 0
	v_mov_b32_dpp v2, v0 quad_perm:[1,0,3,2] row_mask:0xf bank_mask:0xf
	s_nop 0
	v_mov_b32_dpp v3, v1 quad_perm:[1,0,3,2] row_mask:0xf bank_mask:0xf
	v_cndmask_b32_e32 v1, v1, v2, vcc
	v_cndmask_b32_e32 v0, v3, v0, vcc
	v_lshlrev_b32_e32 v2, 16, v1
	v_and_or_b32 v2, v0, s0, v2
	v_lshrrev_b32_e32 v0, 16, v0
	v_and_or_b32 v0, v1, s17, v0
	global_store_dword v[82:83], v2, off offset:3328 nt
	global_store_dword v[82:83], v0, off offset:3392 nt
	v_cvt_pk_bf16_f32 v0, v8, v24
	v_mov_b32_e32 v2, 0
	v_cvt_pk_bf16_f32 v1, v40, v56
	v_mov_b32_e32 v3, 0
	v_mov_b32_dpp v2, v0 quad_perm:[1,0,3,2] row_mask:0xf bank_mask:0xf
	v_cndmask_b32_e32 v2, v1, v2, vcc
	v_mov_b32_dpp v3, v1 quad_perm:[1,0,3,2] row_mask:0xf bank_mask:0xf
	v_cndmask_b32_e32 v3, v3, v0, vcc
	v_lshlrev_b32_e32 v0, 16, v2
	v_and_or_b32 v4, v3, s0, v0
	v_add_co_u32_e64 v0, s[6:7], s6, v80
	v_lshrrev_b32_e32 v3, 16, v3
	s_nop 0
	v_addc_co_u32_e64 v1, s[6:7], 0, v81, s[6:7]
	v_and_or_b32 v2, v2, s17, v3
	global_store_dword v[0:1], v4, off offset:512 nt
	global_store_dword v[0:1], v2, off offset:576 nt
	v_cvt_pk_bf16_f32 v2, v9, v25
	v_mov_b32_e32 v4, 0
	v_cvt_pk_bf16_f32 v3, v41, v57
	s_mov_b64 s[6:7], 0x400000
	v_mov_b32_dpp v4, v2 quad_perm:[1,0,3,2] row_mask:0xf bank_mask:0xf
	v_mov_b32_dpp v5, v3 quad_perm:[1,0,3,2] row_mask:0xf bank_mask:0xf
	v_cndmask_b32_e32 v3, v3, v4, vcc
	v_cndmask_b32_e32 v2, v5, v2, vcc
	v_lshlrev_b32_e32 v4, 16, v3
	v_and_or_b32 v4, v2, s0, v4
	v_lshrrev_b32_e32 v2, 16, v2
	v_and_or_b32 v2, v3, s17, v2
	global_store_dword v[0:1], v4, off offset:768 nt
	global_store_dword v[0:1], v2, off offset:832 nt
	v_cvt_pk_bf16_f32 v2, v10, v26
	v_mov_b32_e32 v4, 0
	v_cvt_pk_bf16_f32 v3, v42, v58
	v_mov_b32_e32 v5, 0
	v_mov_b32_dpp v4, v2 quad_perm:[1,0,3,2] row_mask:0xf bank_mask:0xf
	v_lshl_add_u64 v[78:79], v[78:79], 0, s[6:7]
	v_mov_b32_dpp v5, v3 quad_perm:[1,0,3,2] row_mask:0xf bank_mask:0xf
	v_cndmask_b32_e32 v3, v3, v4, vcc
	v_cndmask_b32_e32 v2, v5, v2, vcc
	v_lshlrev_b32_e32 v4, 16, v3
	v_and_or_b32 v4, v2, s0, v4
	v_lshrrev_b32_e32 v2, 16, v2
	v_and_or_b32 v2, v3, s17, v2
	global_store_dword v[0:1], v4, off offset:1024 nt
	global_store_dword v[0:1], v2, off offset:1088 nt
	v_cvt_pk_bf16_f32 v2, v11, v27
	v_mov_b32_e32 v4, 0
	v_cvt_pk_bf16_f32 v3, v43, v59
	v_mov_b32_e32 v5, 0
	v_mov_b32_dpp v4, v2 quad_perm:[1,0,3,2] row_mask:0xf bank_mask:0xf
	s_nop 0
	v_mov_b32_dpp v5, v3 quad_perm:[1,0,3,2] row_mask:0xf bank_mask:0xf
	v_cndmask_b32_e32 v3, v3, v4, vcc
	v_cndmask_b32_e32 v2, v5, v2, vcc
	v_lshlrev_b32_e32 v4, 16, v3
	v_and_or_b32 v4, v2, s0, v4
	v_lshrrev_b32_e32 v2, 16, v2
	v_and_or_b32 v2, v3, s17, v2
	global_store_dword v[0:1], v4, off offset:1280 nt
	global_store_dword v[0:1], v2, off offset:1344 nt
	v_cvt_pk_bf16_f32 v2, v12, v28
	v_mov_b32_e32 v4, 0
	v_cvt_pk_bf16_f32 v3, v44, v60
	v_mov_b32_e32 v5, 0
	v_mov_b32_dpp v4, v2 quad_perm:[1,0,3,2] row_mask:0xf bank_mask:0xf
	s_nop 0
	v_mov_b32_dpp v5, v3 quad_perm:[1,0,3,2] row_mask:0xf bank_mask:0xf
	v_cndmask_b32_e32 v3, v3, v4, vcc
	v_cndmask_b32_e32 v2, v5, v2, vcc
	v_lshlrev_b32_e32 v4, 16, v3
	v_and_or_b32 v4, v2, s0, v4
	v_lshrrev_b32_e32 v2, 16, v2
	v_and_or_b32 v2, v3, s17, v2
	global_store_dword v[0:1], v4, off offset:2560 nt
	global_store_dword v[0:1], v2, off offset:2624 nt
	v_cvt_pk_bf16_f32 v2, v13, v29
	v_mov_b32_e32 v4, 0
	v_cvt_pk_bf16_f32 v3, v45, v61
	v_mov_b32_e32 v5, 0
	v_mov_b32_dpp v4, v2 quad_perm:[1,0,3,2] row_mask:0xf bank_mask:0xf
	s_nop 0
	v_mov_b32_dpp v5, v3 quad_perm:[1,0,3,2] row_mask:0xf bank_mask:0xf
	v_cndmask_b32_e32 v3, v3, v4, vcc
	v_cndmask_b32_e32 v2, v5, v2, vcc
	v_lshlrev_b32_e32 v4, 16, v3
	v_and_or_b32 v4, v2, s0, v4
	v_lshrrev_b32_e32 v2, 16, v2
	v_and_or_b32 v2, v3, s17, v2
	global_store_dword v[0:1], v4, off offset:2816 nt
	global_store_dword v[0:1], v2, off offset:2880 nt
	v_cvt_pk_bf16_f32 v2, v14, v30
	v_mov_b32_e32 v4, 0
	v_cvt_pk_bf16_f32 v3, v46, v62
	v_mov_b32_e32 v5, 0
	v_mov_b32_dpp v4, v2 quad_perm:[1,0,3,2] row_mask:0xf bank_mask:0xf
	s_nop 0
	v_mov_b32_dpp v5, v3 quad_perm:[1,0,3,2] row_mask:0xf bank_mask:0xf
	v_cndmask_b32_e32 v3, v3, v4, vcc
	v_cndmask_b32_e32 v2, v5, v2, vcc
	v_lshlrev_b32_e32 v4, 16, v3
	v_and_or_b32 v4, v2, s0, v4
	v_lshrrev_b32_e32 v2, 16, v2
	v_and_or_b32 v2, v3, s17, v2
	global_store_dword v[0:1], v4, off offset:3072 nt
	global_store_dword v[0:1], v2, off offset:3136 nt
	v_cvt_pk_bf16_f32 v2, v15, v31
	v_mov_b32_e32 v4, 0
	v_cvt_pk_bf16_f32 v3, v47, v63
	v_mov_b32_e32 v5, 0
	v_mov_b32_dpp v4, v2 quad_perm:[1,0,3,2] row_mask:0xf bank_mask:0xf
	s_nop 0
	v_mov_b32_dpp v5, v3 quad_perm:[1,0,3,2] row_mask:0xf bank_mask:0xf
	v_cndmask_b32_e32 v3, v3, v4, vcc
	v_cndmask_b32_e32 v2, v5, v2, vcc
	v_lshlrev_b32_e32 v4, 16, v3
	v_and_or_b32 v4, v2, s0, v4
	v_lshrrev_b32_e32 v2, 16, v2
	v_and_or_b32 v2, v3, s17, v2
	global_store_dword v[0:1], v4, off offset:3328 nt
	global_store_dword v[0:1], v2, off offset:3392 nt
	s_barrier
	s_cbranch_scc0 .LBB0_1799
	v_ashrrev_i32_e32 v24, 6, v70
	s_lshl_b64 s[94:95], s[18:19], 6
	v_readfirstlane_b32 s8, v24
	s_cmp_gt_i32 s8, 5
	s_cselect_b64 s[96:97], -1, 0
	s_cmp_lt_i32 s8, 6
	s_cselect_b32 s7, s21, s23
	s_cselect_b32 s6, s20, s22
	v_lshlrev_b32_e32 v4, 5, v66
	global_load_dwordx4 v[0:3], v4, s[6:7] offset:512
	s_nop 0
	global_load_dwordx4 v[4:7], v4, s[6:7] offset:528
	v_and_b32_e32 v8, 4, v70
	v_cmp_eq_u32_e64 s[6:7], 0, v8
	v_xor_b32_e32 v8, 1, v254
	v_add_u32_e32 v9, 64, v71
	v_cmp_lt_i32_e32 vcc, v8, v9
	s_lshl_b32 s10, s8, 7
	s_mov_b32 s78, s10
	v_cndmask_b32_e32 v8, v254, v8, vcc
	v_lshlrev_b32_e32 v25, 2, v8
	v_xor_b32_e32 v8, 2, v254
	v_cmp_lt_i32_e32 vcc, v8, v9
	s_ashr_i32 s11, s10, 31
	s_lshl_b64 s[28:29], s[78:79], 1
	v_cndmask_b32_e32 v8, v254, v8, vcc
	v_lshlrev_b32_e32 v74, 2, v8
	v_xor_b32_e32 v8, 4, v254
	v_cmp_lt_i32_e32 vcc, v8, v9
	v_bfe_u32 v28, v70, 4, 2
	v_mov_b32_e32 v29, v65
	v_cndmask_b32_e32 v8, v254, v8, vcc
	v_lshlrev_b32_e32 v75, 2, v8
	v_xor_b32_e32 v8, 8, v254
	v_cmp_lt_i32_e32 vcc, v8, v9
	s_add_u32 s28, s12, s28
	v_mov_b64_e32 v[10:11], s[70:71]
	v_cndmask_b32_e32 v8, v254, v8, vcc
	v_lshlrev_b32_e32 v76, 2, v8
	v_lshl_add_u64 v[8:9], s[72:73], 0, v[28:29]
	s_addc_u32 s29, s13, s29
	s_lshl_b64 s[50:51], s[10:11], 1
	v_mad_u64_u32 v[34:35], s[10:11], v8, s1, v[10:11]
	v_mov_b32_e32 v12, v35
	v_mad_u64_u32 v[12:13], s[10:11], v9, s1, v[12:13]
	v_lshlrev_b64 v[8:9], 13, v[8:9]
	v_or_b32_e32 v8, v8, v72
	v_lshl_add_u64 v[36:37], s[36:37], 0, v[8:9]
	v_lshl_add_u64 v[8:9], s[74:75], 0, v[28:29]
	v_mad_u64_u32 v[38:39], s[10:11], v8, s1, v[10:11]
	v_mov_b32_e32 v35, v12
	v_mov_b32_e32 v12, v39
	v_mad_u64_u32 v[12:13], s[10:11], v9, s1, v[12:13]
	v_lshlrev_b64 v[8:9], 13, v[8:9]
	v_or_b32_e32 v8, v8, v72
	v_lshl_add_u64 v[40:41], s[36:37], 0, v[8:9]
	v_lshl_add_u64 v[8:9], s[76:77], 0, v[28:29]
	v_mad_u64_u32 v[42:43], s[10:11], v8, s1, v[10:11]
	v_mov_b32_e32 v39, v12
	v_mov_b32_e32 v12, v43
	v_mad_u64_u32 v[12:13], s[10:11], v9, s1, v[12:13]
	v_lshlrev_b64 v[8:9], 13, v[8:9]
	v_or_b32_e32 v8, v8, v72
	v_lshl_add_u64 v[44:45], s[36:37], 0, v[8:9]
	v_lshl_add_u64 v[8:9], s[64:65], 0, v[28:29]
	v_mad_u64_u32 v[46:47], s[10:11], v8, s1, v[10:11]
	v_mov_b32_e32 v10, v47
	v_mad_u64_u32 v[10:11], s[10:11], v9, s1, v[10:11]
	v_lshlrev_b64 v[8:9], 13, v[8:9]
	v_lshrrev_b32_e32 v27, 4, v68
	v_and_b32_e32 v64, 0x60, v73
	v_or_b32_e32 v8, v8, v72
	v_lshlrev_b32_e32 v26, 3, v66
	s_mov_b32 s19, 0
	v_cmp_gt_u32_e64 s[8:9], 8, v66
	v_lshl_add_u64 v[30:31], s[34:35], 0, v[64:65]
	v_lshl_add_u64 v[32:33], s[42:43], 0, v[64:65]
	v_or_b32_e32 v77, 4, v27
	v_or_b32_e32 v78, 8, v27
	v_or_b32_e32 v79, 12, v27
	v_mov_b32_e32 v43, v12
	v_mov_b32_e32 v47, v10
	v_lshl_add_u64 v[48:49], s[36:37], 0, v[8:9]
	s_mov_b32 s78, 0
	s_branch .LBB0_1802
.LBB0_1801:
	s_waitcnt vmcnt(0) lgkmcnt(6)
	v_pk_mul_f32 v[20:21], v[20:21], v[72:73]
	s_waitcnt lgkmcnt(2)
	v_pk_mul_f32 v[12:13], v[12:13], v[60:61]
	v_cndmask_b32_e64 v21, v21, -v21, s[6:7]
	v_cndmask_b32_e64 v20, v20, -v20, s[6:7]
	v_cndmask_b32_e64 v13, v13, -v13, s[6:7]
	v_cndmask_b32_e64 v12, v12, -v12, s[6:7]
	v_pk_fma_f32 v[16:17], v[16:17], v[70:71], v[20:21]
	v_pk_mul_f32 v[20:21], v[22:23], v[62:63]
	v_pk_fma_f32 v[12:13], v[8:9], v[54:55], v[12:13]
	s_waitcnt lgkmcnt(0)
	v_pk_mul_f32 v[8:9], v[14:15], v[56:57]
	v_cndmask_b32_e64 v21, v21, -v21, s[6:7]
	v_cndmask_b32_e64 v20, v20, -v20, s[6:7]
	v_cndmask_b32_e64 v9, v9, -v9, s[6:7]
	v_cndmask_b32_e64 v8, v8, -v8, s[6:7]
	v_pk_fma_f32 v[18:19], v[18:19], v[58:59], v[20:21]
	v_pk_fma_f32 v[14:15], v[10:11], v[50:51], v[8:9]
	s_add_i32 s78, s78, 4
	s_add_i32 s19, s19, 16
	v_cvt_pk_bf16_f32 v8, v16, v17
	v_cvt_pk_bf16_f32 v9, v18, v19
	v_cvt_pk_bf16_f32 v10, v12, v13
	v_cvt_pk_bf16_f32 v11, v14, v15
	v_lshl_add_u64 v[12:13], v[52:53], 0, v[64:65]
	v_lshl_add_u64 v[34:35], v[34:35], 0, s[90:91]
	v_lshl_add_u64 v[36:37], v[36:37], 0, s[82:83]
	v_lshl_add_u64 v[38:39], v[38:39], 0, s[90:91]
	v_lshl_add_u64 v[40:41], v[40:41], 0, s[82:83]
	v_lshl_add_u64 v[42:43], v[42:43], 0, s[90:91]
	v_lshl_add_u64 v[44:45], v[44:45], 0, s[82:83]
	v_lshl_add_u64 v[46:47], v[46:47], 0, s[90:91]
	s_cmp_eq_u32 s19, 64
	v_lshl_add_u64 v[48:49], v[48:49], 0, s[82:83]
	global_store_dwordx4 v[12:13], v[8:11], off nt
	s_cbranch_scc1 .LBB0_1818

.LBB0_1806:
	s_waitcnt vmcnt(0) lgkmcnt(6)
	v_pk_mul_f32 v[20:21], v[20:21], v[72:73]
	s_waitcnt lgkmcnt(2)
	v_pk_mul_f32 v[12:13], v[12:13], v[60:61]
	v_cndmask_b32_e64 v21, v21, -v21, s[6:7]
	v_cndmask_b32_e64 v20, v20, -v20, s[6:7]
	v_cndmask_b32_e64 v13, v13, -v13, s[6:7]
	v_cndmask_b32_e64 v12, v12, -v12, s[6:7]
	v_pk_fma_f32 v[16:17], v[16:17], v[70:71], v[20:21]
	v_pk_mul_f32 v[20:21], v[22:23], v[62:63]
	v_pk_fma_f32 v[12:13], v[8:9], v[54:55], v[12:13]
	s_waitcnt lgkmcnt(0)
	v_pk_mul_f32 v[8:9], v[14:15], v[56:57]
	v_cndmask_b32_e64 v21, v21, -v21, s[6:7]
	v_cndmask_b32_e64 v20, v20, -v20, s[6:7]
	v_cndmask_b32_e64 v9, v9, -v9, s[6:7]
	v_cndmask_b32_e64 v8, v8, -v8, s[6:7]
	v_pk_fma_f32 v[18:19], v[18:19], v[58:59], v[20:21]
	v_pk_fma_f32 v[14:15], v[10:11], v[50:51], v[8:9]
	v_lshlrev_b32_e32 v64, 1, v26
	v_cvt_pk_bf16_f32 v8, v16, v17
	v_cvt_pk_bf16_f32 v9, v18, v19
	v_cvt_pk_bf16_f32 v10, v12, v13
	v_cvt_pk_bf16_f32 v11, v14, v15
	v_lshl_add_u64 v[12:13], v[52:53], 0, v[64:65]
	global_store_dwordx4 v[12:13], v[8:11], off nt
	s_mov_b64 s[30:31], -1
	s_nop 0
	v_lshl_add_u64 v[8:9], v[44:45], 0, s[50:51]
	global_load_dwordx4 v[50:53], v[8:9], off
	v_add_u32_e32 v8, 4, v29
	v_mov_b32_e32 v10, s16
	v_cndmask_b32_e64 v8, v8, v10, s[8:9]
	v_mov_b32_e32 v9, v65
	v_lshlrev_b32_e32 v8, 5, v8
	v_lshlrev_b64 v[8:9], 2, v[8:9]
	v_lshl_add_u64 v[12:13], v[30:31], 0, v[8:9]
	v_lshl_add_u64 v[20:21], v[32:33], 0, v[8:9]
	global_load_dwordx4 v[8:11], v[12:13], off offset:16
	global_load_dwordx4 v[16:19], v[12:13], off
	s_nop 0
	global_load_dwordx4 v[12:15], v[20:21], off offset:16
	s_nop 0
	global_load_dwordx4 v[20:23], v[20:21], off
	s_waitcnt vmcnt(4)
	v_lshlrev_b32_e32 v58, 16, v50
	v_and_b32_e32 v59, 0xffff0000, v50
	v_lshlrev_b32_e32 v54, 16, v53
	v_and_b32_e32 v55, 0xffff0000, v53
	v_lshlrev_b32_e32 v56, 16, v52
	v_and_b32_e32 v57, 0xffff0000, v52
	v_lshlrev_b32_e32 v52, 16, v51
	v_and_b32_e32 v53, 0xffff0000, v51
	v_pk_mul_f32 v[70:71], v[58:59], v[58:59]
	v_pk_mul_f32 v[62:63], v[52:53], v[52:53]
	v_add_f32_e32 v70, v70, v71
	v_add_f32_e32 v62, v62, v70
	v_pk_mul_f32 v[60:61], v[56:57], v[56:57]
	v_add_f32_e32 v62, v63, v62
	v_add_f32_e32 v60, v60, v62
	v_pk_mul_f32 v[50:51], v[54:55], v[54:55]
	v_add_f32_e32 v60, v61, v60
	v_add_f32_e32 v50, v50, v60
	v_add_f32_e32 v50, v51, v50
	ds_bpermute_b32 v51, v25, v50
	s_waitcnt lgkmcnt(0)
	v_add_f32_e32 v50, v50, v51
	ds_bpermute_b32 v51, v74, v50
	s_waitcnt lgkmcnt(0)
	v_add_f32_e32 v50, v50, v51
	ds_bpermute_b32 v51, v75, v50
	s_waitcnt lgkmcnt(0)
	v_add_f32_e32 v50, v50, v51
	ds_bpermute_b32 v51, v76, v50
	s_waitcnt lgkmcnt(0)
	v_add_f32_e32 v50, v50, v51
	v_fmamk_f32 v50, v50, 0x3c000000, v85
	v_mul_f32_e32 v51, 0x4b800000, v50
	v_cmp_gt_f32_e32 vcc, s81, v50
	s_nop 1
	v_cndmask_b32_e32 v50, v50, v51, vcc
	v_rsq_f32_e32 v50, v50
	s_nop 0
	v_mul_f32_e32 v51, 0x45800000, v50
	v_cndmask_b32_e32 v50, v50, v51, vcc
	v_pk_mul_f32 v[60:61], v[0:1], v[50:51] op_sel_hi:[1,0]
	v_pk_mul_f32 v[62:63], v[2:3], v[50:51] op_sel_hi:[1,0]
	v_pk_mul_f32 v[72:73], v[4:5], v[50:51] op_sel_hi:[1,0]
	v_pk_mul_f32 v[50:51], v[6:7], v[50:51] op_sel_hi:[1,0]
	v_pk_mul_f32 v[70:71], v[60:61], v[58:59]
	v_pk_mul_f32 v[58:59], v[62:63], v[52:53]
	v_pk_mul_f32 v[52:53], v[72:73], v[56:57]
	v_pk_mul_f32 v[50:51], v[50:51], v[54:55]
	ds_bpermute_b32 v72, v75, v70
	ds_bpermute_b32 v73, v75, v71
	ds_bpermute_b32 v62, v75, v58
	ds_bpermute_b32 v63, v75, v59
	ds_bpermute_b32 v60, v75, v52
	ds_bpermute_b32 v61, v75, v53
	ds_bpermute_b32 v56, v75, v50
	ds_bpermute_b32 v57, v75, v51
	v_cndmask_b32_e64 v54, 0, 1, s[96:97]
	v_cmp_ne_u32_e64 s[10:11], 1, v54
	s_andn2_b64 vcc, exec, s[96:97]
	s_cbranch_vccnz .LBB0_1808
	v_or_b32_e32 v54, s84, v77
	v_or_b32_e32 v54, s94, v54
	v_mov_b32_e32 v55, s95
	v_lshlrev_b64 v[54:55], 9, v[54:55]
	v_lshl_add_u64 v[54:55], s[28:29], 0, v[54:55]
	v_lshl_add_u64 v[54:55], v[54:55], 0, s[88:89]
	s_mov_b64 s[30:31], 0

.LBB0_1810:
	s_waitcnt vmcnt(0) lgkmcnt(6)
	v_pk_mul_f32 v[20:21], v[20:21], v[72:73]
	s_waitcnt lgkmcnt(2)
	v_pk_mul_f32 v[12:13], v[12:13], v[60:61]
	v_cndmask_b32_e64 v21, v21, -v21, s[6:7]
	v_cndmask_b32_e64 v20, v20, -v20, s[6:7]
	v_cndmask_b32_e64 v13, v13, -v13, s[6:7]
	v_cndmask_b32_e64 v12, v12, -v12, s[6:7]
	v_pk_fma_f32 v[16:17], v[16:17], v[70:71], v[20:21]
	v_pk_mul_f32 v[20:21], v[22:23], v[62:63]
	v_pk_fma_f32 v[12:13], v[8:9], v[52:53], v[12:13]
	s_waitcnt lgkmcnt(0)
	v_pk_mul_f32 v[8:9], v[14:15], v[56:57]
	v_cndmask_b32_e64 v21, v21, -v21, s[6:7]
	v_cndmask_b32_e64 v20, v20, -v20, s[6:7]
	v_cndmask_b32_e64 v9, v9, -v9, s[6:7]
	v_cndmask_b32_e64 v8, v8, -v8, s[6:7]
	v_pk_fma_f32 v[18:19], v[18:19], v[58:59], v[20:21]
	v_pk_fma_f32 v[14:15], v[10:11], v[50:51], v[8:9]
	v_cvt_pk_bf16_f32 v8, v16, v17
	v_cvt_pk_bf16_f32 v9, v18, v19
	v_cvt_pk_bf16_f32 v10, v12, v13
	v_cvt_pk_bf16_f32 v11, v14, v15
	v_lshl_add_u64 v[12:13], v[54:55], 0, v[64:65]
	global_store_dwordx4 v[12:13], v[8:11], off nt
	s_mov_b64 s[30:31], -1
	s_nop 0
	v_lshl_add_u64 v[8:9], v[40:41], 0, s[50:51]
	global_load_dwordx4 v[50:53], v[8:9], off
	v_add_u32_e32 v8, 8, v29
	v_mov_b32_e32 v10, s16
	v_cndmask_b32_e64 v8, v8, v10, s[8:9]
	v_mov_b32_e32 v9, v65
	v_lshlrev_b32_e32 v8, 5, v8
	v_lshlrev_b64 v[8:9], 2, v[8:9]
	v_lshl_add_u64 v[12:13], v[30:31], 0, v[8:9]
	v_lshl_add_u64 v[20:21], v[32:33], 0, v[8:9]
	global_load_dwordx4 v[8:11], v[12:13], off offset:16
	global_load_dwordx4 v[16:19], v[12:13], off
	s_nop 0
	global_load_dwordx4 v[12:15], v[20:21], off offset:16
	s_nop 0
	global_load_dwordx4 v[20:23], v[20:21], off
	s_waitcnt vmcnt(4)
	v_lshlrev_b32_e32 v58, 16, v50
	v_and_b32_e32 v59, 0xffff0000, v50
	v_lshlrev_b32_e32 v56, 16, v53
	v_and_b32_e32 v57, 0xffff0000, v53
	v_lshlrev_b32_e32 v54, 16, v52
	v_and_b32_e32 v55, 0xffff0000, v52
	v_lshlrev_b32_e32 v52, 16, v51
	v_and_b32_e32 v53, 0xffff0000, v51
	v_pk_mul_f32 v[70:71], v[58:59], v[58:59]
	v_pk_mul_f32 v[62:63], v[52:53], v[52:53]
	v_add_f32_e32 v70, v70, v71
	v_add_f32_e32 v62, v62, v70
	v_pk_mul_f32 v[60:61], v[54:55], v[54:55]
	v_add_f32_e32 v62, v63, v62
	v_add_f32_e32 v60, v60, v62
	v_pk_mul_f32 v[50:51], v[56:57], v[56:57]
	v_add_f32_e32 v60, v61, v60
	v_add_f32_e32 v50, v50, v60
	v_add_f32_e32 v50, v51, v50
	ds_bpermute_b32 v51, v25, v50
	s_waitcnt lgkmcnt(0)
	v_add_f32_e32 v50, v50, v51
	ds_bpermute_b32 v51, v74, v50
	s_waitcnt lgkmcnt(0)
	v_add_f32_e32 v50, v50, v51
	ds_bpermute_b32 v51, v75, v50
	s_waitcnt lgkmcnt(0)
	v_add_f32_e32 v50, v50, v51
	ds_bpermute_b32 v51, v76, v50
	s_waitcnt lgkmcnt(0)
	v_add_f32_e32 v50, v50, v51
	v_fmamk_f32 v50, v50, 0x3c000000, v85
	v_mul_f32_e32 v51, 0x4b800000, v50
	v_cmp_gt_f32_e32 vcc, s81, v50
	s_nop 1
	v_cndmask_b32_e32 v50, v50, v51, vcc
	v_rsq_f32_e32 v50, v50
	s_nop 0
	v_mul_f32_e32 v51, 0x45800000, v50
	v_cndmask_b32_e32 v50, v50, v51, vcc
	v_pk_mul_f32 v[60:61], v[0:1], v[50:51] op_sel_hi:[1,0]
	v_pk_mul_f32 v[62:63], v[2:3], v[50:51] op_sel_hi:[1,0]
	v_pk_mul_f32 v[72:73], v[4:5], v[50:51] op_sel_hi:[1,0]
	v_pk_mul_f32 v[50:51], v[6:7], v[50:51] op_sel_hi:[1,0]
	v_pk_mul_f32 v[70:71], v[60:61], v[58:59]
	v_pk_mul_f32 v[58:59], v[62:63], v[52:53]
	v_pk_mul_f32 v[54:55], v[72:73], v[54:55]
	v_pk_mul_f32 v[50:51], v[50:51], v[56:57]
	ds_bpermute_b32 v72, v75, v70
	ds_bpermute_b32 v73, v75, v71
	ds_bpermute_b32 v62, v75, v58
	ds_bpermute_b32 v63, v75, v59
	ds_bpermute_b32 v60, v75, v54
	ds_bpermute_b32 v61, v75, v55
	ds_bpermute_b32 v56, v75, v50
	ds_bpermute_b32 v57, v75, v51
	s_and_b64 vcc, exec, s[10:11]
	s_cbranch_vccnz .LBB0_1812
	v_or_b32_e32 v52, s84, v78
	v_or_b32_e32 v52, s94, v52
	v_mov_b32_e32 v53, s95
	v_lshlrev_b64 v[52:53], 9, v[52:53]
	v_lshl_add_u64 v[52:53], s[28:29], 0, v[52:53]
	v_lshl_add_u64 v[52:53], v[52:53], 0, s[88:89]
	s_mov_b64 s[30:31], 0

.LBB0_1814:
	s_waitcnt vmcnt(0) lgkmcnt(6)
	v_pk_mul_f32 v[20:21], v[20:21], v[72:73]
	s_waitcnt lgkmcnt(2)
	v_pk_mul_f32 v[12:13], v[12:13], v[60:61]
	v_cndmask_b32_e64 v21, v21, -v21, s[6:7]
	v_cndmask_b32_e64 v20, v20, -v20, s[6:7]
	v_cndmask_b32_e64 v13, v13, -v13, s[6:7]
	v_cndmask_b32_e64 v12, v12, -v12, s[6:7]
	v_pk_fma_f32 v[16:17], v[16:17], v[70:71], v[20:21]
	v_pk_mul_f32 v[20:21], v[22:23], v[62:63]
	v_pk_fma_f32 v[12:13], v[8:9], v[54:55], v[12:13]
	s_waitcnt lgkmcnt(0)
	v_pk_mul_f32 v[8:9], v[14:15], v[56:57]
	v_cndmask_b32_e64 v21, v21, -v21, s[6:7]
	v_cndmask_b32_e64 v20, v20, -v20, s[6:7]
	v_cndmask_b32_e64 v9, v9, -v9, s[6:7]
	v_cndmask_b32_e64 v8, v8, -v8, s[6:7]
	v_pk_fma_f32 v[18:19], v[18:19], v[58:59], v[20:21]
	v_pk_fma_f32 v[14:15], v[10:11], v[50:51], v[8:9]
	v_cvt_pk_bf16_f32 v8, v16, v17
	v_cvt_pk_bf16_f32 v9, v18, v19
	v_cvt_pk_bf16_f32 v10, v12, v13
	v_cvt_pk_bf16_f32 v11, v14, v15
	v_lshl_add_u64 v[12:13], v[52:53], 0, v[64:65]
	global_store_dwordx4 v[12:13], v[8:11], off nt
	s_nop 1
	v_lshl_add_u64 v[8:9], v[36:37], 0, s[50:51]
	global_load_dwordx4 v[50:53], v[8:9], off
	v_add_u32_e32 v8, 12, v29
	v_mov_b32_e32 v10, s16
	v_cndmask_b32_e64 v8, v8, v10, s[8:9]
	v_mov_b32_e32 v9, v65
	v_lshlrev_b32_e32 v8, 5, v8
	v_lshlrev_b64 v[8:9], 2, v[8:9]
	v_lshl_add_u64 v[12:13], v[30:31], 0, v[8:9]
	v_lshl_add_u64 v[20:21], v[32:33], 0, v[8:9]
	global_load_dwordx4 v[8:11], v[12:13], off offset:16
	global_load_dwordx4 v[16:19], v[12:13], off
	s_nop 0
	global_load_dwordx4 v[12:15], v[20:21], off offset:16
	s_nop 0
	global_load_dwordx4 v[20:23], v[20:21], off
	s_waitcnt vmcnt(4)
	v_lshlrev_b32_e32 v58, 16, v50
	v_and_b32_e32 v59, 0xffff0000, v50
	v_lshlrev_b32_e32 v56, 16, v53
	v_and_b32_e32 v57, 0xffff0000, v53
	v_lshlrev_b32_e32 v54, 16, v52
	v_and_b32_e32 v55, 0xffff0000, v52
	v_lshlrev_b32_e32 v52, 16, v51
	v_and_b32_e32 v53, 0xffff0000, v51
	v_pk_mul_f32 v[70:71], v[58:59], v[58:59]
	v_pk_mul_f32 v[62:63], v[52:53], v[52:53]
	v_add_f32_e32 v29, v70, v71
	v_add_f32_e32 v29, v62, v29
	v_pk_mul_f32 v[60:61], v[54:55], v[54:55]
	v_add_f32_e32 v29, v63, v29
	v_add_f32_e32 v29, v60, v29
	v_pk_mul_f32 v[50:51], v[56:57], v[56:57]
	v_add_f32_e32 v29, v61, v29
	v_add_f32_e32 v29, v50, v29
	v_add_f32_e32 v29, v51, v29
	ds_bpermute_b32 v50, v25, v29
	s_waitcnt lgkmcnt(0)
	v_add_f32_e32 v29, v29, v50
	ds_bpermute_b32 v50, v74, v29
	s_waitcnt lgkmcnt(0)
	v_add_f32_e32 v29, v29, v50
	ds_bpermute_b32 v50, v75, v29
	s_waitcnt lgkmcnt(0)
	v_add_f32_e32 v29, v29, v50
	ds_bpermute_b32 v50, v76, v29
	s_waitcnt lgkmcnt(0)
	v_add_f32_e32 v29, v29, v50
	v_fmamk_f32 v29, v29, 0x3c000000, v85
	v_mul_f32_e32 v50, 0x4b800000, v29
	v_cmp_gt_f32_e32 vcc, s81, v29
	s_nop 1
	v_cndmask_b32_e32 v29, v29, v50, vcc
	v_rsq_f32_e32 v29, v29
	s_nop 0
	v_mul_f32_e32 v50, 0x45800000, v29
	v_cndmask_b32_e32 v50, v29, v50, vcc
	v_pk_mul_f32 v[60:61], v[0:1], v[50:51] op_sel_hi:[1,0]
	v_pk_mul_f32 v[62:63], v[2:3], v[50:51] op_sel_hi:[1,0]
	v_pk_mul_f32 v[72:73], v[4:5], v[50:51] op_sel_hi:[1,0]
	v_pk_mul_f32 v[50:51], v[6:7], v[50:51] op_sel_hi:[1,0]
	v_pk_mul_f32 v[70:71], v[60:61], v[58:59]
	v_pk_mul_f32 v[58:59], v[62:63], v[52:53]
	v_pk_mul_f32 v[54:55], v[72:73], v[54:55]
	v_pk_mul_f32 v[50:51], v[50:51], v[56:57]
	ds_bpermute_b32 v72, v75, v70
	ds_bpermute_b32 v73, v75, v71
	ds_bpermute_b32 v62, v75, v58
	ds_bpermute_b32 v63, v75, v59
	ds_bpermute_b32 v60, v75, v54
	ds_bpermute_b32 v61, v75, v55
	ds_bpermute_b32 v56, v75, v50
	ds_bpermute_b32 v57, v75, v51
	s_and_b64 vcc, exec, s[10:11]
	s_mov_b64 s[10:11], -1
	s_cbranch_vccnz .LBB0_1816
	v_or_b32_e32 v29, s84, v79
	v_or_b32_e32 v52, s94, v29
	v_mov_b32_e32 v53, s95
	v_lshlrev_b64 v[52:53], 9, v[52:53]
	v_lshl_add_u64 v[52:53], s[28:29], 0, v[52:53]
	v_lshl_add_u64 v[52:53], v[52:53], 0, s[88:89]
	s_mov_b64 s[10:11], 0

.LBB0_1821:
	v_lshl_add_u64 v[20:21], s[12:13], 0, v[18:19]
	global_load_dword v23, v[20:21], off offset:-768
	global_load_dword v25, v[20:21], off offset:-512
	global_load_dword v29, v[20:21], off offset:-256
	v_mov_b32_e32 v36, v65
	v_mov_b32_e32 v37, v65
	s_waitcnt vmcnt(2)
	v_lshlrev_b32_e32 v22, 16, v23
	v_and_b32_e32 v23, 0xffff0000, v23
	s_waitcnt vmcnt(0)
	v_lshlrev_b32_e32 v28, 16, v29
	v_and_b32_e32 v29, 0xffff0000, v29
	v_lshlrev_b32_e32 v26, 16, v25
	v_and_b32_e32 v27, 0xffff0000, v25
	v_mov_b32_e32 v34, v23
	v_mov_b32_e32 v35, v29
	v_pk_mul_f32 v[30:31], v[26:27], v[26:27]
	v_mov_b32_e32 v32, v22
	v_mov_b32_e32 v33, v28
	v_pk_mul_f32 v[34:35], v[34:35], v[34:35]
	v_add_f32_e32 v25, v30, v31
	v_pk_fma_f32 v[30:31], v[32:33], v[32:33], v[34:35]
	s_nop 0
	v_add_f32_e32 v25, v30, v25
	v_add_f32_e32 v25, v25, v31
	s_nop 1
	v_add_f32_dpp v25, v25, v25 quad_perm:[1,0,3,2] row_mask:0xf bank_mask:0xf bound_ctrl:1
	s_nop 1
	v_add_f32_dpp v25, v25, v25 quad_perm:[2,3,0,1] row_mask:0xf bank_mask:0xf bound_ctrl:1
	s_nop 1
	v_add_f32_dpp v25, v25, v25 row_half_mirror row_mask:0xf bank_mask:0xf bound_ctrl:1
	s_nop 1
	v_add_f32_dpp v25, v25, v25 row_mirror row_mask:0xf bank_mask:0xf bound_ctrl:1
	s_nop 1
	v_mov_b32_dpp v36, v25 row_bcast:15 row_mask:0xa bank_mask:0xf
	v_add_f32_e32 v25, v25, v36
	s_nop 1
	v_mov_b32_dpp v37, v25 row_bcast:31 row_mask:0xc bank_mask:0xf
	v_add_f32_e32 v25, v25, v37
	s_nop 0
	v_readlane_b32 s6, v25, 63
	s_nop 1
	v_fma_f32 v25, s6, v89, v85
	v_mul_f32_e32 v30, 0x4b800000, v25
	v_cmp_gt_f32_e32 vcc, s81, v25
	s_nop 1
	v_cndmask_b32_e32 v25, v25, v30, vcc
	v_rsq_f32_e32 v25, v25
	v_lshl_add_u64 v[30:31], s[12:13], 0, v[16:17]
	v_mul_f32_e32 v32, 0x45800000, v25
	v_cndmask_b32_e32 v32, v25, v32, vcc
	v_pk_mul_f32 v[22:23], v[32:33], v[22:23] op_sel_hi:[0,1]
	v_pk_mul_f32 v[26:27], v[32:33], v[26:27] op_sel_hi:[0,1]
	v_pk_mul_f32 v[28:29], v[32:33], v[28:29] op_sel_hi:[0,1]
	v_pk_mul_f32 v[22:23], v[2:3], v[22:23]
	v_pk_mul_f32 v[26:27], v[4:5], v[26:27]
	v_pk_mul_f32 v[28:29], v[0:1], v[28:29]
	v_cvt_pk_bf16_f32 v22, v22, v23
	v_cvt_pk_bf16_f32 v23, v26, v27
	v_cvt_pk_bf16_f32 v25, v28, v29
	global_store_dword v[30:31], v22, off offset:-256 nt
	global_store_dword v[30:31], v23, off nt
	global_store_dword v[30:31], v25, off offset:256 nt
	global_load_dword v23, v[20:21], off
	s_nop 0
	global_load_dword v25, v[20:21], off offset:256
	v_mov_b32_e32 v32, v65
	v_mov_b32_e32 v33, v65
	v_lshl_add_u64 v[20:21], s[12:13], 0, v[12:13]
	v_add_co_u32_e32 v20, vcc, 0x4b160000, v20
	s_waitcnt vmcnt(1)
	v_lshlrev_b32_e32 v22, 16, v23
	v_and_b32_e32 v23, 0xffff0000, v23
	s_waitcnt vmcnt(0)
	v_and_b32_e32 v27, 0xffff0000, v25
	v_lshlrev_b32_e32 v26, 16, v25
	v_mov_b32_e32 v30, v23
	v_mov_b32_e32 v31, v27
	v_mov_b32_e32 v28, v22
	v_mov_b32_e32 v29, v26
	v_pk_mul_f32 v[30:31], v[30:31], v[30:31]
	v_addc_co_u32_e32 v21, vcc, 0, v21, vcc
	v_pk_fma_f32 v[28:29], v[28:29], v[28:29], v[30:31]
	s_nop 0
	v_add_f32_e32 v25, v28, v29
	s_nop 1
	v_add_f32_dpp v25, v25, v25 quad_perm:[1,0,3,2] row_mask:0xf bank_mask:0xf bound_ctrl:1
	s_nop 1
	v_add_f32_dpp v25, v25, v25 quad_perm:[2,3,0,1] row_mask:0xf bank_mask:0xf bound_ctrl:1
	s_nop 1
	v_add_f32_dpp v25, v25, v25 row_half_mirror row_mask:0xf bank_mask:0xf bound_ctrl:1
	s_nop 1
	v_add_f32_dpp v25, v25, v25 row_mirror row_mask:0xf bank_mask:0xf bound_ctrl:1
	s_nop 1
	v_mov_b32_dpp v32, v25 row_bcast:15 row_mask:0xa bank_mask:0xf
	v_add_f32_e32 v25, v25, v32
	s_nop 1
	v_mov_b32_dpp v33, v25 row_bcast:31 row_mask:0xc bank_mask:0xf
	v_add_f32_e32 v25, v25, v33
	s_nop 0
	v_readlane_b32 s6, v25, 63
	s_nop 1
	v_fma_f32 v25, s6, v90, v85
	v_mul_f32_e32 v28, 0x4b800000, v25
	v_cmp_gt_f32_e64 s[6:7], s81, v25
	s_nop 1
	v_cndmask_b32_e64 v25, v25, v28, s[6:7]
	v_rsq_f32_e32 v25, v25
	s_nop 0
	v_mul_f32_e32 v28, 0x45800000, v25
	v_cndmask_b32_e64 v28, v25, v28, s[6:7]
	v_pk_mul_f32 v[22:23], v[28:29], v[22:23] op_sel_hi:[0,1]
	v_pk_mul_f32 v[26:27], v[28:29], v[26:27] op_sel_hi:[0,1]
	v_pk_mul_f32 v[22:23], v[8:9], v[22:23]
	v_pk_mul_f32 v[26:27], v[6:7], v[26:27]
	v_cvt_pk_bf16_f32 v22, v22, v23
	v_cvt_pk_bf16_f32 v23, v26, v27
	global_store_dword v[20:21], v22, off offset:512 nt
	global_store_dword v[20:21], v23, off offset:768 nt
	s_and_saveexec_b64 s[6:7], s[4:5]
	s_cbranch_execz .LBB0_1820
	v_mov_b32_e32 v20, s16
	v_cndmask_b32_e64 v20, v24, v20, s[2:3]
	v_lshl_or_b32 v20, v20, 4, v66
	v_ashrrev_i32_e32 v21, 31, v20
	v_lshl_add_u64 v[26:27], s[12:13], 0, v[14:15]
	v_lshlrev_b64 v[20:21], 2, v[20:21]
	v_add_co_u32_e32 v26, vcc, 0x40561000, v26
	v_lshl_add_u64 v[22:23], s[44:45], 0, v[20:21]
	s_nop 0
	v_addc_co_u32_e32 v27, vcc, 0, v27, vcc
	v_lshl_add_u64 v[20:21], s[46:47], 0, v[20:21]
	global_load_ushort v25, v[26:27], off offset:256
	s_nop 0
	global_load_ushort v26, v[26:27], off offset:288
	s_nop 0
	global_load_dword v27, v[20:21], off
	s_nop 0
	global_load_dword v22, v[22:23], off
	v_lshl_add_u64 v[20:21], s[12:13], 0, v[10:11]
	v_add_co_u32_e32 v20, vcc, 0x4b960000, v20
	s_waitcnt vmcnt(3)
	v_lshlrev_b32_e32 v23, 16, v25
	s_waitcnt vmcnt(2)
	v_lshlrev_b32_e32 v25, 16, v26
	s_waitcnt vmcnt(1)
	v_mul_f32_e32 v26, v27, v25
	s_waitcnt vmcnt(0)
	v_mul_f32_e32 v25, v22, v25
	v_fma_f32 v22, v22, v23, -v26
	v_addc_co_u32_e32 v21, vcc, 0, v21, vcc
	v_fmac_f32_e32 v25, v27, v23
	v_cvt_pk_bf16_f32 v22, v22, s0
	v_cvt_pk_bf16_f32 v23, v25, s0
	global_store_short v[20:21], v22, off offset:512 nt
	global_store_short v[20:21], v23, off offset:544 nt
	s_branch .LBB0_1820

.LBB0_2180:
	s_or_b64 exec, exec, s[4:5]
	s_lshl_b64 s[2:3], s[24:25], 2
	s_add_u32 s4, s30, s2
	s_addc_u32 s5, s31, s3
	s_waitcnt lgkmcnt(0)
	v_add_u32_e32 v77, s59, v176
	v_ashrrev_i32_e32 v179, 31, v178
	v_lshl_add_u64 v[64:65], v[178:179], 2, s[4:5]
	v_lshl_add_u64 v[66:67], v[64:65], 0, s[14:15]
	v_add_co_u32_e32 v64, vcc, s33, v64
	v_mov_b32_e32 v82, v0
	s_nop 0
	v_addc_co_u32_e32 v65, vcc, 0, v65, vcc
	global_load_dword v71, v[64:65], off
	global_load_dword v70, v[66:67], off offset:128
	global_load_dword v69, v[66:67], off offset:256
	global_load_dword v68, v[66:67], off offset:384
	ds_read_b128 v[78:81], v77
	v_and_b32_e32 v65, 64, v254
	v_xor_b32_e32 v64, 1, v254
	v_add_u32_e32 v76, 64, v65
	v_cmp_lt_i32_e32 vcc, v64, v76
	v_mov_b32_e32 v83, v48
	v_mov_b32_e32 v86, v32
	v_cndmask_b32_e32 v72, v254, v64, vcc
	ds_read_b128 v[64:67], v77 offset:32
	s_waitcnt lgkmcnt(1)
	v_rcp_f32_e32 v74, v78
	v_rcp_f32_e32 v0, v79
	v_mov_b32_e32 v87, v16
	v_mov_b32_e32 v48, v1
	v_pk_mul_f32 v[82:83], v[82:83], v[74:75] op_sel_hi:[1,0]
	v_pk_mul_f32 v[78:79], v[86:87], v[74:75] op_sel_hi:[1,0]
	v_pk_mul_f32 v[86:87], v[48:49], v[0:1] op_sel_hi:[1,0]
	v_mov_b32_e32 v16, v33
	v_pk_mul_f32 v[84:85], v[82:83], v[82:83]
	v_pk_mul_f32 v[48:49], v[86:87], v[86:87]
	v_pk_mul_f32 v[0:1], v[16:17], v[0:1] op_sel_hi:[1,0]
	v_pk_mul_f32 v[74:75], v[78:79], v[78:79]
	v_pk_mul_f32 v[16:17], v[0:1], v[0:1]
	v_mov_b32_e32 v32, v48
	v_mov_b32_e32 v33, v84
	v_mov_b32_e32 v84, v49
	v_pk_add_f32 v[32:33], v[32:33], v[84:85]
	v_mov_b32_e32 v48, v17
	v_mov_b32_e32 v49, v75
	v_pk_add_f32 v[32:33], v[48:49], v[32:33]
	v_mov_b32_e32 v17, v74
	v_lshlrev_b32_e32 v72, 2, v72
	v_pk_add_f32 v[16:17], v[16:17], v[32:33]
	ds_bpermute_b32 v33, v72, v17
	ds_bpermute_b32 v32, v72, v16
	v_xor_b32_e32 v48, 2, v254
	v_cmp_lt_i32_e32 vcc, v48, v76
	s_lshl_b64 s[2:3], s[34:35], 11
	s_add_u32 s2, s26, s2
	v_cndmask_b32_e32 v48, v254, v48, vcc
	v_lshlrev_b32_e32 v73, 2, v48
	s_waitcnt lgkmcnt(0)
	v_pk_add_f32 v[16:17], v[16:17], v[32:33]
	ds_bpermute_b32 v33, v73, v17
	ds_bpermute_b32 v32, v73, v16
	v_xor_b32_e32 v48, 4, v254
	v_cmp_lt_i32_e32 vcc, v48, v76
	s_addc_u32 s3, s27, s3
	s_add_u32 s2, s2, s24
	v_cndmask_b32_e32 v48, v254, v48, vcc
	v_lshlrev_b32_e32 v74, 2, v48
	s_waitcnt lgkmcnt(0)
	v_pk_add_f32 v[16:17], v[16:17], v[32:33]
	ds_bpermute_b32 v33, v74, v17
	ds_bpermute_b32 v32, v74, v16
	v_xor_b32_e32 v48, 8, v254
	v_cmp_lt_i32_e32 vcc, v48, v76
	s_addc_u32 s3, s3, s25
	v_mov_b32_e32 v90, 0
	v_cndmask_b32_e32 v48, v254, v48, vcc
	v_lshlrev_b32_e32 v75, 2, v48
	s_waitcnt lgkmcnt(0)
	v_pk_add_f32 v[16:17], v[16:17], v[32:33]
	ds_bpermute_b32 v33, v75, v17
	ds_bpermute_b32 v32, v75, v16
	v_xor_b32_e32 v48, 16, v254
	v_cmp_lt_i32_e32 vcc, v48, v76
	s_mov_b32 s24, 0
	s_waitcnt lgkmcnt(0)
	v_pk_add_f32 v[16:17], v[16:17], v[32:33]
	v_cndmask_b32_e32 v48, v254, v48, vcc
	v_lshlrev_b32_e32 v76, 2, v48
	ds_bpermute_b32 v33, v76, v17
	ds_bpermute_b32 v32, v76, v16
	v_lshlrev_b32_e32 v48, 2, v178
	v_ashrrev_i32_e32 v49, 31, v48
	v_lshl_add_u64 v[84:85], s[2:3], 0, v[48:49]
	v_mov_b64_e32 v[48:49], s[22:23]
	s_waitcnt lgkmcnt(0)
	v_pk_add_f32 v[16:17], v[16:17], v[32:33]
	v_lshl_or_b32 v32, v189, 2, s58
	v_pk_fma_f32 v[88:89], v[16:17], s[20:21], v[48:49] op_sel_hi:[1,0,0]
	v_ashrrev_i32_e32 v33, 31, v32
	v_mul_f32_e32 v16, 0x4b800000, v89
	v_cmp_gt_f32_e32 vcc, s56, v89
	s_nop 1
	v_cndmask_b32_e32 v16, v89, v16, vcc
	v_rsq_f32_e32 v89, v16
	v_lshl_add_u64 v[16:17], v[84:85], 0, s[18:19]
	v_mul_f32_e32 v84, 0x45800000, v89
	v_cndmask_b32_e32 v84, v89, v84, vcc
	v_mul_f32_e32 v82, v82, v84
	v_mul_f32_e32 v83, v83, v84
	s_waitcnt vmcnt(3)
	v_mul_f32_e32 v82, v71, v82
	s_waitcnt vmcnt(2)
	v_mul_f32_e32 v83, v70, v83
	v_cvt_pk_fp8_f32 v90, v82, v83
	v_mul_f32_e32 v79, v79, v84
	v_mul_f32_e32 v78, v78, v84
	s_waitcnt vmcnt(1)
	v_mul_f32_e32 v79, v69, v79
	s_waitcnt vmcnt(0)
	v_mul_f32_e32 v78, v68, v78
	v_cvt_pk_fp8_f32 v90, v79, v78 op_sel:[0,0,1]
	v_mul_f32_e32 v78, 0x4b800000, v88
	v_cmp_gt_f32_e32 vcc, s56, v88
	v_mov_b32_e32 v82, v2
	v_rcp_f32_e32 v2, v81
	v_cndmask_b32_e32 v79, v88, v78, vcc
	v_rcp_f32_e32 v78, v80
	v_mov_b32_e32 v83, v50
	v_mov_b32_e32 v50, v3
	v_mov_b32_e32 v88, v34
	v_pk_mul_f32 v[82:83], v[82:83], v[78:79] op_sel_hi:[1,0]
	v_mov_b32_e32 v89, v18
	v_pk_mul_f32 v[50:51], v[50:51], v[2:3] op_sel_hi:[1,0]
	v_mov_b32_e32 v18, v35
	v_rsq_f32_e32 v91, v79
	v_pk_mul_f32 v[84:85], v[82:83], v[82:83]
	v_pk_mul_f32 v[78:79], v[88:89], v[78:79] op_sel_hi:[1,0]
	v_pk_mul_f32 v[88:89], v[50:51], v[50:51]
	v_pk_mul_f32 v[2:3], v[18:19], v[2:3] op_sel_hi:[1,0]
	v_pk_mul_f32 v[80:81], v[78:79], v[78:79]
	v_pk_mul_f32 v[18:19], v[2:3], v[2:3]
	v_mov_b32_e32 v34, v88
	v_mov_b32_e32 v35, v84
	v_mov_b32_e32 v84, v89
	v_pk_add_f32 v[34:35], v[34:35], v[84:85]
	v_mov_b32_e32 v84, v19
	v_mov_b32_e32 v85, v81
	v_pk_add_f32 v[34:35], v[84:85], v[34:35]
	v_mov_b32_e32 v19, v80
	v_pk_add_f32 v[18:19], v[18:19], v[34:35]
	ds_bpermute_b32 v35, v72, v19
	ds_bpermute_b32 v34, v72, v18
	v_lshlrev_b64 v[80:81], 11, v[32:33]
	v_mul_f32_e32 v33, 0x45800000, v91
	v_lshl_add_u64 v[80:81], v[16:17], 0, v[80:81]
	v_cndmask_b32_e32 v33, v91, v33, vcc
	s_waitcnt lgkmcnt(0)
	v_pk_add_f32 v[18:19], v[18:19], v[34:35]
	ds_bpermute_b32 v35, v73, v19
	ds_bpermute_b32 v34, v73, v18
	global_store_dword v[80:81], v90, off nt
	v_mul_f32_e32 v80, v86, v33
	v_mul_f32_e32 v81, v87, v33
	v_mul_f32_e32 v80, v71, v80
	s_waitcnt lgkmcnt(0)
	v_pk_add_f32 v[18:19], v[18:19], v[34:35]
	ds_bpermute_b32 v35, v74, v19
	ds_bpermute_b32 v34, v74, v18
	v_mul_f32_e32 v81, v70, v81
	v_mov_b32_e32 v84, 0
	v_cvt_pk_fp8_f32 v84, v80, v81
	v_mul_f32_e32 v1, v1, v33
	s_waitcnt lgkmcnt(0)
	v_pk_add_f32 v[18:19], v[18:19], v[34:35]
	ds_bpermute_b32 v35, v75, v19
	ds_bpermute_b32 v34, v75, v18
	v_mul_f32_e32 v0, v0, v33
	v_mul_f32_e32 v1, v69, v1
	v_mul_f32_e32 v0, v68, v0
	v_cvt_pk_fp8_f32 v84, v1, v0 op_sel:[0,0,1]
	s_waitcnt lgkmcnt(0)
	v_pk_add_f32 v[0:1], v[18:19], v[34:35]
	ds_bpermute_b32 v19, v76, v1
	ds_bpermute_b32 v18, v76, v0
	v_or_b32_e32 v34, 1, v32
	v_ashrrev_i32_e32 v35, 31, v34
	v_lshlrev_b64 v[34:35], 11, v[34:35]
	v_lshl_add_u64 v[34:35], v[16:17], 0, v[34:35]
	s_waitcnt lgkmcnt(0)
	v_pk_add_f32 v[0:1], v[0:1], v[18:19]
	global_store_dword v[34:35], v84, off nt
	v_pk_fma_f32 v[0:1], v[0:1], s[20:21], v[48:49] op_sel_hi:[1,0,0]
	v_mov_b32_e32 v80, v36
	v_mul_f32_e32 v18, 0x4b800000, v1
	v_cmp_gt_f32_e32 vcc, s56, v1
	v_mov_b32_e32 v81, v20
	v_mov_b32_e32 v20, v37
	v_cndmask_b32_e32 v1, v1, v18, vcc
	v_rsq_f32_e32 v1, v1
	v_or_b32_e32 v18, 2, v32
	v_ashrrev_i32_e32 v19, 31, v18
	v_lshlrev_b64 v[18:19], 11, v[18:19]
	v_mul_f32_e32 v33, 0x45800000, v1
	v_cndmask_b32_e32 v1, v1, v33, vcc
	v_mul_f32_e32 v33, v82, v1
	v_mul_f32_e32 v34, v83, v1
	v_mul_f32_e32 v33, v71, v33
	v_mul_f32_e32 v34, v70, v34
	v_mov_b32_e32 v82, 0
	v_cvt_pk_fp8_f32 v82, v33, v34
	v_mul_f32_e32 v35, v79, v1
	v_mul_f32_e32 v1, v78, v1
	v_mul_f32_e32 v33, v69, v35
	v_mul_f32_e32 v1, v68, v1
	v_cvt_pk_fp8_f32 v82, v33, v1 op_sel:[0,0,1]
	v_mul_f32_e32 v1, 0x4b800000, v0
	v_cmp_gt_f32_e32 vcc, s56, v0
	v_mov_b32_e32 v34, v4
	v_rcp_f32_e32 v4, v65
	v_cndmask_b32_e32 v1, v0, v1, vcc
	v_rcp_f32_e32 v0, v64
	v_mov_b32_e32 v35, v52
	v_mov_b32_e32 v52, v5
	v_pk_mul_f32 v[52:53], v[52:53], v[4:5] op_sel_hi:[1,0]
	v_pk_mul_f32 v[34:35], v[34:35], v[0:1] op_sel_hi:[1,0]
	v_rsq_f32_e32 v33, v1
	v_pk_mul_f32 v[78:79], v[34:35], v[34:35]
	v_pk_mul_f32 v[0:1], v[80:81], v[0:1] op_sel_hi:[1,0]
	v_pk_mul_f32 v[80:81], v[52:53], v[52:53]
	v_pk_mul_f32 v[4:5], v[20:21], v[4:5] op_sel_hi:[1,0]
	v_pk_mul_f32 v[64:65], v[0:1], v[0:1]
	v_pk_mul_f32 v[20:21], v[4:5], v[4:5]
	v_mov_b32_e32 v36, v80
	v_mov_b32_e32 v37, v78
	v_mov_b32_e32 v78, v81
	v_pk_add_f32 v[36:37], v[36:37], v[78:79]
	v_mov_b32_e32 v78, v21
	v_mov_b32_e32 v79, v65
	v_pk_add_f32 v[36:37], v[78:79], v[36:37]
	v_mov_b32_e32 v21, v64
	v_pk_add_f32 v[20:21], v[20:21], v[36:37]
	ds_bpermute_b32 v37, v72, v21
	ds_bpermute_b32 v36, v72, v20
	v_lshl_add_u64 v[18:19], v[16:17], 0, v[18:19]
	global_store_dword v[18:19], v82, off nt
	v_mul_f32_e32 v64, 0x45800000, v33
	v_cndmask_b32_e32 v33, v33, v64, vcc
	s_waitcnt lgkmcnt(0)
	v_pk_add_f32 v[18:19], v[20:21], v[36:37]
	ds_bpermute_b32 v21, v73, v19
	ds_bpermute_b32 v20, v73, v18
	v_mul_f32_e32 v36, v50, v33
	v_mul_f32_e32 v37, v51, v33
	v_mul_f32_e32 v36, v71, v36
	v_mul_f32_e32 v37, v70, v37
	s_waitcnt lgkmcnt(0)
	v_pk_add_f32 v[18:19], v[18:19], v[20:21]
	ds_bpermute_b32 v21, v74, v19
	ds_bpermute_b32 v20, v74, v18
	v_mov_b32_e32 v50, 0
	v_cvt_pk_fp8_f32 v50, v36, v37
	v_mul_f32_e32 v3, v3, v33
	v_mul_f32_e32 v2, v2, v33
	s_waitcnt lgkmcnt(0)
	v_pk_add_f32 v[18:19], v[18:19], v[20:21]
	ds_bpermute_b32 v21, v75, v19
	ds_bpermute_b32 v20, v75, v18
	v_mul_f32_e32 v3, v69, v3
	v_mul_f32_e32 v2, v68, v2
	v_cvt_pk_fp8_f32 v50, v3, v2 op_sel:[0,0,1]
	v_mov_b32_e32 v33, 0
	s_waitcnt lgkmcnt(0)
	v_pk_add_f32 v[2:3], v[18:19], v[20:21]
	ds_bpermute_b32 v19, v76, v3
	ds_bpermute_b32 v18, v76, v2
	v_or_b32_e32 v20, 3, v32
	v_ashrrev_i32_e32 v21, 31, v20
	v_lshlrev_b64 v[20:21], 11, v[20:21]
	v_lshl_add_u64 v[20:21], v[16:17], 0, v[20:21]
	s_waitcnt lgkmcnt(0)
	v_pk_add_f32 v[2:3], v[2:3], v[18:19]
	global_store_dword v[20:21], v50, off nt
	v_pk_fma_f32 v[2:3], v[2:3], s[20:21], v[48:49] op_sel_hi:[1,0,0]
	v_or_b32_e32 v36, 8, v32
	v_mul_f32_e32 v18, 0x4b800000, v3
	v_cmp_gt_f32_e32 vcc, s56, v3
	v_ashrrev_i32_e32 v37, 31, v36
	s_nop 0
	v_cndmask_b32_e32 v3, v3, v18, vcc
	v_rsq_f32_e32 v3, v3
	s_nop 0
	v_mul_f32_e32 v18, 0x45800000, v3
	v_cndmask_b32_e32 v3, v3, v18, vcc
	v_mul_f32_e32 v18, v34, v3
	v_mul_f32_e32 v19, v35, v3
	v_mul_f32_e32 v18, v71, v18
	v_mul_f32_e32 v19, v70, v19
	v_cvt_pk_fp8_f32 v33, v18, v19
	v_mul_f32_e32 v1, v1, v3
	v_mul_f32_e32 v0, v0, v3
	v_mul_f32_e32 v1, v69, v1
	v_mul_f32_e32 v0, v68, v0
	v_cvt_pk_fp8_f32 v33, v1, v0 op_sel:[0,0,1]
	v_mul_f32_e32 v0, 0x4b800000, v2
	v_cmp_gt_f32_e32 vcc, s56, v2
	v_mov_b32_e32 v3, v54
	v_mov_b32_e32 v54, v7
	v_cndmask_b32_e32 v1, v2, v0, vcc
	v_rcp_f32_e32 v0, v66
	v_mov_b32_e32 v2, v6
	v_rcp_f32_e32 v6, v67
	v_mov_b32_e32 v18, v38
	v_pk_mul_f32 v[2:3], v[2:3], v[0:1] op_sel_hi:[1,0]
	v_mov_b32_e32 v19, v22
	v_pk_mul_f32 v[20:21], v[54:55], v[6:7] op_sel_hi:[1,0]
	v_mov_b32_e32 v22, v39
	v_rsq_f32_e32 v64, v1
	v_pk_mul_f32 v[34:35], v[2:3], v[2:3]
	v_pk_mul_f32 v[0:1], v[18:19], v[0:1] op_sel_hi:[1,0]
	v_pk_mul_f32 v[54:55], v[20:21], v[20:21]
	v_pk_mul_f32 v[18:19], v[22:23], v[6:7] op_sel_hi:[1,0]
	v_pk_mul_f32 v[50:51], v[0:1], v[0:1]
	v_pk_mul_f32 v[6:7], v[18:19], v[18:19]
	v_mov_b32_e32 v22, v54
	v_mov_b32_e32 v23, v34
	v_mov_b32_e32 v34, v55
	v_pk_add_f32 v[22:23], v[22:23], v[34:35]
	v_mov_b32_e32 v34, v7
	v_mov_b32_e32 v35, v51
	v_pk_add_f32 v[22:23], v[34:35], v[22:23]
	v_mov_b32_e32 v7, v50
	v_pk_add_f32 v[6:7], v[6:7], v[22:23]
	ds_bpermute_b32 v23, v72, v7
	ds_bpermute_b32 v22, v72, v6
	v_lshlrev_b64 v[34:35], 11, v[36:37]
	v_lshl_add_u64 v[34:35], v[16:17], 0, v[34:35]
	global_store_dword v[34:35], v33, off nt
	v_mul_f32_e32 v33, 0x45800000, v64
	s_waitcnt lgkmcnt(0)
	v_pk_add_f32 v[6:7], v[6:7], v[22:23]
	ds_bpermute_b32 v23, v73, v7
	ds_bpermute_b32 v22, v73, v6
	v_cndmask_b32_e32 v33, v64, v33, vcc
	v_mul_f32_e32 v34, v52, v33
	v_mul_f32_e32 v35, v53, v33
	v_mul_f32_e32 v34, v71, v34
	s_waitcnt lgkmcnt(0)
	v_pk_add_f32 v[6:7], v[6:7], v[22:23]
	ds_bpermute_b32 v23, v74, v7
	ds_bpermute_b32 v22, v74, v6
	v_mul_f32_e32 v35, v70, v35
	v_mov_b32_e32 v36, 0
	v_cvt_pk_fp8_f32 v36, v34, v35
	v_mul_f32_e32 v5, v5, v33
	s_waitcnt lgkmcnt(0)
	v_pk_add_f32 v[6:7], v[6:7], v[22:23]
	ds_bpermute_b32 v23, v75, v7
	ds_bpermute_b32 v22, v75, v6
	v_mul_f32_e32 v4, v4, v33
	v_mul_f32_e32 v5, v69, v5
	v_mul_f32_e32 v4, v68, v4
	v_cvt_pk_fp8_f32 v36, v5, v4 op_sel:[0,0,1]
	s_waitcnt lgkmcnt(0)
	v_pk_add_f32 v[4:5], v[6:7], v[22:23]
	ds_bpermute_b32 v7, v76, v5
	ds_bpermute_b32 v6, v76, v4
	v_mov_b32_e32 v33, 0
	v_or_b32_e32 v22, 9, v32
	v_ashrrev_i32_e32 v23, 31, v22
	v_lshlrev_b64 v[22:23], 11, v[22:23]
	s_waitcnt lgkmcnt(0)
	v_pk_add_f32 v[4:5], v[4:5], v[6:7]
	v_lshl_add_u64 v[22:23], v[16:17], 0, v[22:23]
	v_pk_fma_f32 v[34:35], v[4:5], s[20:21], v[48:49] op_sel_hi:[1,0,0]
	v_mov_b32_e32 v38, v40
	v_mul_f32_e32 v4, 0x4b800000, v35
	v_cmp_gt_f32_e32 vcc, s56, v35
	v_mov_b32_e32 v39, v24
	v_mov_b32_e32 v24, v41
	v_cndmask_b32_e32 v4, v35, v4, vcc
	v_rsq_f32_e32 v4, v4
	v_mov_b32_e32 v35, v56
	v_mov_b32_e32 v56, v9
	global_store_dword v[22:23], v36, off nt
	v_mul_f32_e32 v5, 0x45800000, v4
	v_cndmask_b32_e32 v4, v4, v5, vcc
	v_mul_f32_e32 v2, v2, v4
	v_mul_f32_e32 v3, v3, v4
	v_mul_f32_e32 v2, v71, v2
	v_mul_f32_e32 v3, v70, v3
	v_cvt_pk_fp8_f32 v33, v2, v3
	v_mul_f32_e32 v1, v1, v4
	v_mul_f32_e32 v0, v0, v4
	ds_read_b128 v[4:7], v77 offset:64
	v_mul_f32_e32 v1, v69, v1
	v_mul_f32_e32 v0, v68, v0
	v_cvt_pk_fp8_f32 v33, v1, v0 op_sel:[0,0,1]
	v_mul_f32_e32 v0, 0x4b800000, v34
	v_cmp_gt_f32_e32 vcc, s56, v34
	v_or_b32_e32 v22, 10, v32
	v_ashrrev_i32_e32 v23, 31, v22
	v_cndmask_b32_e32 v34, v34, v0, vcc
	ds_read_b128 v[0:3], v77 offset:96
	s_waitcnt lgkmcnt(1)
	v_rcp_f32_e32 v4, v4
	v_rsq_f32_e32 v54, v34
	v_mov_b32_e32 v34, v8
	v_rcp_f32_e32 v8, v5
	v_pk_mul_f32 v[34:35], v[34:35], v[4:5] op_sel_hi:[1,0]
	v_pk_mul_f32 v[4:5], v[38:39], v[4:5] op_sel_hi:[1,0]
	v_pk_mul_f32 v[36:37], v[34:35], v[34:35]
	v_pk_mul_f32 v[50:51], v[56:57], v[8:9] op_sel_hi:[1,0]
	v_pk_mul_f32 v[8:9], v[24:25], v[8:9] op_sel_hi:[1,0]
	v_pk_mul_f32 v[52:53], v[50:51], v[50:51]
	v_pk_mul_f32 v[38:39], v[4:5], v[4:5]
	v_pk_mul_f32 v[24:25], v[8:9], v[8:9]
	v_mov_b32_e32 v40, v52
	v_mov_b32_e32 v41, v36
	v_mov_b32_e32 v36, v53
	v_pk_add_f32 v[36:37], v[40:41], v[36:37]
	v_mov_b32_e32 v40, v25
	v_mov_b32_e32 v41, v39
	v_pk_add_f32 v[36:37], v[40:41], v[36:37]
	v_mov_b32_e32 v25, v38
	v_pk_add_f32 v[24:25], v[24:25], v[36:37]
	ds_bpermute_b32 v37, v72, v25
	ds_bpermute_b32 v36, v72, v24
	v_lshlrev_b64 v[22:23], 11, v[22:23]
	v_lshl_add_u64 v[22:23], v[16:17], 0, v[22:23]
	global_store_dword v[22:23], v33, off nt
	v_mul_f32_e32 v33, 0x45800000, v54
	s_waitcnt lgkmcnt(0)
	v_pk_add_f32 v[22:23], v[24:25], v[36:37]
	ds_bpermute_b32 v25, v73, v23
	ds_bpermute_b32 v24, v73, v22
	v_cndmask_b32_e32 v33, v54, v33, vcc
	v_mul_f32_e32 v20, v20, v33
	v_mul_f32_e32 v36, v71, v20
	v_mul_f32_e32 v37, v21, v33
	s_waitcnt lgkmcnt(0)
	v_pk_add_f32 v[20:21], v[22:23], v[24:25]
	ds_bpermute_b32 v23, v74, v21
	ds_bpermute_b32 v22, v74, v20
	v_mul_f32_e32 v24, v70, v37
	v_mov_b32_e32 v25, 0
	v_cvt_pk_fp8_f32 v25, v36, v24
	v_mul_f32_e32 v19, v19, v33
	s_waitcnt lgkmcnt(0)
	v_pk_add_f32 v[20:21], v[20:21], v[22:23]
	ds_bpermute_b32 v23, v75, v21
	ds_bpermute_b32 v22, v75, v20
	v_mul_f32_e32 v18, v18, v33
	v_mul_f32_e32 v19, v69, v19
	v_mul_f32_e32 v18, v68, v18
	v_cvt_pk_fp8_f32 v25, v19, v18 op_sel:[0,0,1]
	s_waitcnt lgkmcnt(0)
	v_pk_add_f32 v[18:19], v[20:21], v[22:23]
	ds_bpermute_b32 v21, v76, v19
	ds_bpermute_b32 v20, v76, v18
	v_or_b32_e32 v22, 11, v32
	v_ashrrev_i32_e32 v23, 31, v22
	v_lshlrev_b64 v[22:23], 11, v[22:23]
	v_lshl_add_u64 v[22:23], v[16:17], 0, v[22:23]
	s_waitcnt lgkmcnt(0)
	v_pk_add_f32 v[18:19], v[18:19], v[20:21]
	global_store_dword v[22:23], v25, off nt
	v_pk_fma_f32 v[18:19], v[18:19], s[20:21], v[48:49] op_sel_hi:[1,0,0]
	v_mov_b32_e32 v33, 0
	v_mul_f32_e32 v20, 0x4b800000, v19
	v_cmp_gt_f32_e32 vcc, s56, v19
	v_mov_b32_e32 v24, v42
	v_mov_b32_e32 v25, v26
	v_cndmask_b32_e32 v19, v19, v20, vcc
	v_rsq_f32_e32 v19, v19
	v_mov_b32_e32 v26, v43
	v_or_b32_e32 v20, 16, v32
	v_ashrrev_i32_e32 v21, 31, v20
	v_mul_f32_e32 v22, 0x45800000, v19
	v_cndmask_b32_e32 v19, v19, v22, vcc
	v_mul_f32_e32 v22, v34, v19
	v_mul_f32_e32 v23, v35, v19
	v_mul_f32_e32 v22, v71, v22
	v_mul_f32_e32 v23, v70, v23
	v_cvt_pk_fp8_f32 v33, v22, v23
	v_mul_f32_e32 v5, v5, v19
	v_mul_f32_e32 v4, v4, v19
	v_mul_f32_e32 v5, v69, v5
	v_mul_f32_e32 v4, v68, v4
	v_cvt_pk_fp8_f32 v33, v5, v4 op_sel:[0,0,1]
	v_mul_f32_e32 v4, 0x4b800000, v18
	v_cmp_gt_f32_e32 vcc, s56, v18
	v_mov_b32_e32 v19, v58
	v_mov_b32_e32 v58, v11
	v_cndmask_b32_e32 v5, v18, v4, vcc
	v_rcp_f32_e32 v4, v6
	v_rcp_f32_e32 v6, v7
	v_mov_b32_e32 v18, v10
	v_rsq_f32_e32 v38, v5
	v_pk_mul_f32 v[18:19], v[18:19], v[4:5] op_sel_hi:[1,0]
	v_pk_mul_f32 v[10:11], v[58:59], v[6:7] op_sel_hi:[1,0]
	v_pk_mul_f32 v[22:23], v[18:19], v[18:19]
	v_pk_mul_f32 v[4:5], v[24:25], v[4:5] op_sel_hi:[1,0]
	v_pk_mul_f32 v[34:35], v[10:11], v[10:11]
	v_pk_mul_f32 v[6:7], v[26:27], v[6:7] op_sel_hi:[1,0]
	v_pk_mul_f32 v[24:25], v[4:5], v[4:5]
	v_pk_mul_f32 v[26:27], v[6:7], v[6:7]
	v_mov_b32_e32 v36, v34
	v_mov_b32_e32 v37, v22
	v_mov_b32_e32 v22, v35
	v_pk_add_f32 v[22:23], v[36:37], v[22:23]
	v_mov_b32_e32 v34, v27
	v_mov_b32_e32 v35, v25
	v_pk_add_f32 v[22:23], v[34:35], v[22:23]
	v_mov_b32_e32 v27, v24
	v_pk_add_f32 v[22:23], v[26:27], v[22:23]
	ds_bpermute_b32 v25, v72, v23
	ds_bpermute_b32 v24, v72, v22
	v_lshlrev_b64 v[20:21], 11, v[20:21]
	v_lshl_add_u64 v[20:21], v[16:17], 0, v[20:21]
	global_store_dword v[20:21], v33, off nt
	v_mul_f32_e32 v26, 0x45800000, v38
	s_waitcnt lgkmcnt(0)
	v_pk_add_f32 v[20:21], v[22:23], v[24:25]
	ds_bpermute_b32 v23, v73, v21
	ds_bpermute_b32 v22, v73, v20
	v_cndmask_b32_e32 v24, v38, v26, vcc
	v_mul_f32_e32 v25, v50, v24
	v_mul_f32_e32 v26, v51, v24
	v_mul_f32_e32 v25, v71, v25
	s_waitcnt lgkmcnt(0)
	v_pk_add_f32 v[20:21], v[20:21], v[22:23]
	ds_bpermute_b32 v23, v74, v21
	ds_bpermute_b32 v22, v74, v20
	v_mul_f32_e32 v26, v70, v26
	v_mov_b32_e32 v27, 0
	v_cvt_pk_fp8_f32 v27, v25, v26
	v_mul_f32_e32 v9, v9, v24
	s_waitcnt lgkmcnt(0)
	v_pk_add_f32 v[20:21], v[20:21], v[22:23]
	ds_bpermute_b32 v23, v75, v21
	ds_bpermute_b32 v22, v75, v20
	v_mul_f32_e32 v8, v8, v24
	v_mul_f32_e32 v9, v69, v9
	v_mul_f32_e32 v8, v68, v8
	v_cvt_pk_fp8_f32 v27, v9, v8 op_sel:[0,0,1]
	s_waitcnt lgkmcnt(0)
	v_pk_add_f32 v[8:9], v[20:21], v[22:23]
	ds_bpermute_b32 v21, v76, v9
	ds_bpermute_b32 v20, v76, v8
	v_or_b32_e32 v22, 17, v32
	v_ashrrev_i32_e32 v23, 31, v22
	v_lshlrev_b64 v[22:23], 11, v[22:23]
	v_lshl_add_u64 v[22:23], v[16:17], 0, v[22:23]
	s_waitcnt lgkmcnt(0)
	v_pk_add_f32 v[8:9], v[8:9], v[20:21]
	global_store_dword v[22:23], v27, off nt
	v_pk_fma_f32 v[8:9], v[8:9], s[20:21], v[48:49] op_sel_hi:[1,0,0]
	v_mov_b32_e32 v33, 0
	v_mul_f32_e32 v20, 0x4b800000, v9
	v_cmp_gt_f32_e32 vcc, s56, v9
	v_rcp_f32_e32 v0, v0
	s_nop 0
	v_cndmask_b32_e32 v9, v9, v20, vcc
	v_rsq_f32_e32 v9, v9
	v_or_b32_e32 v20, 18, v32
	v_ashrrev_i32_e32 v21, 31, v20
	v_lshlrev_b64 v[20:21], 11, v[20:21]
	v_mul_f32_e32 v22, 0x45800000, v9
	v_cndmask_b32_e32 v9, v9, v22, vcc
	v_mul_f32_e32 v18, v18, v9
	v_mul_f32_e32 v19, v19, v9
	v_mul_f32_e32 v18, v71, v18
	v_mul_f32_e32 v19, v70, v19
	v_cvt_pk_fp8_f32 v33, v18, v19
	v_mul_f32_e32 v5, v5, v9
	v_mul_f32_e32 v4, v4, v9
	v_mul_f32_e32 v5, v69, v5
	v_mul_f32_e32 v4, v68, v4
	v_cvt_pk_fp8_f32 v33, v5, v4 op_sel:[0,0,1]
	v_mul_f32_e32 v4, 0x4b800000, v8
	v_cmp_gt_f32_e32 vcc, s56, v8
	v_mov_b32_e32 v5, v60
	v_mov_b32_e32 v60, v13
	v_cndmask_b32_e32 v4, v8, v4, vcc
	v_rsq_f32_e32 v34, v4
	v_mov_b32_e32 v4, v12
	v_rcp_f32_e32 v12, v1
	v_pk_mul_f32 v[4:5], v[4:5], v[0:1] op_sel_hi:[1,0]
	v_mov_b32_e32 v18, v44
	v_mov_b32_e32 v19, v28
	v_pk_mul_f32 v[22:23], v[60:61], v[12:13] op_sel_hi:[1,0]
	v_mov_b32_e32 v28, v45
	v_pk_mul_f32 v[8:9], v[4:5], v[4:5]
	v_pk_mul_f32 v[0:1], v[18:19], v[0:1] op_sel_hi:[1,0]
	v_pk_mul_f32 v[24:25], v[22:23], v[22:23]
	v_pk_mul_f32 v[12:13], v[28:29], v[12:13] op_sel_hi:[1,0]
	v_pk_mul_f32 v[18:19], v[0:1], v[0:1]
	v_pk_mul_f32 v[26:27], v[12:13], v[12:13]
	v_mov_b32_e32 v28, v24
	v_mov_b32_e32 v29, v8
	v_mov_b32_e32 v8, v25
	v_pk_add_f32 v[8:9], v[28:29], v[8:9]
	v_mov_b32_e32 v24, v27
	v_mov_b32_e32 v25, v19
	v_pk_add_f32 v[8:9], v[24:25], v[8:9]
	v_mov_b32_e32 v27, v18
	v_pk_add_f32 v[8:9], v[26:27], v[8:9]
	ds_bpermute_b32 v19, v72, v9
	ds_bpermute_b32 v18, v72, v8
	v_lshl_add_u64 v[20:21], v[16:17], 0, v[20:21]
	global_store_dword v[20:21], v33, off nt
	v_mul_f32_e32 v20, 0x45800000, v34
	v_cndmask_b32_e32 v20, v34, v20, vcc
	s_waitcnt lgkmcnt(0)
	v_pk_add_f32 v[8:9], v[8:9], v[18:19]
	ds_bpermute_b32 v19, v73, v9
	ds_bpermute_b32 v18, v73, v8
	v_mul_f32_e32 v10, v10, v20
	v_mul_f32_e32 v21, v71, v10
	v_mul_f32_e32 v24, v11, v20
	v_mul_f32_e32 v7, v7, v20
	s_waitcnt lgkmcnt(0)
	v_pk_add_f32 v[8:9], v[8:9], v[18:19]
	ds_bpermute_b32 v11, v74, v9
	ds_bpermute_b32 v10, v74, v8
	v_mul_f32_e32 v18, v70, v24
	v_mov_b32_e32 v19, 0
	v_cvt_pk_fp8_f32 v19, v21, v18
	v_mul_f32_e32 v6, v6, v20
	s_waitcnt lgkmcnt(0)
	v_pk_add_f32 v[8:9], v[8:9], v[10:11]
	ds_bpermute_b32 v11, v75, v9
	ds_bpermute_b32 v10, v75, v8
	v_mul_f32_e32 v7, v69, v7
	v_mul_f32_e32 v6, v68, v6
	v_cvt_pk_fp8_f32 v19, v7, v6 op_sel:[0,0,1]
	v_mov_b32_e32 v26, 0
	s_waitcnt lgkmcnt(0)
	v_pk_add_f32 v[6:7], v[8:9], v[10:11]
	ds_bpermute_b32 v9, v76, v7
	ds_bpermute_b32 v8, v76, v6
	v_or_b32_e32 v10, 19, v32
	v_ashrrev_i32_e32 v11, 31, v10
	v_lshlrev_b64 v[10:11], 11, v[10:11]
	v_lshl_add_u64 v[10:11], v[16:17], 0, v[10:11]
	s_waitcnt lgkmcnt(0)
	v_pk_add_f32 v[6:7], v[6:7], v[8:9]
	global_store_dword v[10:11], v19, off nt
	v_pk_fma_f32 v[6:7], v[6:7], s[20:21], v[48:49] op_sel_hi:[1,0,0]
	v_mov_b32_e32 v11, v30
	v_mul_f32_e32 v8, 0x4b800000, v7
	v_cmp_gt_f32_e32 vcc, s56, v7
	v_mov_b32_e32 v30, v47
	s_nop 0
	v_cndmask_b32_e32 v7, v7, v8, vcc
	v_rsq_f32_e32 v7, v7
	v_or_b32_e32 v8, 24, v32
	v_ashrrev_i32_e32 v9, 31, v8
	v_lshlrev_b64 v[8:9], 11, v[8:9]
	v_mul_f32_e32 v10, 0x45800000, v7
	v_cndmask_b32_e32 v7, v7, v10, vcc
	v_mul_f32_e32 v4, v4, v7
	v_mul_f32_e32 v5, v5, v7
	v_mul_f32_e32 v4, v71, v4
	v_mul_f32_e32 v5, v70, v5
	v_cvt_pk_fp8_f32 v26, v4, v5
	v_mul_f32_e32 v1, v1, v7
	v_mul_f32_e32 v0, v0, v7
	v_mul_f32_e32 v1, v69, v1
	v_mul_f32_e32 v0, v68, v0
	v_cvt_pk_fp8_f32 v26, v1, v0 op_sel:[0,0,1]
	v_mul_f32_e32 v0, 0x4b800000, v6
	v_cmp_gt_f32_e32 vcc, s56, v6
	v_mov_b32_e32 v4, v14
	v_mov_b32_e32 v5, v62
	v_cndmask_b32_e32 v1, v6, v0, vcc
	v_rcp_f32_e32 v0, v2
	v_rcp_f32_e32 v2, v3
	v_mov_b32_e32 v62, v15
	v_mov_b32_e32 v10, v46
	v_pk_mul_f32 v[4:5], v[4:5], v[0:1] op_sel_hi:[1,0]
	v_pk_mul_f32 v[14:15], v[62:63], v[2:3] op_sel_hi:[1,0]
	v_rsq_f32_e32 v27, v1
	v_pk_mul_f32 v[6:7], v[4:5], v[4:5]
	v_pk_mul_f32 v[0:1], v[10:11], v[0:1] op_sel_hi:[1,0]
	v_pk_mul_f32 v[18:19], v[14:15], v[14:15]
	v_pk_mul_f32 v[2:3], v[30:31], v[2:3] op_sel_hi:[1,0]
	v_pk_mul_f32 v[10:11], v[0:1], v[0:1]
	v_pk_mul_f32 v[20:21], v[2:3], v[2:3]
	v_mov_b32_e32 v24, v18
	v_mov_b32_e32 v25, v6
	v_mov_b32_e32 v6, v19
	v_pk_add_f32 v[6:7], v[24:25], v[6:7]
	v_mov_b32_e32 v18, v21
	v_mov_b32_e32 v19, v11
	v_pk_add_f32 v[6:7], v[18:19], v[6:7]
	v_mov_b32_e32 v21, v10
	v_pk_add_f32 v[6:7], v[20:21], v[6:7]
	ds_bpermute_b32 v11, v72, v7
	ds_bpermute_b32 v10, v72, v6
	v_lshl_add_u64 v[8:9], v[16:17], 0, v[8:9]
	global_store_dword v[8:9], v26, off nt
	v_mul_f32_e32 v18, 0x45800000, v27
	v_mov_b32_e32 v19, 0
	s_waitcnt lgkmcnt(0)
	v_pk_add_f32 v[6:7], v[6:7], v[10:11]
	ds_bpermute_b32 v9, v73, v7
	ds_bpermute_b32 v8, v73, v6
	v_cndmask_b32_e32 v10, v27, v18, vcc
	v_mul_f32_e32 v11, v22, v10
	v_mul_f32_e32 v18, v23, v10
	v_mul_f32_e32 v11, v71, v11
	s_waitcnt lgkmcnt(0)
	v_pk_add_f32 v[6:7], v[6:7], v[8:9]
	ds_bpermute_b32 v9, v74, v7
	ds_bpermute_b32 v8, v74, v6
	v_mul_f32_e32 v18, v70, v18
	v_cvt_pk_fp8_f32 v19, v11, v18
	v_mul_f32_e32 v13, v13, v10
	v_mul_f32_e32 v10, v12, v10
	s_waitcnt lgkmcnt(0)
	v_pk_add_f32 v[6:7], v[6:7], v[8:9]
	ds_bpermute_b32 v9, v75, v7
	ds_bpermute_b32 v8, v75, v6
	v_mul_f32_e32 v11, v69, v13
	v_mul_f32_e32 v10, v68, v10
	v_cvt_pk_fp8_f32 v19, v11, v10 op_sel:[0,0,1]
	v_or_b32_e32 v10, 25, v32
	s_waitcnt lgkmcnt(0)
	v_pk_add_f32 v[6:7], v[6:7], v[8:9]
	ds_bpermute_b32 v9, v76, v7
	ds_bpermute_b32 v8, v76, v6
	v_ashrrev_i32_e32 v11, 31, v10
	v_lshlrev_b64 v[10:11], 11, v[10:11]
	v_lshl_add_u64 v[10:11], v[16:17], 0, v[10:11]
	global_store_dword v[10:11], v19, off nt
	s_waitcnt lgkmcnt(0)
	v_pk_add_f32 v[6:7], v[6:7], v[8:9]
	s_nop 0
	v_pk_fma_f32 v[6:7], v[6:7], s[20:21], v[48:49] op_sel_hi:[1,0,0]
	s_nop 0
	v_mul_f32_e32 v8, 0x4b800000, v7
	v_cmp_gt_f32_e32 vcc, s56, v7
	s_nop 1
	v_cndmask_b32_e32 v7, v7, v8, vcc
	v_rsq_f32_e32 v7, v7
	v_or_b32_e32 v8, 26, v32
	v_ashrrev_i32_e32 v9, 31, v8
	v_mul_f32_e32 v10, 0x45800000, v7
	v_cndmask_b32_e32 v7, v7, v10, vcc
	v_mul_f32_e32 v4, v4, v7
	v_mul_f32_e32 v5, v5, v7
	v_mul_f32_e32 v4, v71, v4
	v_mul_f32_e32 v5, v70, v5
	v_mov_b32_e32 v10, 0
	v_cvt_pk_fp8_f32 v10, v4, v5
	v_mul_f32_e32 v1, v1, v7
	v_mul_f32_e32 v0, v0, v7
	v_mul_f32_e32 v1, v69, v1
	v_mul_f32_e32 v0, v68, v0
	v_cvt_pk_fp8_f32 v10, v1, v0 op_sel:[0,0,1]
	v_mul_f32_e32 v0, 0x4b800000, v6
	v_cmp_gt_f32_e32 vcc, s56, v6
	v_mov_b32_e32 v5, 0
	s_nop 0
	v_cndmask_b32_e32 v0, v6, v0, vcc
	v_rsq_f32_e32 v4, v0
	v_lshlrev_b64 v[0:1], 11, v[8:9]
	v_lshl_add_u64 v[0:1], v[16:17], 0, v[0:1]
	global_store_dword v[0:1], v10, off nt
	v_mul_f32_e32 v0, 0x45800000, v4
	v_cndmask_b32_e32 v0, v4, v0, vcc
	v_mul_f32_e32 v1, v14, v0
	v_mul_f32_e32 v4, v15, v0
	v_mul_f32_e32 v1, v71, v1
	v_mul_f32_e32 v4, v70, v4
	v_cvt_pk_fp8_f32 v5, v1, v4
	v_mul_f32_e32 v3, v3, v0
	v_mul_f32_e32 v0, v2, v0
	v_mul_f32_e32 v1, v69, v3
	v_mul_f32_e32 v0, v68, v0
	v_cvt_pk_fp8_f32 v5, v1, v0 op_sel:[0,0,1]
	v_or_b32_e32 v0, 27, v32
	v_ashrrev_i32_e32 v1, 31, v0
	v_lshlrev_b64 v[0:1], 11, v[0:1]
	v_lshl_add_u64 v[0:1], v[16:17], 0, v[0:1]
	global_store_dword v[0:1], v5, off nt
	s_barrier

.LBB0_2209:
	s_or_b64 exec, exec, s[4:5]
	s_lshl_b32 s2, s70, 7
	s_ashr_i32 s3, s2, 31
	s_lshl_b64 s[4:5], s[2:3], 2
	s_add_u32 s4, s26, s4
	s_addc_u32 s5, s27, s5
	s_waitcnt lgkmcnt(0)
	v_lshl_add_u32 v77, v171, 4, s72
	v_ashrrev_i32_e32 v147, 31, v146
	v_lshl_add_u64 v[64:65], v[146:147], 2, s[4:5]
	v_lshl_add_u64 v[66:67], v[64:65], 0, s[14:15]
	v_add_co_u32_e32 v64, vcc, s67, v64
	v_mov_b32_e32 v82, v0
	s_nop 0
	v_addc_co_u32_e32 v65, vcc, 0, v65, vcc
	global_load_dword v71, v[64:65], off offset:3072
	global_load_dword v70, v[66:67], off offset:128
	global_load_dword v69, v[66:67], off offset:256
	global_load_dword v68, v[66:67], off offset:384
	ds_read_b128 v[78:81], v77
	v_and_b32_e32 v65, 64, v254
	v_xor_b32_e32 v64, 1, v254
	v_add_u32_e32 v76, 64, v65
	v_cmp_lt_i32_e32 vcc, v64, v76
	v_mov_b32_e32 v83, v48
	v_mov_b32_e32 v86, v32
	v_cndmask_b32_e32 v72, v254, v64, vcc
	ds_read_b128 v[64:67], v77 offset:32
	s_waitcnt lgkmcnt(1)
	v_rcp_f32_e32 v74, v78
	v_rcp_f32_e32 v0, v79
	v_mov_b32_e32 v87, v16
	v_mov_b32_e32 v48, v1
	v_pk_mul_f32 v[82:83], v[82:83], v[74:75] op_sel_hi:[1,0]
	v_pk_mul_f32 v[78:79], v[86:87], v[74:75] op_sel_hi:[1,0]
	v_pk_mul_f32 v[86:87], v[48:49], v[0:1] op_sel_hi:[1,0]
	v_mov_b32_e32 v16, v33
	v_pk_mul_f32 v[84:85], v[82:83], v[82:83]
	v_pk_mul_f32 v[48:49], v[86:87], v[86:87]
	v_pk_mul_f32 v[0:1], v[16:17], v[0:1] op_sel_hi:[1,0]
	v_pk_mul_f32 v[74:75], v[78:79], v[78:79]
	v_pk_mul_f32 v[16:17], v[0:1], v[0:1]
	v_mov_b32_e32 v32, v48
	v_mov_b32_e32 v33, v84
	v_mov_b32_e32 v84, v49
	v_pk_add_f32 v[32:33], v[32:33], v[84:85]
	v_mov_b32_e32 v48, v17
	v_mov_b32_e32 v49, v75
	v_pk_add_f32 v[32:33], v[48:49], v[32:33]
	v_mov_b32_e32 v17, v74
	v_lshlrev_b32_e32 v72, 2, v72
	v_pk_add_f32 v[16:17], v[16:17], v[32:33]
	ds_bpermute_b32 v33, v72, v17
	ds_bpermute_b32 v32, v72, v16
	v_xor_b32_e32 v48, 2, v254
	v_cmp_lt_i32_e32 vcc, v48, v76
	s_lshl_b64 s[26:27], s[30:31], 11
	s_add_u32 s24, s24, s26
	v_cndmask_b32_e32 v48, v254, v48, vcc
	v_lshlrev_b32_e32 v73, 2, v48
	s_waitcnt lgkmcnt(0)
	v_pk_add_f32 v[16:17], v[16:17], v[32:33]
	ds_bpermute_b32 v33, v73, v17
	ds_bpermute_b32 v32, v73, v16
	v_xor_b32_e32 v48, 4, v254
	v_cmp_lt_i32_e32 vcc, v48, v76
	s_addc_u32 s25, s25, s27
	s_add_u32 s2, s24, s2
	v_cndmask_b32_e32 v48, v254, v48, vcc
	v_lshlrev_b32_e32 v74, 2, v48
	s_waitcnt lgkmcnt(0)
	v_pk_add_f32 v[16:17], v[16:17], v[32:33]
	ds_bpermute_b32 v33, v74, v17
	ds_bpermute_b32 v32, v74, v16
	v_xor_b32_e32 v48, 8, v254
	v_cmp_lt_i32_e32 vcc, v48, v76
	s_addc_u32 s3, s25, s3
	v_mov_b32_e32 v90, 0
	v_cndmask_b32_e32 v48, v254, v48, vcc
	v_lshlrev_b32_e32 v75, 2, v48
	s_waitcnt lgkmcnt(0)
	v_pk_add_f32 v[16:17], v[16:17], v[32:33]
	ds_bpermute_b32 v33, v75, v17
	ds_bpermute_b32 v32, v75, v16
	v_xor_b32_e32 v48, 16, v254
	v_cmp_lt_i32_e32 vcc, v48, v76
	s_mov_b32 s28, 0
	s_waitcnt lgkmcnt(0)
	v_pk_add_f32 v[16:17], v[16:17], v[32:33]
	v_cndmask_b32_e32 v48, v254, v48, vcc
	v_lshlrev_b32_e32 v76, 2, v48
	ds_bpermute_b32 v33, v76, v17
	ds_bpermute_b32 v32, v76, v16
	v_lshlrev_b32_e32 v48, 2, v146
	v_ashrrev_i32_e32 v49, 31, v48
	v_lshl_add_u64 v[84:85], s[2:3], 0, v[48:49]
	v_mov_b64_e32 v[48:49], s[22:23]
	s_waitcnt lgkmcnt(0)
	v_pk_add_f32 v[16:17], v[16:17], v[32:33]
	v_lshl_or_b32 v32, v171, 2, s71
	v_pk_fma_f32 v[88:89], v[16:17], s[20:21], v[48:49] op_sel_hi:[1,0,0]
	v_ashrrev_i32_e32 v33, 31, v32
	v_mul_f32_e32 v16, 0x4b800000, v89
	v_cmp_gt_f32_e32 vcc, s68, v89
	s_nop 1
	v_cndmask_b32_e32 v16, v89, v16, vcc
	v_rsq_f32_e32 v89, v16
	v_lshl_add_u64 v[16:17], v[84:85], 0, s[18:19]
	v_mul_f32_e32 v84, 0x45800000, v89
	v_cndmask_b32_e32 v84, v89, v84, vcc
	v_mul_f32_e32 v82, v82, v84
	v_mul_f32_e32 v83, v83, v84
	s_waitcnt vmcnt(3)
	v_mul_f32_e32 v82, v71, v82
	s_waitcnt vmcnt(2)
	v_mul_f32_e32 v83, v70, v83
	v_cvt_pk_fp8_f32 v90, v82, v83
	v_mul_f32_e32 v79, v79, v84
	v_mul_f32_e32 v78, v78, v84
	s_waitcnt vmcnt(1)
	v_mul_f32_e32 v79, v69, v79
	s_waitcnt vmcnt(0)
	v_mul_f32_e32 v78, v68, v78
	v_cvt_pk_fp8_f32 v90, v79, v78 op_sel:[0,0,1]
	v_mul_f32_e32 v78, 0x4b800000, v88
	v_cmp_gt_f32_e32 vcc, s68, v88
	v_mov_b32_e32 v82, v2
	v_rcp_f32_e32 v2, v81
	v_cndmask_b32_e32 v79, v88, v78, vcc
	v_rcp_f32_e32 v78, v80
	v_mov_b32_e32 v83, v50
	v_mov_b32_e32 v50, v3
	v_mov_b32_e32 v88, v34
	v_pk_mul_f32 v[82:83], v[82:83], v[78:79] op_sel_hi:[1,0]
	v_mov_b32_e32 v89, v18
	v_pk_mul_f32 v[50:51], v[50:51], v[2:3] op_sel_hi:[1,0]
	v_mov_b32_e32 v18, v35
	v_rsq_f32_e32 v91, v79
	v_pk_mul_f32 v[84:85], v[82:83], v[82:83]
	v_pk_mul_f32 v[78:79], v[88:89], v[78:79] op_sel_hi:[1,0]
	v_pk_mul_f32 v[88:89], v[50:51], v[50:51]
	v_pk_mul_f32 v[2:3], v[18:19], v[2:3] op_sel_hi:[1,0]
	v_pk_mul_f32 v[80:81], v[78:79], v[78:79]
	v_pk_mul_f32 v[18:19], v[2:3], v[2:3]
	v_mov_b32_e32 v34, v88
	v_mov_b32_e32 v35, v84
	v_mov_b32_e32 v84, v89
	v_pk_add_f32 v[34:35], v[34:35], v[84:85]
	v_mov_b32_e32 v84, v19
	v_mov_b32_e32 v85, v81
	v_pk_add_f32 v[34:35], v[84:85], v[34:35]
	v_mov_b32_e32 v19, v80
	v_pk_add_f32 v[18:19], v[18:19], v[34:35]
	ds_bpermute_b32 v35, v72, v19
	ds_bpermute_b32 v34, v72, v18
	v_lshlrev_b64 v[80:81], 11, v[32:33]
	v_mul_f32_e32 v33, 0x45800000, v91
	v_lshl_add_u64 v[80:81], v[16:17], 0, v[80:81]
	v_cndmask_b32_e32 v33, v91, v33, vcc
	s_waitcnt lgkmcnt(0)
	v_pk_add_f32 v[18:19], v[18:19], v[34:35]
	ds_bpermute_b32 v35, v73, v19
	ds_bpermute_b32 v34, v73, v18
	global_store_dword v[80:81], v90, off nt
	v_mul_f32_e32 v80, v86, v33
	v_mul_f32_e32 v81, v87, v33
	v_mul_f32_e32 v80, v71, v80
	s_waitcnt lgkmcnt(0)
	v_pk_add_f32 v[18:19], v[18:19], v[34:35]
	ds_bpermute_b32 v35, v74, v19
	ds_bpermute_b32 v34, v74, v18
	v_mul_f32_e32 v81, v70, v81
	v_mov_b32_e32 v84, 0
	v_cvt_pk_fp8_f32 v84, v80, v81
	v_mul_f32_e32 v1, v1, v33
	s_waitcnt lgkmcnt(0)
	v_pk_add_f32 v[18:19], v[18:19], v[34:35]
	ds_bpermute_b32 v35, v75, v19
	ds_bpermute_b32 v34, v75, v18
	v_mul_f32_e32 v0, v0, v33
	v_mul_f32_e32 v1, v69, v1
	v_mul_f32_e32 v0, v68, v0
	v_cvt_pk_fp8_f32 v84, v1, v0 op_sel:[0,0,1]
	s_waitcnt lgkmcnt(0)
	v_pk_add_f32 v[0:1], v[18:19], v[34:35]
	ds_bpermute_b32 v19, v76, v1
	ds_bpermute_b32 v18, v76, v0
	v_or_b32_e32 v34, 1, v32
	v_ashrrev_i32_e32 v35, 31, v34
	v_lshlrev_b64 v[34:35], 11, v[34:35]
	v_lshl_add_u64 v[34:35], v[16:17], 0, v[34:35]
	s_waitcnt lgkmcnt(0)
	v_pk_add_f32 v[0:1], v[0:1], v[18:19]
	global_store_dword v[34:35], v84, off nt
	v_pk_fma_f32 v[0:1], v[0:1], s[20:21], v[48:49] op_sel_hi:[1,0,0]
	v_mov_b32_e32 v80, v36
	v_mul_f32_e32 v18, 0x4b800000, v1
	v_cmp_gt_f32_e32 vcc, s68, v1
	v_mov_b32_e32 v81, v20
	v_mov_b32_e32 v20, v37
	v_cndmask_b32_e32 v1, v1, v18, vcc
	v_rsq_f32_e32 v1, v1
	v_or_b32_e32 v18, 2, v32
	v_ashrrev_i32_e32 v19, 31, v18
	v_lshlrev_b64 v[18:19], 11, v[18:19]
	v_mul_f32_e32 v33, 0x45800000, v1
	v_cndmask_b32_e32 v1, v1, v33, vcc
	v_mul_f32_e32 v33, v82, v1
	v_mul_f32_e32 v34, v83, v1
	v_mul_f32_e32 v33, v71, v33
	v_mul_f32_e32 v34, v70, v34
	v_mov_b32_e32 v82, 0
	v_cvt_pk_fp8_f32 v82, v33, v34
	v_mul_f32_e32 v35, v79, v1
	v_mul_f32_e32 v1, v78, v1
	v_mul_f32_e32 v33, v69, v35
	v_mul_f32_e32 v1, v68, v1
	v_cvt_pk_fp8_f32 v82, v33, v1 op_sel:[0,0,1]
	v_mul_f32_e32 v1, 0x4b800000, v0
	v_cmp_gt_f32_e32 vcc, s68, v0
	v_mov_b32_e32 v34, v4
	v_rcp_f32_e32 v4, v65
	v_cndmask_b32_e32 v1, v0, v1, vcc
	v_rcp_f32_e32 v0, v64
	v_mov_b32_e32 v35, v52
	v_mov_b32_e32 v52, v5
	v_pk_mul_f32 v[52:53], v[52:53], v[4:5] op_sel_hi:[1,0]
	v_pk_mul_f32 v[34:35], v[34:35], v[0:1] op_sel_hi:[1,0]
	v_rsq_f32_e32 v33, v1
	v_pk_mul_f32 v[78:79], v[34:35], v[34:35]
	v_pk_mul_f32 v[0:1], v[80:81], v[0:1] op_sel_hi:[1,0]
	v_pk_mul_f32 v[80:81], v[52:53], v[52:53]
	v_pk_mul_f32 v[4:5], v[20:21], v[4:5] op_sel_hi:[1,0]
	v_pk_mul_f32 v[64:65], v[0:1], v[0:1]
	v_pk_mul_f32 v[20:21], v[4:5], v[4:5]
	v_mov_b32_e32 v36, v80
	v_mov_b32_e32 v37, v78
	v_mov_b32_e32 v78, v81
	v_pk_add_f32 v[36:37], v[36:37], v[78:79]
	v_mov_b32_e32 v78, v21
	v_mov_b32_e32 v79, v65
	v_pk_add_f32 v[36:37], v[78:79], v[36:37]
	v_mov_b32_e32 v21, v64
	v_pk_add_f32 v[20:21], v[20:21], v[36:37]
	ds_bpermute_b32 v37, v72, v21
	ds_bpermute_b32 v36, v72, v20
	v_lshl_add_u64 v[18:19], v[16:17], 0, v[18:19]
	global_store_dword v[18:19], v82, off nt
	v_mul_f32_e32 v64, 0x45800000, v33
	v_cndmask_b32_e32 v33, v33, v64, vcc
	s_waitcnt lgkmcnt(0)
	v_pk_add_f32 v[18:19], v[20:21], v[36:37]
	ds_bpermute_b32 v21, v73, v19
	ds_bpermute_b32 v20, v73, v18
	v_mul_f32_e32 v36, v50, v33
	v_mul_f32_e32 v37, v51, v33
	v_mul_f32_e32 v36, v71, v36
	v_mul_f32_e32 v37, v70, v37
	s_waitcnt lgkmcnt(0)
	v_pk_add_f32 v[18:19], v[18:19], v[20:21]
	ds_bpermute_b32 v21, v74, v19
	ds_bpermute_b32 v20, v74, v18
	v_mov_b32_e32 v50, 0
	v_cvt_pk_fp8_f32 v50, v36, v37
	v_mul_f32_e32 v3, v3, v33
	v_mul_f32_e32 v2, v2, v33
	s_waitcnt lgkmcnt(0)
	v_pk_add_f32 v[18:19], v[18:19], v[20:21]
	ds_bpermute_b32 v21, v75, v19
	ds_bpermute_b32 v20, v75, v18
	v_mul_f32_e32 v3, v69, v3
	v_mul_f32_e32 v2, v68, v2
	v_cvt_pk_fp8_f32 v50, v3, v2 op_sel:[0,0,1]
	v_mov_b32_e32 v33, 0
	s_waitcnt lgkmcnt(0)
	v_pk_add_f32 v[2:3], v[18:19], v[20:21]
	ds_bpermute_b32 v19, v76, v3
	ds_bpermute_b32 v18, v76, v2
	v_or_b32_e32 v20, 3, v32
	v_ashrrev_i32_e32 v21, 31, v20
	v_lshlrev_b64 v[20:21], 11, v[20:21]
	v_lshl_add_u64 v[20:21], v[16:17], 0, v[20:21]
	s_waitcnt lgkmcnt(0)
	v_pk_add_f32 v[2:3], v[2:3], v[18:19]
	global_store_dword v[20:21], v50, off nt
	v_pk_fma_f32 v[2:3], v[2:3], s[20:21], v[48:49] op_sel_hi:[1,0,0]
	v_or_b32_e32 v36, 8, v32
	v_mul_f32_e32 v18, 0x4b800000, v3
	v_cmp_gt_f32_e32 vcc, s68, v3
	v_ashrrev_i32_e32 v37, 31, v36
	s_nop 0
	v_cndmask_b32_e32 v3, v3, v18, vcc
	v_rsq_f32_e32 v3, v3
	s_nop 0
	v_mul_f32_e32 v18, 0x45800000, v3
	v_cndmask_b32_e32 v3, v3, v18, vcc
	v_mul_f32_e32 v18, v34, v3
	v_mul_f32_e32 v19, v35, v3
	v_mul_f32_e32 v18, v71, v18
	v_mul_f32_e32 v19, v70, v19
	v_cvt_pk_fp8_f32 v33, v18, v19
	v_mul_f32_e32 v1, v1, v3
	v_mul_f32_e32 v0, v0, v3
	v_mul_f32_e32 v1, v69, v1
	v_mul_f32_e32 v0, v68, v0
	v_cvt_pk_fp8_f32 v33, v1, v0 op_sel:[0,0,1]
	v_mul_f32_e32 v0, 0x4b800000, v2
	v_cmp_gt_f32_e32 vcc, s68, v2
	v_mov_b32_e32 v3, v54
	v_mov_b32_e32 v54, v7
	v_cndmask_b32_e32 v1, v2, v0, vcc
	v_rcp_f32_e32 v0, v66
	v_mov_b32_e32 v2, v6
	v_rcp_f32_e32 v6, v67
	v_mov_b32_e32 v18, v38
	v_pk_mul_f32 v[2:3], v[2:3], v[0:1] op_sel_hi:[1,0]
	v_mov_b32_e32 v19, v22
	v_pk_mul_f32 v[20:21], v[54:55], v[6:7] op_sel_hi:[1,0]
	v_mov_b32_e32 v22, v39
	v_rsq_f32_e32 v64, v1
	v_pk_mul_f32 v[34:35], v[2:3], v[2:3]
	v_pk_mul_f32 v[0:1], v[18:19], v[0:1] op_sel_hi:[1,0]
	v_pk_mul_f32 v[54:55], v[20:21], v[20:21]
	v_pk_mul_f32 v[18:19], v[22:23], v[6:7] op_sel_hi:[1,0]
	v_pk_mul_f32 v[50:51], v[0:1], v[0:1]
	v_pk_mul_f32 v[6:7], v[18:19], v[18:19]
	v_mov_b32_e32 v22, v54
	v_mov_b32_e32 v23, v34
	v_mov_b32_e32 v34, v55
	v_pk_add_f32 v[22:23], v[22:23], v[34:35]
	v_mov_b32_e32 v34, v7
	v_mov_b32_e32 v35, v51
	v_pk_add_f32 v[22:23], v[34:35], v[22:23]
	v_mov_b32_e32 v7, v50
	v_pk_add_f32 v[6:7], v[6:7], v[22:23]
	ds_bpermute_b32 v23, v72, v7
	ds_bpermute_b32 v22, v72, v6
	v_lshlrev_b64 v[34:35], 11, v[36:37]
	v_lshl_add_u64 v[34:35], v[16:17], 0, v[34:35]
	global_store_dword v[34:35], v33, off nt
	v_mul_f32_e32 v33, 0x45800000, v64
	s_waitcnt lgkmcnt(0)
	v_pk_add_f32 v[6:7], v[6:7], v[22:23]
	ds_bpermute_b32 v23, v73, v7
	ds_bpermute_b32 v22, v73, v6
	v_cndmask_b32_e32 v33, v64, v33, vcc
	v_mul_f32_e32 v34, v52, v33
	v_mul_f32_e32 v35, v53, v33
	v_mul_f32_e32 v34, v71, v34
	s_waitcnt lgkmcnt(0)
	v_pk_add_f32 v[6:7], v[6:7], v[22:23]
	ds_bpermute_b32 v23, v74, v7
	ds_bpermute_b32 v22, v74, v6
	v_mul_f32_e32 v35, v70, v35
	v_mov_b32_e32 v36, 0
	v_cvt_pk_fp8_f32 v36, v34, v35
	v_mul_f32_e32 v5, v5, v33
	s_waitcnt lgkmcnt(0)
	v_pk_add_f32 v[6:7], v[6:7], v[22:23]
	ds_bpermute_b32 v23, v75, v7
	ds_bpermute_b32 v22, v75, v6
	v_mul_f32_e32 v4, v4, v33
	v_mul_f32_e32 v5, v69, v5
	v_mul_f32_e32 v4, v68, v4
	v_cvt_pk_fp8_f32 v36, v5, v4 op_sel:[0,0,1]
	s_waitcnt lgkmcnt(0)
	v_pk_add_f32 v[4:5], v[6:7], v[22:23]
	ds_bpermute_b32 v7, v76, v5
	ds_bpermute_b32 v6, v76, v4
	v_mov_b32_e32 v33, 0
	v_or_b32_e32 v22, 9, v32
	v_ashrrev_i32_e32 v23, 31, v22
	v_lshlrev_b64 v[22:23], 11, v[22:23]
	s_waitcnt lgkmcnt(0)
	v_pk_add_f32 v[4:5], v[4:5], v[6:7]
	v_lshl_add_u64 v[22:23], v[16:17], 0, v[22:23]
	v_pk_fma_f32 v[34:35], v[4:5], s[20:21], v[48:49] op_sel_hi:[1,0,0]
	v_mov_b32_e32 v38, v40
	v_mul_f32_e32 v4, 0x4b800000, v35
	v_cmp_gt_f32_e32 vcc, s68, v35
	v_mov_b32_e32 v39, v24
	v_mov_b32_e32 v24, v41
	v_cndmask_b32_e32 v4, v35, v4, vcc
	v_rsq_f32_e32 v4, v4
	v_mov_b32_e32 v35, v56
	v_mov_b32_e32 v56, v9
	global_store_dword v[22:23], v36, off nt
	v_mul_f32_e32 v5, 0x45800000, v4
	v_cndmask_b32_e32 v4, v4, v5, vcc
	v_mul_f32_e32 v2, v2, v4
	v_mul_f32_e32 v3, v3, v4
	v_mul_f32_e32 v2, v71, v2
	v_mul_f32_e32 v3, v70, v3
	v_cvt_pk_fp8_f32 v33, v2, v3
	v_mul_f32_e32 v1, v1, v4
	v_mul_f32_e32 v0, v0, v4
	ds_read_b128 v[4:7], v77 offset:64
	v_mul_f32_e32 v1, v69, v1
	v_mul_f32_e32 v0, v68, v0
	v_cvt_pk_fp8_f32 v33, v1, v0 op_sel:[0,0,1]
	v_mul_f32_e32 v0, 0x4b800000, v34
	v_cmp_gt_f32_e32 vcc, s68, v34
	v_or_b32_e32 v22, 10, v32
	v_ashrrev_i32_e32 v23, 31, v22
	v_cndmask_b32_e32 v34, v34, v0, vcc
	ds_read_b128 v[0:3], v77 offset:96
	s_waitcnt lgkmcnt(1)
	v_rcp_f32_e32 v4, v4
	v_rsq_f32_e32 v54, v34
	v_mov_b32_e32 v34, v8
	v_rcp_f32_e32 v8, v5
	v_pk_mul_f32 v[34:35], v[34:35], v[4:5] op_sel_hi:[1,0]
	v_pk_mul_f32 v[4:5], v[38:39], v[4:5] op_sel_hi:[1,0]
	v_pk_mul_f32 v[36:37], v[34:35], v[34:35]
	v_pk_mul_f32 v[50:51], v[56:57], v[8:9] op_sel_hi:[1,0]
	v_pk_mul_f32 v[8:9], v[24:25], v[8:9] op_sel_hi:[1,0]
	v_pk_mul_f32 v[52:53], v[50:51], v[50:51]
	v_pk_mul_f32 v[38:39], v[4:5], v[4:5]
	v_pk_mul_f32 v[24:25], v[8:9], v[8:9]
	v_mov_b32_e32 v40, v52
	v_mov_b32_e32 v41, v36
	v_mov_b32_e32 v36, v53
	v_pk_add_f32 v[36:37], v[40:41], v[36:37]
	v_mov_b32_e32 v40, v25
	v_mov_b32_e32 v41, v39
	v_pk_add_f32 v[36:37], v[40:41], v[36:37]
	v_mov_b32_e32 v25, v38
	v_pk_add_f32 v[24:25], v[24:25], v[36:37]
	ds_bpermute_b32 v37, v72, v25
	ds_bpermute_b32 v36, v72, v24
	v_lshlrev_b64 v[22:23], 11, v[22:23]
	v_lshl_add_u64 v[22:23], v[16:17], 0, v[22:23]
	global_store_dword v[22:23], v33, off nt
	v_mul_f32_e32 v33, 0x45800000, v54
	s_waitcnt lgkmcnt(0)
	v_pk_add_f32 v[22:23], v[24:25], v[36:37]
	ds_bpermute_b32 v25, v73, v23
	ds_bpermute_b32 v24, v73, v22
	v_cndmask_b32_e32 v33, v54, v33, vcc
	v_mul_f32_e32 v20, v20, v33
	v_mul_f32_e32 v36, v71, v20
	v_mul_f32_e32 v37, v21, v33
	s_waitcnt lgkmcnt(0)
	v_pk_add_f32 v[20:21], v[22:23], v[24:25]
	ds_bpermute_b32 v23, v74, v21
	ds_bpermute_b32 v22, v74, v20
	v_mul_f32_e32 v24, v70, v37
	v_mov_b32_e32 v25, 0
	v_cvt_pk_fp8_f32 v25, v36, v24
	v_mul_f32_e32 v19, v19, v33
	s_waitcnt lgkmcnt(0)
	v_pk_add_f32 v[20:21], v[20:21], v[22:23]
	ds_bpermute_b32 v23, v75, v21
	ds_bpermute_b32 v22, v75, v20
	v_mul_f32_e32 v18, v18, v33
	v_mul_f32_e32 v19, v69, v19
	v_mul_f32_e32 v18, v68, v18
	v_cvt_pk_fp8_f32 v25, v19, v18 op_sel:[0,0,1]
	s_waitcnt lgkmcnt(0)
	v_pk_add_f32 v[18:19], v[20:21], v[22:23]
	ds_bpermute_b32 v21, v76, v19
	ds_bpermute_b32 v20, v76, v18
	v_or_b32_e32 v22, 11, v32
	v_ashrrev_i32_e32 v23, 31, v22
	v_lshlrev_b64 v[22:23], 11, v[22:23]
	v_lshl_add_u64 v[22:23], v[16:17], 0, v[22:23]
	s_waitcnt lgkmcnt(0)
	v_pk_add_f32 v[18:19], v[18:19], v[20:21]
	global_store_dword v[22:23], v25, off nt
	v_pk_fma_f32 v[18:19], v[18:19], s[20:21], v[48:49] op_sel_hi:[1,0,0]
	v_mov_b32_e32 v33, 0
	v_mul_f32_e32 v20, 0x4b800000, v19
	v_cmp_gt_f32_e32 vcc, s68, v19
	v_mov_b32_e32 v24, v42
	v_mov_b32_e32 v25, v26
	v_cndmask_b32_e32 v19, v19, v20, vcc
	v_rsq_f32_e32 v19, v19
	v_mov_b32_e32 v26, v43
	v_or_b32_e32 v20, 16, v32
	v_ashrrev_i32_e32 v21, 31, v20
	v_mul_f32_e32 v22, 0x45800000, v19
	v_cndmask_b32_e32 v19, v19, v22, vcc
	v_mul_f32_e32 v22, v34, v19
	v_mul_f32_e32 v23, v35, v19
	v_mul_f32_e32 v22, v71, v22
	v_mul_f32_e32 v23, v70, v23
	v_cvt_pk_fp8_f32 v33, v22, v23
	v_mul_f32_e32 v5, v5, v19
	v_mul_f32_e32 v4, v4, v19
	v_mul_f32_e32 v5, v69, v5
	v_mul_f32_e32 v4, v68, v4
	v_cvt_pk_fp8_f32 v33, v5, v4 op_sel:[0,0,1]
	v_mul_f32_e32 v4, 0x4b800000, v18
	v_cmp_gt_f32_e32 vcc, s68, v18
	v_mov_b32_e32 v19, v58
	v_mov_b32_e32 v58, v11
	v_cndmask_b32_e32 v5, v18, v4, vcc
	v_rcp_f32_e32 v4, v6
	v_rcp_f32_e32 v6, v7
	v_mov_b32_e32 v18, v10
	v_rsq_f32_e32 v38, v5
	v_pk_mul_f32 v[18:19], v[18:19], v[4:5] op_sel_hi:[1,0]
	v_pk_mul_f32 v[10:11], v[58:59], v[6:7] op_sel_hi:[1,0]
	v_pk_mul_f32 v[22:23], v[18:19], v[18:19]
	v_pk_mul_f32 v[4:5], v[24:25], v[4:5] op_sel_hi:[1,0]
	v_pk_mul_f32 v[34:35], v[10:11], v[10:11]
	v_pk_mul_f32 v[6:7], v[26:27], v[6:7] op_sel_hi:[1,0]
	v_pk_mul_f32 v[24:25], v[4:5], v[4:5]
	v_pk_mul_f32 v[26:27], v[6:7], v[6:7]
	v_mov_b32_e32 v36, v34
	v_mov_b32_e32 v37, v22
	v_mov_b32_e32 v22, v35
	v_pk_add_f32 v[22:23], v[36:37], v[22:23]
	v_mov_b32_e32 v34, v27
	v_mov_b32_e32 v35, v25
	v_pk_add_f32 v[22:23], v[34:35], v[22:23]
	v_mov_b32_e32 v27, v24
	v_pk_add_f32 v[22:23], v[26:27], v[22:23]
	ds_bpermute_b32 v25, v72, v23
	ds_bpermute_b32 v24, v72, v22
	v_lshlrev_b64 v[20:21], 11, v[20:21]
	v_lshl_add_u64 v[20:21], v[16:17], 0, v[20:21]
	global_store_dword v[20:21], v33, off nt
	v_mul_f32_e32 v26, 0x45800000, v38
	s_waitcnt lgkmcnt(0)
	v_pk_add_f32 v[20:21], v[22:23], v[24:25]
	ds_bpermute_b32 v23, v73, v21
	ds_bpermute_b32 v22, v73, v20
	v_cndmask_b32_e32 v24, v38, v26, vcc
	v_mul_f32_e32 v25, v50, v24
	v_mul_f32_e32 v26, v51, v24
	v_mul_f32_e32 v25, v71, v25
	s_waitcnt lgkmcnt(0)
	v_pk_add_f32 v[20:21], v[20:21], v[22:23]
	ds_bpermute_b32 v23, v74, v21
	ds_bpermute_b32 v22, v74, v20
	v_mul_f32_e32 v26, v70, v26
	v_mov_b32_e32 v27, 0
	v_cvt_pk_fp8_f32 v27, v25, v26
	v_mul_f32_e32 v9, v9, v24
	s_waitcnt lgkmcnt(0)
	v_pk_add_f32 v[20:21], v[20:21], v[22:23]
	ds_bpermute_b32 v23, v75, v21
	ds_bpermute_b32 v22, v75, v20
	v_mul_f32_e32 v8, v8, v24
	v_mul_f32_e32 v9, v69, v9
	v_mul_f32_e32 v8, v68, v8
	v_cvt_pk_fp8_f32 v27, v9, v8 op_sel:[0,0,1]
	s_waitcnt lgkmcnt(0)
	v_pk_add_f32 v[8:9], v[20:21], v[22:23]
	ds_bpermute_b32 v21, v76, v9
	ds_bpermute_b32 v20, v76, v8
	v_or_b32_e32 v22, 17, v32
	v_ashrrev_i32_e32 v23, 31, v22
	v_lshlrev_b64 v[22:23], 11, v[22:23]
	v_lshl_add_u64 v[22:23], v[16:17], 0, v[22:23]
	s_waitcnt lgkmcnt(0)
	v_pk_add_f32 v[8:9], v[8:9], v[20:21]
	global_store_dword v[22:23], v27, off nt
	v_pk_fma_f32 v[8:9], v[8:9], s[20:21], v[48:49] op_sel_hi:[1,0,0]
	v_mov_b32_e32 v33, 0
	v_mul_f32_e32 v20, 0x4b800000, v9
	v_cmp_gt_f32_e32 vcc, s68, v9
	v_rcp_f32_e32 v0, v0
	s_nop 0
	v_cndmask_b32_e32 v9, v9, v20, vcc
	v_rsq_f32_e32 v9, v9
	v_or_b32_e32 v20, 18, v32
	v_ashrrev_i32_e32 v21, 31, v20
	v_lshlrev_b64 v[20:21], 11, v[20:21]
	v_mul_f32_e32 v22, 0x45800000, v9
	v_cndmask_b32_e32 v9, v9, v22, vcc
	v_mul_f32_e32 v18, v18, v9
	v_mul_f32_e32 v19, v19, v9
	v_mul_f32_e32 v18, v71, v18
	v_mul_f32_e32 v19, v70, v19
	v_cvt_pk_fp8_f32 v33, v18, v19
	v_mul_f32_e32 v5, v5, v9
	v_mul_f32_e32 v4, v4, v9
	v_mul_f32_e32 v5, v69, v5
	v_mul_f32_e32 v4, v68, v4
	v_cvt_pk_fp8_f32 v33, v5, v4 op_sel:[0,0,1]
	v_mul_f32_e32 v4, 0x4b800000, v8
	v_cmp_gt_f32_e32 vcc, s68, v8
	v_mov_b32_e32 v5, v60
	v_mov_b32_e32 v60, v13
	v_cndmask_b32_e32 v4, v8, v4, vcc
	v_rsq_f32_e32 v34, v4
	v_mov_b32_e32 v4, v12
	v_rcp_f32_e32 v12, v1
	v_pk_mul_f32 v[4:5], v[4:5], v[0:1] op_sel_hi:[1,0]
	v_mov_b32_e32 v18, v44
	v_mov_b32_e32 v19, v28
	v_pk_mul_f32 v[22:23], v[60:61], v[12:13] op_sel_hi:[1,0]
	v_mov_b32_e32 v28, v45
	v_pk_mul_f32 v[8:9], v[4:5], v[4:5]
	v_pk_mul_f32 v[0:1], v[18:19], v[0:1] op_sel_hi:[1,0]
	v_pk_mul_f32 v[24:25], v[22:23], v[22:23]
	v_pk_mul_f32 v[12:13], v[28:29], v[12:13] op_sel_hi:[1,0]
	v_pk_mul_f32 v[18:19], v[0:1], v[0:1]
	v_pk_mul_f32 v[26:27], v[12:13], v[12:13]
	v_mov_b32_e32 v28, v24
	v_mov_b32_e32 v29, v8
	v_mov_b32_e32 v8, v25
	v_pk_add_f32 v[8:9], v[28:29], v[8:9]
	v_mov_b32_e32 v24, v27
	v_mov_b32_e32 v25, v19
	v_pk_add_f32 v[8:9], v[24:25], v[8:9]
	v_mov_b32_e32 v27, v18
	v_pk_add_f32 v[8:9], v[26:27], v[8:9]
	ds_bpermute_b32 v19, v72, v9
	ds_bpermute_b32 v18, v72, v8
	v_lshl_add_u64 v[20:21], v[16:17], 0, v[20:21]
	global_store_dword v[20:21], v33, off nt
	v_mul_f32_e32 v20, 0x45800000, v34
	v_cndmask_b32_e32 v20, v34, v20, vcc
	s_waitcnt lgkmcnt(0)
	v_pk_add_f32 v[8:9], v[8:9], v[18:19]
	ds_bpermute_b32 v19, v73, v9
	ds_bpermute_b32 v18, v73, v8
	v_mul_f32_e32 v10, v10, v20
	v_mul_f32_e32 v21, v71, v10
	v_mul_f32_e32 v24, v11, v20
	v_mul_f32_e32 v7, v7, v20
	s_waitcnt lgkmcnt(0)
	v_pk_add_f32 v[8:9], v[8:9], v[18:19]
	ds_bpermute_b32 v11, v74, v9
	ds_bpermute_b32 v10, v74, v8
	v_mul_f32_e32 v18, v70, v24
	v_mov_b32_e32 v19, 0
	v_cvt_pk_fp8_f32 v19, v21, v18
	v_mul_f32_e32 v6, v6, v20
	s_waitcnt lgkmcnt(0)
	v_pk_add_f32 v[8:9], v[8:9], v[10:11]
	ds_bpermute_b32 v11, v75, v9
	ds_bpermute_b32 v10, v75, v8
	v_mul_f32_e32 v7, v69, v7
	v_mul_f32_e32 v6, v68, v6
	v_cvt_pk_fp8_f32 v19, v7, v6 op_sel:[0,0,1]
	v_mov_b32_e32 v26, 0
	s_waitcnt lgkmcnt(0)
	v_pk_add_f32 v[6:7], v[8:9], v[10:11]
	ds_bpermute_b32 v9, v76, v7
	ds_bpermute_b32 v8, v76, v6
	v_or_b32_e32 v10, 19, v32
	v_ashrrev_i32_e32 v11, 31, v10
	v_lshlrev_b64 v[10:11], 11, v[10:11]
	v_lshl_add_u64 v[10:11], v[16:17], 0, v[10:11]
	s_waitcnt lgkmcnt(0)
	v_pk_add_f32 v[6:7], v[6:7], v[8:9]
	global_store_dword v[10:11], v19, off nt
	v_pk_fma_f32 v[6:7], v[6:7], s[20:21], v[48:49] op_sel_hi:[1,0,0]
	v_mov_b32_e32 v11, v30
	v_mul_f32_e32 v8, 0x4b800000, v7
	v_cmp_gt_f32_e32 vcc, s68, v7
	v_mov_b32_e32 v30, v47
	s_nop 0
	v_cndmask_b32_e32 v7, v7, v8, vcc
	v_rsq_f32_e32 v7, v7
	v_or_b32_e32 v8, 24, v32
	v_ashrrev_i32_e32 v9, 31, v8
	v_lshlrev_b64 v[8:9], 11, v[8:9]
	v_mul_f32_e32 v10, 0x45800000, v7
	v_cndmask_b32_e32 v7, v7, v10, vcc
	v_mul_f32_e32 v4, v4, v7
	v_mul_f32_e32 v5, v5, v7
	v_mul_f32_e32 v4, v71, v4
	v_mul_f32_e32 v5, v70, v5
	v_cvt_pk_fp8_f32 v26, v4, v5
	v_mul_f32_e32 v1, v1, v7
	v_mul_f32_e32 v0, v0, v7
	v_mul_f32_e32 v1, v69, v1
	v_mul_f32_e32 v0, v68, v0
	v_cvt_pk_fp8_f32 v26, v1, v0 op_sel:[0,0,1]
	v_mul_f32_e32 v0, 0x4b800000, v6
	v_cmp_gt_f32_e32 vcc, s68, v6
	v_mov_b32_e32 v4, v14
	v_mov_b32_e32 v5, v62
	v_cndmask_b32_e32 v1, v6, v0, vcc
	v_rcp_f32_e32 v0, v2
	v_rcp_f32_e32 v2, v3
	v_mov_b32_e32 v62, v15
	v_mov_b32_e32 v10, v46
	v_pk_mul_f32 v[4:5], v[4:5], v[0:1] op_sel_hi:[1,0]
	v_pk_mul_f32 v[14:15], v[62:63], v[2:3] op_sel_hi:[1,0]
	v_rsq_f32_e32 v27, v1
	v_pk_mul_f32 v[6:7], v[4:5], v[4:5]
	v_pk_mul_f32 v[0:1], v[10:11], v[0:1] op_sel_hi:[1,0]
	v_pk_mul_f32 v[18:19], v[14:15], v[14:15]
	v_pk_mul_f32 v[2:3], v[30:31], v[2:3] op_sel_hi:[1,0]
	v_pk_mul_f32 v[10:11], v[0:1], v[0:1]
	v_pk_mul_f32 v[20:21], v[2:3], v[2:3]
	v_mov_b32_e32 v24, v18
	v_mov_b32_e32 v25, v6
	v_mov_b32_e32 v6, v19
	v_pk_add_f32 v[6:7], v[24:25], v[6:7]
	v_mov_b32_e32 v18, v21
	v_mov_b32_e32 v19, v11
	v_pk_add_f32 v[6:7], v[18:19], v[6:7]
	v_mov_b32_e32 v21, v10
	v_pk_add_f32 v[6:7], v[20:21], v[6:7]
	ds_bpermute_b32 v11, v72, v7
	ds_bpermute_b32 v10, v72, v6
	v_lshl_add_u64 v[8:9], v[16:17], 0, v[8:9]
	global_store_dword v[8:9], v26, off nt
	v_mul_f32_e32 v18, 0x45800000, v27
	v_mov_b32_e32 v19, 0
	s_waitcnt lgkmcnt(0)
	v_pk_add_f32 v[6:7], v[6:7], v[10:11]
	ds_bpermute_b32 v9, v73, v7
	ds_bpermute_b32 v8, v73, v6
	v_cndmask_b32_e32 v10, v27, v18, vcc
	v_mul_f32_e32 v11, v22, v10
	v_mul_f32_e32 v18, v23, v10
	v_mul_f32_e32 v11, v71, v11
	s_waitcnt lgkmcnt(0)
	v_pk_add_f32 v[6:7], v[6:7], v[8:9]
	ds_bpermute_b32 v9, v74, v7
	ds_bpermute_b32 v8, v74, v6
	v_mul_f32_e32 v18, v70, v18
	v_cvt_pk_fp8_f32 v19, v11, v18
	v_mul_f32_e32 v13, v13, v10
	v_mul_f32_e32 v10, v12, v10
	s_waitcnt lgkmcnt(0)
	v_pk_add_f32 v[6:7], v[6:7], v[8:9]
	ds_bpermute_b32 v9, v75, v7
	ds_bpermute_b32 v8, v75, v6
	v_mul_f32_e32 v11, v69, v13
	v_mul_f32_e32 v10, v68, v10
	v_cvt_pk_fp8_f32 v19, v11, v10 op_sel:[0,0,1]
	v_or_b32_e32 v10, 25, v32
	s_waitcnt lgkmcnt(0)
	v_pk_add_f32 v[6:7], v[6:7], v[8:9]
	ds_bpermute_b32 v9, v76, v7
	ds_bpermute_b32 v8, v76, v6
	v_ashrrev_i32_e32 v11, 31, v10
	v_lshlrev_b64 v[10:11], 11, v[10:11]
	v_lshl_add_u64 v[10:11], v[16:17], 0, v[10:11]
	global_store_dword v[10:11], v19, off nt
	s_waitcnt lgkmcnt(0)
	v_pk_add_f32 v[6:7], v[6:7], v[8:9]
	s_nop 0
	v_pk_fma_f32 v[6:7], v[6:7], s[20:21], v[48:49] op_sel_hi:[1,0,0]
	s_nop 0
	v_mul_f32_e32 v8, 0x4b800000, v7
	v_cmp_gt_f32_e32 vcc, s68, v7
	s_nop 1
	v_cndmask_b32_e32 v7, v7, v8, vcc
	v_rsq_f32_e32 v7, v7
	v_or_b32_e32 v8, 26, v32
	v_ashrrev_i32_e32 v9, 31, v8
	v_mul_f32_e32 v10, 0x45800000, v7
	v_cndmask_b32_e32 v7, v7, v10, vcc
	v_mul_f32_e32 v4, v4, v7
	v_mul_f32_e32 v5, v5, v7
	v_mul_f32_e32 v4, v71, v4
	v_mul_f32_e32 v5, v70, v5
	v_mov_b32_e32 v10, 0
	v_cvt_pk_fp8_f32 v10, v4, v5
	v_mul_f32_e32 v1, v1, v7
	v_mul_f32_e32 v0, v0, v7
	v_mul_f32_e32 v1, v69, v1
	v_mul_f32_e32 v0, v68, v0
	v_cvt_pk_fp8_f32 v10, v1, v0 op_sel:[0,0,1]
	v_mul_f32_e32 v0, 0x4b800000, v6
	v_cmp_gt_f32_e32 vcc, s68, v6
	v_mov_b32_e32 v5, 0
	s_nop 0
	v_cndmask_b32_e32 v0, v6, v0, vcc
	v_rsq_f32_e32 v4, v0
	v_lshlrev_b64 v[0:1], 11, v[8:9]
	v_lshl_add_u64 v[0:1], v[16:17], 0, v[0:1]
	global_store_dword v[0:1], v10, off nt
	v_mul_f32_e32 v0, 0x45800000, v4
	v_cndmask_b32_e32 v0, v4, v0, vcc
	v_mul_f32_e32 v1, v14, v0
	v_mul_f32_e32 v4, v15, v0
	v_mul_f32_e32 v1, v71, v1
	v_mul_f32_e32 v4, v70, v4
	v_cvt_pk_fp8_f32 v5, v1, v4
	v_mul_f32_e32 v3, v3, v0
	v_mul_f32_e32 v0, v2, v0
	v_mul_f32_e32 v1, v69, v3
	v_mul_f32_e32 v0, v68, v0
	v_cvt_pk_fp8_f32 v5, v1, v0 op_sel:[0,0,1]
	v_or_b32_e32 v0, 27, v32
	v_ashrrev_i32_e32 v1, 31, v0
	v_lshlrev_b64 v[0:1], 11, v[0:1]
	v_lshl_add_u64 v[0:1], v[16:17], 0, v[0:1]
	global_store_dword v[0:1], v5, off nt
	s_barrier
